# LDS-DMA re-phasing (A halves in SP1, B halves in SP2, 4 pieces per load interval, waits 8/6/8/6) extended from P9 to P1, P3, P4, P6
# speedup vs baseline: 1.0185x; 1.0104x over previous
; #define PG8_STAGE(bufoff, gbase, voff) do { PG8_GLDS((const char*)(gbase), (voff)[0], ldsb + (bufoff)); PG8_GLDS((const char*)(gbase), (voff)[1], ldsb + (bufoff) + 8192u); } while (0)
; #define PG8_STAGEA(bufoff, gbase, o0, o1) do { PG8_GLDS((const char*)(gbase), (o0), ldsb + (bufoff)); PG8_GLDS((const char*)(gbase), (o1), ldsb + (bufoff) + 8192u); } while (0)
; #define PG8_STAGEA1(bufoff, gbase) do { if constexpr (Sched::GATHER) { PG8_STAGEA(bufoff, gbase, vA2, vA3); } else { PG8_STAGEA(bufoff, (gbase) + hstep, vA0, vA1); } } while (0)
; #define PG8_LDA(dst, b, h) do { if constexpr (F8) { _Pragma("unroll") for (int m = 0; m < 4; ++m) dst##8[m] = PG8_LD32(lds + PG8_SA(b, h) + aoff + m * 2048); } else { \
;         _Pragma("unroll") for (int m = 0; m < 4; ++m) _Pragma("unroll") for (int k = 0; k < 2; ++k) dst[m][k] = *(const LAS bf16x8*)(lds + PG8_SA(b, h) + aoff + m * 2048 + k * 1024); } } while (0)
; #define PG8_LDB(dst, b, h) do { if constexpr (F8) { _Pragma("unroll") for (int n = 0; n < 2; ++n) dst##8[n] = PG8_LD32(lds + PG8_SB(b, h) + boff + n * 2048); } else { \
;         _Pragma("unroll") for (int n = 0; n < 2; ++n) _Pragma("unroll") for (int k = 0; k < 2; ++k) dst[n][k] = *(const LAS bf16x8*)(lds + PG8_SB(b, h) + boff + n * 2048 + k * 1024); } } while (0)
; #define PG8_WAIT_VR() PG8_WAIT_V(8)
; #define PG8_WAIT_VX() do { if (relax) asm volatile("s_waitcnt vmcnt(%0)" :: "n"(8 + Epi::RELAX) : "memory"); else PG8_WAIT_V(8); } while (0)
; #define PG8_WAIT_L(n) asm volatile("s_waitcnt lgkmcnt(" #n ")" ::: "memory")
; #define PG8_BAR __builtin_amdgcn_s_barrier()
; template <class Epi, class Sched, bool F8 = false, bool PF = false, bool I8 = false, int PID = -1>
; __device__ __forceinline__ void gemm_phase(LAS unsigned char* lds, LAS unsigned char* xlds, const int RP, const int RPB, const int nt, const Sched& S, const Epi& E, const int stagger_ticks) {
;     ...
;             PG8_LDA(At, 0, 1); PG8_STAGE(PG8_SB(0, 0), b2, voffB); PG8_STAGE(PG8_SB(0, 1), b2 + hstepB, voffB); PG8_STAGEA(PG8_SA(0, 0), a2, vA0, vA1);
;             PG8_WAIT_VX(); PG8_WAIT_L(0); PG8_BAR; PG8_MMA(1, 0, At, B0); PG8_MMA(1, 1, At, B1); PG8_BAR; PG8_SCHED;
;             PG8_LDB(B0, 1, 0); PG8_LDB(B1, 1, 1); PG8_SCHED; PG8_LDA(At, 1, 0); PG8_STAGEA1(PG8_SA(0, 1), a2);
;             PG8_WAIT_VR(); PG8_WAIT_L(0); PG8_BAR; PG8_MMA(0, 0, At, B0); PG8_MMA(0, 1, At, B1); PG8_BAR; PG8_SCHED;
.LBB0_213:
	s_add_u32 s48, s2, 0xfffe0080
	s_addc_u32 s49, s3, -1
	s_cmp_eq_u32 s79, 4
	s_cselect_b32 s62, s10, s48
	s_cselect_b32 s63, s11, s49
	s_cselect_b32 s50, s12, s76
	s_cselect_b32 s51, s13, s77
	s_add_u32 s48, s62, 0x80
	s_addc_u32 s49, s63, 0
	s_add_u32 s60, s50, 0x80
	s_addc_u32 s61, s51, 0
	ds_read_b128 v[122:125], v185 offset:16384
	ds_read_b128 v[126:129], v185 offset:17408
	ds_read_b128 v[138:141], v185 offset:18432
	ds_read_b128 v[142:145], v185 offset:19456
	ds_read_b128 v[186:189], v185 offset:20480
	ds_read_b128 v[190:193], v185 offset:21504
	ds_read_b128 v[194:197], v185 offset:22528
	ds_read_b128 v[198:201], v185 offset:23552
	s_add_i32 s83, s82, 0x10000
	s_mov_b32 m0, s83
	s_nop 0
	global_load_lds_dwordx4 v182, s[50:51]
	s_add_i32 s83, s82, 0x12000
	s_mov_b32 m0, s83
	s_nop 0
	global_load_lds_dwordx4 v183, s[50:51]
	s_add_u32 s86, s50, 0x2000
	s_addc_u32 s87, s51, 0
	s_add_i32 s83, s82, 0x14000
	s_mov_b32 m0, s83
	s_nop 0
	global_load_lds_dwordx4 v182, s[86:87]
	s_add_i32 s83, s82, 0x16000
	s_mov_b32 m0, s83
	s_nop 0
	global_load_lds_dwordx4 v183, s[86:87]
	s_waitcnt vmcnt(6)
	s_waitcnt lgkmcnt(0)
	s_barrier
	s_setprio 1
	s_waitcnt lgkmcnt(7)
	v_mfma_i32_16x16x64_i8 v[78:81], v[162:165], v[122:125], v[78:81]
	v_mfma_i32_16x16x64_i8 v[74:77], v[170:173], v[122:125], v[74:77]
	s_waitcnt lgkmcnt(5)
	v_mfma_i32_16x16x64_i8 v[50:53], v[162:165], v[138:141], v[50:53]
	v_mfma_i32_16x16x64_i8 v[42:45], v[170:173], v[138:141], v[42:45]
	s_waitcnt lgkmcnt(3)
	v_mfma_i32_16x16x64_i8 v[30:33], v[162:165], v[186:189], v[30:33]
	v_mfma_i32_16x16x64_i8 v[26:29], v[170:173], v[186:189], v[26:29]
	s_waitcnt lgkmcnt(1)
	v_mfma_i32_16x16x64_i8 v[14:17], v[162:165], v[194:197], v[14:17]
	v_mfma_i32_16x16x64_i8 v[10:13], v[170:173], v[194:197], v[10:13]
	v_mfma_i32_16x16x64_i8 v[78:81], v[166:169], v[126:129], v[78:81]
	v_mfma_i32_16x16x64_i8 v[74:77], v[174:177], v[126:129], v[74:77]
	v_mfma_i32_16x16x64_i8 v[50:53], v[166:169], v[142:145], v[50:53]
	v_mfma_i32_16x16x64_i8 v[42:45], v[174:177], v[142:145], v[42:45]
	v_mfma_i32_16x16x64_i8 v[30:33], v[166:169], v[190:193], v[30:33]
	v_mfma_i32_16x16x64_i8 v[26:29], v[174:177], v[190:193], v[26:29]
	s_waitcnt lgkmcnt(0)
	v_mfma_i32_16x16x64_i8 v[14:17], v[166:169], v[198:201], v[14:17]
	v_mfma_i32_16x16x64_i8 v[10:13], v[174:177], v[198:201], v[10:13]
	v_mfma_i32_16x16x64_i8 v[70:73], v[146:149], v[122:125], v[70:73]
	v_mfma_i32_16x16x64_i8 v[62:65], v[154:157], v[122:125], v[62:65]
	v_mfma_i32_16x16x64_i8 v[38:41], v[146:149], v[138:141], v[38:41]
	v_mfma_i32_16x16x64_i8 v[34:37], v[154:157], v[138:141], v[34:37]
	v_mfma_i32_16x16x64_i8 v[22:25], v[146:149], v[186:189], v[22:25]
	v_mfma_i32_16x16x64_i8 v[18:21], v[154:157], v[186:189], v[18:21]
	v_mfma_i32_16x16x64_i8 v[6:9], v[146:149], v[194:197], v[6:9]
	v_mfma_i32_16x16x64_i8 v[2:5], v[154:157], v[194:197], v[2:5]
	v_mfma_i32_16x16x64_i8 v[70:73], v[150:153], v[126:129], v[70:73]
	v_mfma_i32_16x16x64_i8 v[62:65], v[158:161], v[126:129], v[62:65]
	v_mfma_i32_16x16x64_i8 v[38:41], v[150:153], v[142:145], v[38:41]
	v_mfma_i32_16x16x64_i8 v[34:37], v[158:161], v[142:145], v[34:37]
	v_mfma_i32_16x16x64_i8 v[22:25], v[150:153], v[190:193], v[22:25]
	v_mfma_i32_16x16x64_i8 v[18:21], v[158:161], v[190:193], v[18:21]
	v_mfma_i32_16x16x64_i8 v[6:9], v[150:153], v[198:201], v[6:9]
	v_mfma_i32_16x16x64_i8 v[2:5], v[158:161], v[198:201], v[2:5]
	s_setprio 0
	s_barrier
	s_add_i32 s83, s82, 0x2000
	s_mov_b32 m0, s82
	s_nop 0
	global_load_lds_dwordx4 v180, s[62:63]
	s_nop 0
	s_mov_b32 m0, s83
	s_nop 0
	global_load_lds_dwordx4 v181, s[62:63]
	v_add_u32_e32 v122, 0x18000, v184
	ds_read_b128 v[146:149], v122
	ds_read_b128 v[150:153], v122 offset:1024
	ds_read_b128 v[154:157], v122 offset:2048
	ds_read_b128 v[158:161], v122 offset:3072
	v_add_u32_e32 v122, 0x1c000, v184
	ds_read_b128 v[162:165], v122
	ds_read_b128 v[166:169], v122 offset:1024
	ds_read_b128 v[170:173], v122 offset:2048
	ds_read_b128 v[174:177], v122 offset:3072
	ds_read_b128 v[186:189], v185 offset:32768
	ds_read_b128 v[190:193], v185 offset:33792
	ds_read_b128 v[194:197], v185 offset:34816
	ds_read_b128 v[198:201], v185 offset:35840
	ds_read_b128 v[202:205], v185 offset:36864
	ds_read_b128 v[206:209], v185 offset:37888
	ds_read_b128 v[210:213], v185 offset:38912
	ds_read_b128 v[214:217], v185 offset:39936
	s_add_u32 s62, s62, 0x20000
	s_addc_u32 s63, s63, 0
	s_add_i32 s83, s82, 0x4000
	s_mov_b32 m0, s83
	s_nop 0
	global_load_lds_dwordx4 v180, s[62:63]
	s_add_i32 s83, s82, 0x6000
	s_mov_b32 m0, s83
	s_nop 0
	global_load_lds_dwordx4 v181, s[62:63]
	s_waitcnt vmcnt(8)
	s_waitcnt lgkmcnt(0)
	s_barrier
; #define PG8_STAGE(bufoff, gbase, voff) do { PG8_GLDS((const char*)(gbase), (voff)[0], ldsb + (bufoff)); PG8_GLDS((const char*)(gbase), (voff)[1], ldsb + (bufoff) + 8192u); } while (0)
; #define PG8_STAGEA(bufoff, gbase, o0, o1) do { PG8_GLDS((const char*)(gbase), (o0), ldsb + (bufoff)); PG8_GLDS((const char*)(gbase), (o1), ldsb + (bufoff) + 8192u); } while (0)
; #define PG8_LDA(dst, b, h) do { if constexpr (F8) { _Pragma("unroll") for (int m = 0; m < 4; ++m) dst##8[m] = PG8_LD32(lds + PG8_SA(b, h) + aoff + m * 2048); } else { \
;         _Pragma("unroll") for (int m = 0; m < 4; ++m) _Pragma("unroll") for (int k = 0; k < 2; ++k) dst[m][k] = *(const LAS bf16x8*)(lds + PG8_SA(b, h) + aoff + m * 2048 + k * 1024); } } while (0)
; #define PG8_WAIT_VR() PG8_WAIT_V(8)
; #define PG8_WAIT_L(n) asm volatile("s_waitcnt lgkmcnt(" #n ")" ::: "memory")
; #define PG8_BAR __builtin_amdgcn_s_barrier()
; #define PG8_SCHED __builtin_amdgcn_sched_barrier(0)
; template <class Epi, class Sched, bool F8 = false, bool PF = false, bool I8 = false, int PID = -1>
; __device__ __forceinline__ void gemm_phase(LAS unsigned char* lds, LAS unsigned char* xlds, const int RP, const int RPB, const int nt, const Sched& S, const Epi& E, const int stagger_ticks) {
;     ...
;             PG8_WAIT_VR(); PG8_WAIT_L(0); PG8_BAR; PG8_MMA(0, 0, At, B0); PG8_MMA(0, 1, At, B1); PG8_BAR; PG8_SCHED;
;             PG8_LDA(At, 1, 1); PG8_STAGE(PG8_SB(1, 0), b3, voffB); PG8_STAGE(PG8_SB(1, 1), b3 + hstepB, voffB); PG8_STAGEA(PG8_SA(1, 0), a3, vA0, vA1);
;             PG8_WAIT_VR(); PG8_WAIT_L(0); PG8_BAR; PG8_MMA(1, 0, At, B0); PG8_MMA(1, 1, At, B1); PG8_BAR; PG8_SCHED;
	s_setprio 1
	s_waitcnt lgkmcnt(7)
	v_mfma_i32_16x16x64_i8 v[46:49], v[146:149], v[186:189], v[46:49]
	s_waitcnt lgkmcnt(6)
	v_mfma_i32_16x16x64_i8 v[142:145], v[150:153], v[190:193], v[46:49]
	v_mfma_i32_16x16x64_i8 v[46:49], v[154:157], v[186:189], v[54:57]
	v_mfma_i32_16x16x64_i8 v[138:141], v[158:161], v[190:193], v[46:49]
	s_waitcnt lgkmcnt(5)
	v_mfma_i32_16x16x64_i8 v[46:49], v[146:149], v[194:197], v[58:61]
	s_waitcnt lgkmcnt(4)
	v_mfma_i32_16x16x64_i8 v[126:129], v[150:153], v[198:201], v[46:49]
	v_mfma_i32_16x16x64_i8 v[46:49], v[154:157], v[194:197], v[66:69]
	v_mfma_i32_16x16x64_i8 v[122:125], v[158:161], v[198:201], v[46:49]
	s_waitcnt lgkmcnt(3)
	v_mfma_i32_16x16x64_i8 v[46:49], v[146:149], v[202:205], v[110:113]
	s_waitcnt lgkmcnt(2)
	v_mfma_i32_16x16x64_i8 v[110:113], v[150:153], v[206:209], v[46:49]
	v_mfma_i32_16x16x64_i8 v[46:49], v[154:157], v[202:205], v[106:109]
	v_mfma_i32_16x16x64_i8 v[106:109], v[158:161], v[206:209], v[46:49]
	s_waitcnt lgkmcnt(1)
	v_mfma_i32_16x16x64_i8 v[46:49], v[146:149], v[210:213], v[94:97]
	s_waitcnt lgkmcnt(0)
	v_mfma_i32_16x16x64_i8 v[94:97], v[150:153], v[214:217], v[46:49]
	v_mfma_i32_16x16x64_i8 v[46:49], v[154:157], v[210:213], v[90:93]
	v_mfma_i32_16x16x64_i8 v[90:93], v[158:161], v[214:217], v[46:49]
	v_mfma_i32_16x16x64_i8 v[46:49], v[162:165], v[186:189], v[134:137]
	v_mfma_i32_16x16x64_i8 v[134:137], v[166:169], v[190:193], v[46:49]
	v_mfma_i32_16x16x64_i8 v[46:49], v[170:173], v[186:189], v[130:133]
	v_mfma_i32_16x16x64_i8 v[130:133], v[174:177], v[190:193], v[46:49]
	v_mfma_i32_16x16x64_i8 v[46:49], v[162:165], v[194:197], v[118:121]
	v_mfma_i32_16x16x64_i8 v[118:121], v[166:169], v[198:201], v[46:49]
	v_mfma_i32_16x16x64_i8 v[46:49], v[170:173], v[194:197], v[114:117]
	v_mfma_i32_16x16x64_i8 v[114:117], v[174:177], v[198:201], v[46:49]
	v_mfma_i32_16x16x64_i8 v[46:49], v[162:165], v[202:205], v[102:105]
	v_mfma_i32_16x16x64_i8 v[102:105], v[166:169], v[206:209], v[46:49]
	v_mfma_i32_16x16x64_i8 v[46:49], v[170:173], v[202:205], v[98:101]
	v_mfma_i32_16x16x64_i8 v[98:101], v[174:177], v[206:209], v[46:49]
	v_mfma_i32_16x16x64_i8 v[46:49], v[162:165], v[210:213], v[86:89]
	v_mfma_i32_16x16x64_i8 v[86:89], v[166:169], v[214:217], v[46:49]
	v_mfma_i32_16x16x64_i8 v[46:49], v[170:173], v[210:213], v[82:85]
	v_mfma_i32_16x16x64_i8 v[82:85], v[174:177], v[214:217], v[46:49]
	s_setprio 0
	s_barrier
	s_nop 4
	ds_read_b128 v[46:49], v185 offset:49152
	ds_read_b128 v[54:57], v185 offset:50176
	ds_read_b128 v[58:61], v185 offset:51200
	ds_read_b128 v[66:69], v185 offset:52224
	ds_read_b128 v[186:189], v185 offset:53248
	ds_read_b128 v[190:193], v185 offset:54272
	ds_read_b128 v[194:197], v185 offset:55296
	ds_read_b128 v[198:201], v185 offset:56320
	s_add_i32 s62, s82, 0x18000
	s_mov_b32 m0, s62
	s_nop 0
	global_load_lds_dwordx4 v182, s[60:61]
	s_add_i32 s62, s82, 0x1a000
	s_mov_b32 m0, s62
	s_nop 0
	global_load_lds_dwordx4 v183, s[60:61]
	s_add_u32 s50, s50, 0x2080
	s_addc_u32 s51, s51, 0
	s_add_i32 s60, s82, 0x1c000
	s_mov_b32 m0, s60
	s_nop 0
	global_load_lds_dwordx4 v182, s[50:51]
	s_add_i32 s60, s82, 0x1e000
	s_mov_b32 m0, s60
	s_nop 0
	global_load_lds_dwordx4 v183, s[50:51]
	s_waitcnt vmcnt(6)
	s_waitcnt lgkmcnt(0)
	s_barrier
	s_setprio 1
	s_waitcnt lgkmcnt(7)
	v_mfma_i32_16x16x64_i8 v[78:81], v[146:149], v[46:49], v[78:81]
	v_mfma_i32_16x16x64_i8 v[74:77], v[154:157], v[46:49], v[74:77]
	s_waitcnt lgkmcnt(5)
	v_mfma_i32_16x16x64_i8 v[50:53], v[146:149], v[58:61], v[50:53]
	v_mfma_i32_16x16x64_i8 v[42:45], v[154:157], v[58:61], v[42:45]
	s_waitcnt lgkmcnt(3)
	v_mfma_i32_16x16x64_i8 v[30:33], v[146:149], v[186:189], v[30:33]
	v_mfma_i32_16x16x64_i8 v[26:29], v[154:157], v[186:189], v[26:29]
	s_waitcnt lgkmcnt(1)
	v_mfma_i32_16x16x64_i8 v[14:17], v[146:149], v[194:197], v[14:17]
	v_mfma_i32_16x16x64_i8 v[10:13], v[154:157], v[194:197], v[10:13]
	v_mfma_i32_16x16x64_i8 v[78:81], v[150:153], v[54:57], v[78:81]
	v_mfma_i32_16x16x64_i8 v[74:77], v[158:161], v[54:57], v[74:77]
	v_mfma_i32_16x16x64_i8 v[50:53], v[150:153], v[66:69], v[50:53]
	v_mfma_i32_16x16x64_i8 v[42:45], v[158:161], v[66:69], v[42:45]
	v_mfma_i32_16x16x64_i8 v[30:33], v[150:153], v[190:193], v[30:33]
	v_mfma_i32_16x16x64_i8 v[26:29], v[158:161], v[190:193], v[26:29]
	s_waitcnt lgkmcnt(0)
	v_mfma_i32_16x16x64_i8 v[14:17], v[150:153], v[198:201], v[14:17]
	v_mfma_i32_16x16x64_i8 v[10:13], v[158:161], v[198:201], v[10:13]
	v_mfma_i32_16x16x64_i8 v[70:73], v[162:165], v[46:49], v[70:73]
	v_mfma_i32_16x16x64_i8 v[46:49], v[170:173], v[46:49], v[62:65]
	v_mfma_i32_16x16x64_i8 v[38:41], v[162:165], v[58:61], v[38:41]
	v_mfma_i32_16x16x64_i8 v[34:37], v[170:173], v[58:61], v[34:37]
	v_mfma_i32_16x16x64_i8 v[22:25], v[162:165], v[186:189], v[22:25]
	v_mfma_i32_16x16x64_i8 v[18:21], v[170:173], v[186:189], v[18:21]
	v_mfma_i32_16x16x64_i8 v[6:9], v[162:165], v[194:197], v[6:9]
	v_mfma_i32_16x16x64_i8 v[2:5], v[170:173], v[194:197], v[2:5]
	v_mfma_i32_16x16x64_i8 v[70:73], v[166:169], v[54:57], v[70:73]
	v_mfma_i32_16x16x64_i8 v[62:65], v[174:177], v[54:57], v[46:49]
	v_mfma_i32_16x16x64_i8 v[38:41], v[166:169], v[66:69], v[38:41]
	v_mfma_i32_16x16x64_i8 v[34:37], v[174:177], v[66:69], v[34:37]
	v_mfma_i32_16x16x64_i8 v[22:25], v[166:169], v[190:193], v[22:25]
	v_mfma_i32_16x16x64_i8 v[18:21], v[174:177], v[190:193], v[18:21]
	v_mfma_i32_16x16x64_i8 v[6:9], v[166:169], v[198:201], v[6:9]
	v_mfma_i32_16x16x64_i8 v[2:5], v[174:177], v[198:201], v[2:5]
	s_setprio 0
	s_barrier
	s_add_i32 s79, s79, 2
	s_add_u32 s76, s76, 0x100
	s_addc_u32 s77, s77, 0
	s_add_u32 s2, s2, 0x100
	s_addc_u32 s3, s3, 0
	s_cmp_gt_u32 s79, 5
	s_cbranch_scc1 .LBB0_216
; #define PG8_STAGEA1(bufoff, gbase) do { if constexpr (Sched::GATHER) { PG8_STAGEA(bufoff, gbase, vA2, vA3); } else { PG8_STAGEA(bufoff, (gbase) + hstep, vA0, vA1); } } while (0)
; #define PG8_LDA(dst, b, h) do { if constexpr (F8) { _Pragma("unroll") for (int m = 0; m < 4; ++m) dst##8[m] = PG8_LD32(lds + PG8_SA(b, h) + aoff + m * 2048); } else { \
;         _Pragma("unroll") for (int m = 0; m < 4; ++m) _Pragma("unroll") for (int k = 0; k < 2; ++k) dst[m][k] = *(const LAS bf16x8*)(lds + PG8_SA(b, h) + aoff + m * 2048 + k * 1024); } } while (0)
; #define PG8_LDB(dst, b, h) do { if constexpr (F8) { _Pragma("unroll") for (int n = 0; n < 2; ++n) dst##8[n] = PG8_LD32(lds + PG8_SB(b, h) + boff + n * 2048); } else { \
;         _Pragma("unroll") for (int n = 0; n < 2; ++n) _Pragma("unroll") for (int k = 0; k < 2; ++k) dst[n][k] = *(const LAS bf16x8*)(lds + PG8_SB(b, h) + boff + n * 2048 + k * 1024); } } while (0)
; #define PG8_WAIT_VX() do { if (relax) asm volatile("s_waitcnt vmcnt(%0)" :: "n"(8 + Epi::RELAX) : "memory"); else PG8_WAIT_V(8); } while (0)
; #define PG8_WAIT_L(n) asm volatile("s_waitcnt lgkmcnt(" #n ")" ::: "memory")
; #define PG8_BAR __builtin_amdgcn_s_barrier()
; #define PG8_SCHED __builtin_amdgcn_sched_barrier(0)
; template <class Epi, class Sched, bool F8 = false, bool PF = false, bool I8 = false, int PID = -1>
; __device__ __forceinline__ void gemm_phase(LAS unsigned char* lds, LAS unsigned char* xlds, const int RP, const int RPB, const int nt, const Sched& S, const Epi& E, const int stagger_ticks) {
;     ...
;             PG8_LDB(B0, 0, 0); PG8_LDB(B1, 0, 1); PG8_SCHED; PG8_LDA(At, 0, 0); PG8_STAGEA1(PG8_SA(1, 1), a1);
;             if (Sched::GATHER) { if (last) { const u32x4 nv = *nslot; vA0 = nv.x; vA1 = nv.y; vA2 = nv.z; vA3 = nv.w; } }
;             PG8_WAIT_VX(); PG8_WAIT_L(0); PG8_BAR; PG8_MMA(0, 0, At, B0); PG8_MMA(0, 1, At, B1); PG8_BAR; PG8_SCHED;
;             if constexpr (Epi::BIAS_DMA) { if (t == 0 && has_next) E.bias_dma(nxt, xlds + 8192 + ((ui + 1) & 1) * Epi::BIAS_STRIDE, wid, lane); }
.LBB0_214:
	s_mov_b32 s82, s7
	s_add_u32 s100, s2, 0xfffe0000
	s_addc_u32 s101, s3, -1
	s_add_i32 s48, s82, 0x8000
	s_mov_b32 m0, s48
	s_nop 0
	global_load_lds_dwordx4 v180, s[100:101]
	s_add_i32 s48, s82, 0xa000
	s_mov_b32 m0, s48
	s_nop 0
	global_load_lds_dwordx4 v181, s[100:101]
	v_add_u32_e32 v46, 0x10000, v184
	ds_read_b128 v[162:165], v46
	ds_read_b128 v[166:169], v46 offset:1024
	ds_read_b128 v[170:173], v46 offset:2048
	ds_read_b128 v[174:177], v46 offset:3072
	v_add_u32_e32 v46, 0x14000, v184
	ds_read_b128 v[146:149], v46
	ds_read_b128 v[150:153], v46 offset:1024
	ds_read_b128 v[154:157], v46 offset:2048
	ds_read_b128 v[158:161], v46 offset:3072
	ds_read_b128 v[186:189], v185
	ds_read_b128 v[190:193], v185 offset:1024
	ds_read_b128 v[194:197], v185 offset:2048
	ds_read_b128 v[198:201], v185 offset:3072
	ds_read_b128 v[202:205], v185 offset:4096
	ds_read_b128 v[206:209], v185 offset:5120
	ds_read_b128 v[210:213], v185 offset:6144
	ds_read_b128 v[214:217], v185 offset:7168
	s_add_i32 s48, s82, 0xc000
	s_mov_b32 m0, s48
	s_nop 0
	global_load_lds_dwordx4 v180, s[2:3]
	s_add_i32 s48, s82, 0xe000
	s_mov_b32 m0, s48
	s_nop 0
	global_load_lds_dwordx4 v181, s[2:3]
	s_waitcnt vmcnt(8)
	s_waitcnt lgkmcnt(0)
	s_barrier
	s_setprio 1
	s_waitcnt lgkmcnt(7)
	v_mfma_i32_16x16x64_i8 v[46:49], v[162:165], v[186:189], v[142:145]
	v_mfma_i32_16x16x64_i8 v[54:57], v[170:173], v[186:189], v[138:141]
	s_waitcnt lgkmcnt(5)
	v_mfma_i32_16x16x64_i8 v[58:61], v[162:165], v[194:197], v[126:129]
	v_mfma_i32_16x16x64_i8 v[66:69], v[170:173], v[194:197], v[122:125]
	s_waitcnt lgkmcnt(3)
	v_mfma_i32_16x16x64_i8 v[110:113], v[162:165], v[202:205], v[110:113]
	v_mfma_i32_16x16x64_i8 v[106:109], v[170:173], v[202:205], v[106:109]
	s_waitcnt lgkmcnt(1)
	v_mfma_i32_16x16x64_i8 v[94:97], v[162:165], v[210:213], v[94:97]
	v_mfma_i32_16x16x64_i8 v[90:93], v[170:173], v[210:213], v[90:93]
	v_mfma_i32_16x16x64_i8 v[46:49], v[166:169], v[190:193], v[46:49]
	v_mfma_i32_16x16x64_i8 v[54:57], v[174:177], v[190:193], v[54:57]
	v_mfma_i32_16x16x64_i8 v[58:61], v[166:169], v[198:201], v[58:61]
	v_mfma_i32_16x16x64_i8 v[66:69], v[174:177], v[198:201], v[66:69]
	v_mfma_i32_16x16x64_i8 v[110:113], v[166:169], v[206:209], v[110:113]
	v_mfma_i32_16x16x64_i8 v[106:109], v[174:177], v[206:209], v[106:109]
	s_waitcnt lgkmcnt(0)
	v_mfma_i32_16x16x64_i8 v[94:97], v[166:169], v[214:217], v[94:97]
	v_mfma_i32_16x16x64_i8 v[90:93], v[174:177], v[214:217], v[90:93]
	v_mfma_i32_16x16x64_i8 v[122:125], v[146:149], v[186:189], v[134:137]
	v_mfma_i32_16x16x64_i8 v[134:137], v[150:153], v[190:193], v[122:125]
	v_mfma_i32_16x16x64_i8 v[122:125], v[154:157], v[186:189], v[130:133]
	v_mfma_i32_16x16x64_i8 v[118:121], v[146:149], v[194:197], v[118:121]
	v_mfma_i32_16x16x64_i8 v[114:117], v[154:157], v[194:197], v[114:117]
	v_mfma_i32_16x16x64_i8 v[102:105], v[146:149], v[202:205], v[102:105]
	v_mfma_i32_16x16x64_i8 v[98:101], v[154:157], v[202:205], v[98:101]
	v_mfma_i32_16x16x64_i8 v[86:89], v[146:149], v[210:213], v[86:89]
	v_mfma_i32_16x16x64_i8 v[82:85], v[154:157], v[210:213], v[82:85]
	v_mfma_i32_16x16x64_i8 v[130:133], v[158:161], v[190:193], v[122:125]
	v_mfma_i32_16x16x64_i8 v[118:121], v[150:153], v[198:201], v[118:121]
	v_mfma_i32_16x16x64_i8 v[114:117], v[158:161], v[198:201], v[114:117]
	v_mfma_i32_16x16x64_i8 v[102:105], v[150:153], v[206:209], v[102:105]
	v_mfma_i32_16x16x64_i8 v[98:101], v[158:161], v[206:209], v[98:101]
	v_mfma_i32_16x16x64_i8 v[86:89], v[150:153], v[214:217], v[86:89]
	v_mfma_i32_16x16x64_i8 v[82:85], v[158:161], v[214:217], v[82:85]
	s_setprio 0
	s_barrier
	s_cmp_lg_u32 s79, -2
	s_cselect_b64 s[48:49], -1, 0
	s_or_b64 s[48:49], s[46:47], s[48:49]
	s_and_b64 vcc, exec, s[48:49]
	s_cbranch_vccnz .LBB0_213
	s_mov_b32 m0, s78
	s_nop 0
	global_load_lds_dword v1, s[0:1]
	s_branch .LBB0_213
.Lmy_z1t:
	s_mov_b32 s82, s7
	s_add_u32 s100, s2, 0xfffe0000
	s_addc_u32 s101, s3, -1
	s_add_i32 s48, s82, 0x8000
	s_mov_b32 m0, s48
	s_nop 0
	global_load_lds_dwordx4 v180, s[100:101]
	s_add_i32 s48, s82, 0xa000
	s_mov_b32 m0, s48
	s_nop 0
	global_load_lds_dwordx4 v181, s[100:101]
	v_add_u32_e32 v46, 0x10000, v184
	ds_read_b128 v[162:165], v46
	ds_read_b128 v[166:169], v46 offset:1024
	ds_read_b128 v[170:173], v46 offset:2048
	ds_read_b128 v[174:177], v46 offset:3072
	v_add_u32_e32 v46, 0x14000, v184
	ds_read_b128 v[146:149], v46
	ds_read_b128 v[150:153], v46 offset:1024
	ds_read_b128 v[154:157], v46 offset:2048
	ds_read_b128 v[158:161], v46 offset:3072
	ds_read_b128 v[186:189], v185
	ds_read_b128 v[190:193], v185 offset:1024
	ds_read_b128 v[194:197], v185 offset:2048
	ds_read_b128 v[198:201], v185 offset:3072
	ds_read_b128 v[202:205], v185 offset:4096
	ds_read_b128 v[206:209], v185 offset:5120
	ds_read_b128 v[210:213], v185 offset:6144
	ds_read_b128 v[214:217], v185 offset:7168
	s_add_i32 s48, s82, 0xc000
	s_mov_b32 m0, s48
	s_nop 0
	global_load_lds_dwordx4 v180, s[2:3]
	s_add_i32 s48, s82, 0xe000
	s_mov_b32 m0, s48
	s_nop 0
	global_load_lds_dwordx4 v181, s[2:3]
	s_waitcnt vmcnt(8)
	s_waitcnt lgkmcnt(0)
	s_barrier
; #define PG8_STAGE(bufoff, gbase, voff) do { PG8_GLDS((const char*)(gbase), (voff)[0], ldsb + (bufoff)); PG8_GLDS((const char*)(gbase), (voff)[1], ldsb + (bufoff) + 8192u); } while (0)
; #define PG8_STAGEA(bufoff, gbase, o0, o1) do { PG8_GLDS((const char*)(gbase), (o0), ldsb + (bufoff)); PG8_GLDS((const char*)(gbase), (o1), ldsb + (bufoff) + 8192u); } while (0)
; #define PG8_STAGEA1(bufoff, gbase) do { if constexpr (Sched::GATHER) { PG8_STAGEA(bufoff, gbase, vA2, vA3); } else { PG8_STAGEA(bufoff, (gbase) + hstep, vA0, vA1); } } while (0)
; #define PG8_LDA(dst, b, h) do { if constexpr (F8) { _Pragma("unroll") for (int m = 0; m < 4; ++m) dst##8[m] = PG8_LD32(lds + PG8_SA(b, h) + aoff + m * 2048); } else { \
;         _Pragma("unroll") for (int m = 0; m < 4; ++m) _Pragma("unroll") for (int k = 0; k < 2; ++k) dst[m][k] = *(const LAS bf16x8*)(lds + PG8_SA(b, h) + aoff + m * 2048 + k * 1024); } } while (0)
; #define PG8_LDB(dst, b, h) do { if constexpr (F8) { _Pragma("unroll") for (int n = 0; n < 2; ++n) dst##8[n] = PG8_LD32(lds + PG8_SB(b, h) + boff + n * 2048); } else { \
;         _Pragma("unroll") for (int n = 0; n < 2; ++n) _Pragma("unroll") for (int k = 0; k < 2; ++k) dst[n][k] = *(const LAS bf16x8*)(lds + PG8_SB(b, h) + boff + n * 2048 + k * 1024); } } while (0)
; template <class Epi, class Sched, bool F8 = false, bool PF = false, bool I8 = false, int PID = -1>
; __device__ __forceinline__ void gemm_phase(LAS unsigned char* lds, LAS unsigned char* xlds, const int RP, const int RPB, const int nt, const Sched& S, const Epi& E, const int stagger_ticks) {
;     ...
;             PG8_LDB(B0, 0, 0); PG8_LDB(B1, 0, 1); PG8_SCHED; PG8_LDA(At, 0, 0); PG8_STAGEA1(PG8_SA(1, 1), a1);
;             if (Sched::GATHER) { if (last) { const u32x4 nv = *nslot; vA0 = nv.x; vA1 = nv.y; vA2 = nv.z; vA3 = nv.w; } }
;             PG8_WAIT_VX(); PG8_WAIT_L(0); PG8_BAR; PG8_MMA(0, 0, At, B0); PG8_MMA(0, 1, At, B1); PG8_BAR; PG8_SCHED;
;             if constexpr (Epi::BIAS_DMA) { if (t == 0 && has_next) E.bias_dma(nxt, xlds + 8192 + ((ui + 1) & 1) * Epi::BIAS_STRIDE, wid, lane); }
;             PG8_LDA(At, 0, 1); PG8_STAGE(PG8_SB(0, 0), b2, voffB); PG8_STAGE(PG8_SB(0, 1), b2 + hstepB, voffB); PG8_STAGEA(PG8_SA(0, 0), a2, vA0, vA1);
;             PG8_WAIT_VX(); PG8_WAIT_L(0); PG8_BAR; PG8_MMA(1, 0, At, B0); PG8_MMA(1, 1, At, B1); PG8_BAR; PG8_SCHED;
	s_setprio 1
	s_waitcnt lgkmcnt(7)
	v_mfma_i32_16x16x64_i8 v[46:49], v[162:165], v[186:189], 0
	v_mfma_i32_16x16x64_i8 v[54:57], v[170:173], v[186:189], 0
	s_waitcnt lgkmcnt(5)
	v_mfma_i32_16x16x64_i8 v[58:61], v[162:165], v[194:197], 0
	v_mfma_i32_16x16x64_i8 v[66:69], v[170:173], v[194:197], 0
	s_waitcnt lgkmcnt(3)
	v_mfma_i32_16x16x64_i8 v[110:113], v[162:165], v[202:205], 0
	v_mfma_i32_16x16x64_i8 v[106:109], v[170:173], v[202:205], 0
	s_waitcnt lgkmcnt(1)
	v_mfma_i32_16x16x64_i8 v[94:97], v[162:165], v[210:213], 0
	v_mfma_i32_16x16x64_i8 v[90:93], v[170:173], v[210:213], 0
	v_mfma_i32_16x16x64_i8 v[46:49], v[166:169], v[190:193], v[46:49]
	v_mfma_i32_16x16x64_i8 v[54:57], v[174:177], v[190:193], v[54:57]
	v_mfma_i32_16x16x64_i8 v[58:61], v[166:169], v[198:201], v[58:61]
	v_mfma_i32_16x16x64_i8 v[66:69], v[174:177], v[198:201], v[66:69]
	v_mfma_i32_16x16x64_i8 v[110:113], v[166:169], v[206:209], v[110:113]
	v_mfma_i32_16x16x64_i8 v[106:109], v[174:177], v[206:209], v[106:109]
	s_waitcnt lgkmcnt(0)
	v_mfma_i32_16x16x64_i8 v[94:97], v[166:169], v[214:217], v[94:97]
	v_mfma_i32_16x16x64_i8 v[90:93], v[174:177], v[214:217], v[90:93]
	v_mfma_i32_16x16x64_i8 v[122:125], v[146:149], v[186:189], 0
	v_mfma_i32_16x16x64_i8 v[134:137], v[150:153], v[190:193], v[122:125]
	v_mfma_i32_16x16x64_i8 v[122:125], v[154:157], v[186:189], 0
	v_mfma_i32_16x16x64_i8 v[118:121], v[146:149], v[194:197], 0
	v_mfma_i32_16x16x64_i8 v[114:117], v[154:157], v[194:197], 0
	v_mfma_i32_16x16x64_i8 v[102:105], v[146:149], v[202:205], 0
	v_mfma_i32_16x16x64_i8 v[98:101], v[154:157], v[202:205], 0
	v_mfma_i32_16x16x64_i8 v[86:89], v[146:149], v[210:213], 0
	v_mfma_i32_16x16x64_i8 v[82:85], v[154:157], v[210:213], 0
	v_mfma_i32_16x16x64_i8 v[130:133], v[158:161], v[190:193], v[122:125]
	v_mfma_i32_16x16x64_i8 v[118:121], v[150:153], v[198:201], v[118:121]
	v_mfma_i32_16x16x64_i8 v[114:117], v[158:161], v[198:201], v[114:117]
	v_mfma_i32_16x16x64_i8 v[102:105], v[150:153], v[206:209], v[102:105]
	v_mfma_i32_16x16x64_i8 v[98:101], v[158:161], v[206:209], v[98:101]
	v_mfma_i32_16x16x64_i8 v[86:89], v[150:153], v[214:217], v[86:89]
	v_mfma_i32_16x16x64_i8 v[82:85], v[158:161], v[214:217], v[82:85]
	s_setprio 0
	s_barrier
	s_cmp_lg_u32 s79, -2
	s_cselect_b64 s[48:49], -1, 0
	s_or_b64 s[48:49], s[46:47], s[48:49]
	s_and_b64 vcc, exec, s[48:49]
	s_cbranch_vccnz .Lmy_z1b
	s_mov_b32 m0, s78
	s_nop 0
	global_load_lds_dword v1, s[0:1]
	s_branch .Lmy_z1b
.Lmy_z1b:
	s_add_u32 s48, s2, 0xfffe0080
	s_addc_u32 s49, s3, -1
	s_cmp_eq_u32 s79, 4
	s_cselect_b32 s62, s10, s48
	s_cselect_b32 s63, s11, s49
	s_cselect_b32 s50, s12, s76
	s_cselect_b32 s51, s13, s77
	s_add_u32 s48, s62, 0x80
	s_addc_u32 s49, s63, 0
	s_add_u32 s60, s50, 0x80
	s_addc_u32 s61, s51, 0
	ds_read_b128 v[122:125], v185 offset:16384
	ds_read_b128 v[126:129], v185 offset:17408
	ds_read_b128 v[138:141], v185 offset:18432
	ds_read_b128 v[142:145], v185 offset:19456
	ds_read_b128 v[186:189], v185 offset:20480
	ds_read_b128 v[190:193], v185 offset:21504
	ds_read_b128 v[194:197], v185 offset:22528
	ds_read_b128 v[198:201], v185 offset:23552
	s_add_i32 s83, s82, 0x10000
	s_mov_b32 m0, s83
	s_nop 0
	global_load_lds_dwordx4 v182, s[50:51]
	s_add_i32 s83, s82, 0x12000
	s_mov_b32 m0, s83
	s_nop 0
	global_load_lds_dwordx4 v183, s[50:51]
	s_add_u32 s86, s50, 0x2000
	s_addc_u32 s87, s51, 0
	s_add_i32 s83, s82, 0x14000
	s_mov_b32 m0, s83
	s_nop 0
	global_load_lds_dwordx4 v182, s[86:87]
	s_add_i32 s83, s82, 0x16000
	s_mov_b32 m0, s83
	s_nop 0
	global_load_lds_dwordx4 v183, s[86:87]
	s_waitcnt vmcnt(6)
	s_waitcnt lgkmcnt(0)
	s_barrier
	s_setprio 1
	s_waitcnt lgkmcnt(7)
	v_mfma_i32_16x16x64_i8 v[78:81], v[162:165], v[122:125], 0
	v_mfma_i32_16x16x64_i8 v[74:77], v[170:173], v[122:125], 0
	s_waitcnt lgkmcnt(5)
	v_mfma_i32_16x16x64_i8 v[50:53], v[162:165], v[138:141], 0
	v_mfma_i32_16x16x64_i8 v[42:45], v[170:173], v[138:141], 0
	s_waitcnt lgkmcnt(3)
	v_mfma_i32_16x16x64_i8 v[30:33], v[162:165], v[186:189], 0
	v_mfma_i32_16x16x64_i8 v[26:29], v[170:173], v[186:189], 0
	s_waitcnt lgkmcnt(1)
	v_mfma_i32_16x16x64_i8 v[14:17], v[162:165], v[194:197], 0
	v_mfma_i32_16x16x64_i8 v[10:13], v[170:173], v[194:197], 0
	v_mfma_i32_16x16x64_i8 v[78:81], v[166:169], v[126:129], v[78:81]
	v_mfma_i32_16x16x64_i8 v[74:77], v[174:177], v[126:129], v[74:77]
	v_mfma_i32_16x16x64_i8 v[50:53], v[166:169], v[142:145], v[50:53]
	v_mfma_i32_16x16x64_i8 v[42:45], v[174:177], v[142:145], v[42:45]
	v_mfma_i32_16x16x64_i8 v[30:33], v[166:169], v[190:193], v[30:33]
	v_mfma_i32_16x16x64_i8 v[26:29], v[174:177], v[190:193], v[26:29]
	s_waitcnt lgkmcnt(0)
	v_mfma_i32_16x16x64_i8 v[14:17], v[166:169], v[198:201], v[14:17]
	v_mfma_i32_16x16x64_i8 v[10:13], v[174:177], v[198:201], v[10:13]
	v_mfma_i32_16x16x64_i8 v[70:73], v[146:149], v[122:125], 0
	v_mfma_i32_16x16x64_i8 v[62:65], v[154:157], v[122:125], 0
	v_mfma_i32_16x16x64_i8 v[38:41], v[146:149], v[138:141], 0
	v_mfma_i32_16x16x64_i8 v[34:37], v[154:157], v[138:141], 0
	v_mfma_i32_16x16x64_i8 v[22:25], v[146:149], v[186:189], 0
	v_mfma_i32_16x16x64_i8 v[18:21], v[154:157], v[186:189], 0
	v_mfma_i32_16x16x64_i8 v[6:9], v[146:149], v[194:197], 0
	v_mfma_i32_16x16x64_i8 v[2:5], v[154:157], v[194:197], 0
	v_mfma_i32_16x16x64_i8 v[70:73], v[150:153], v[126:129], v[70:73]
	v_mfma_i32_16x16x64_i8 v[62:65], v[158:161], v[126:129], v[62:65]
	v_mfma_i32_16x16x64_i8 v[38:41], v[150:153], v[142:145], v[38:41]
	v_mfma_i32_16x16x64_i8 v[34:37], v[158:161], v[142:145], v[34:37]
	v_mfma_i32_16x16x64_i8 v[22:25], v[150:153], v[190:193], v[22:25]
	v_mfma_i32_16x16x64_i8 v[18:21], v[158:161], v[190:193], v[18:21]
	v_mfma_i32_16x16x64_i8 v[6:9], v[150:153], v[198:201], v[6:9]
	v_mfma_i32_16x16x64_i8 v[2:5], v[158:161], v[198:201], v[2:5]
	s_setprio 0
	s_barrier
; #define PG8_STAGE(bufoff, gbase, voff) do { PG8_GLDS((const char*)(gbase), (voff)[0], ldsb + (bufoff)); PG8_GLDS((const char*)(gbase), (voff)[1], ldsb + (bufoff) + 8192u); } while (0)
; #define PG8_STAGEA(bufoff, gbase, o0, o1) do { PG8_GLDS((const char*)(gbase), (o0), ldsb + (bufoff)); PG8_GLDS((const char*)(gbase), (o1), ldsb + (bufoff) + 8192u); } while (0)
; #define PG8_STAGEA1(bufoff, gbase) do { if constexpr (Sched::GATHER) { PG8_STAGEA(bufoff, gbase, vA2, vA3); } else { PG8_STAGEA(bufoff, (gbase) + hstep, vA0, vA1); } } while (0)
; #define PG8_LDA(dst, b, h) do { if constexpr (F8) { _Pragma("unroll") for (int m = 0; m < 4; ++m) dst##8[m] = PG8_LD32(lds + PG8_SA(b, h) + aoff + m * 2048); } else { \
;         _Pragma("unroll") for (int m = 0; m < 4; ++m) _Pragma("unroll") for (int k = 0; k < 2; ++k) dst[m][k] = *(const LAS bf16x8*)(lds + PG8_SA(b, h) + aoff + m * 2048 + k * 1024); } } while (0)
; #define PG8_LDB(dst, b, h) do { if constexpr (F8) { _Pragma("unroll") for (int n = 0; n < 2; ++n) dst##8[n] = PG8_LD32(lds + PG8_SB(b, h) + boff + n * 2048); } else { \
;         _Pragma("unroll") for (int n = 0; n < 2; ++n) _Pragma("unroll") for (int k = 0; k < 2; ++k) dst[n][k] = *(const LAS bf16x8*)(lds + PG8_SB(b, h) + boff + n * 2048 + k * 1024); } } while (0)
; #define PG8_WAIT_VR() PG8_WAIT_V(8)
; #define PG8_WAIT_L(n) asm volatile("s_waitcnt lgkmcnt(" #n ")" ::: "memory")
; #define PG8_BAR __builtin_amdgcn_s_barrier()
; #define PG8_SCHED __builtin_amdgcn_sched_barrier(0)
; template <class Epi, class Sched, bool F8 = false, bool PF = false, bool I8 = false, int PID = -1>
; __device__ __forceinline__ void gemm_phase(LAS unsigned char* lds, LAS unsigned char* xlds, const int RP, const int RPB, const int nt, const Sched& S, const Epi& E, const int stagger_ticks) {
;     ...
;             PG8_LDB(B0, 1, 0); PG8_LDB(B1, 1, 1); PG8_SCHED; PG8_LDA(At, 1, 0); PG8_STAGEA1(PG8_SA(0, 1), a2);
;             PG8_WAIT_VR(); PG8_WAIT_L(0); PG8_BAR; PG8_MMA(0, 0, At, B0); PG8_MMA(0, 1, At, B1); PG8_BAR; PG8_SCHED;
;             PG8_LDA(At, 1, 1); PG8_STAGE(PG8_SB(1, 0), b3, voffB); PG8_STAGE(PG8_SB(1, 1), b3 + hstepB, voffB); PG8_STAGEA(PG8_SA(1, 0), a3, vA0, vA1);
;             PG8_WAIT_VR(); PG8_WAIT_L(0); PG8_BAR; PG8_MMA(1, 0, At, B0); PG8_MMA(1, 1, At, B1); PG8_BAR; PG8_SCHED;
	s_add_i32 s83, s82, 0x2000
	s_mov_b32 m0, s82
	s_nop 0
	global_load_lds_dwordx4 v180, s[62:63]
	s_nop 0
	s_mov_b32 m0, s83
	s_nop 0
	global_load_lds_dwordx4 v181, s[62:63]
	v_add_u32_e32 v122, 0x18000, v184
	ds_read_b128 v[146:149], v122
	ds_read_b128 v[150:153], v122 offset:1024
	ds_read_b128 v[154:157], v122 offset:2048
	ds_read_b128 v[158:161], v122 offset:3072
	v_add_u32_e32 v122, 0x1c000, v184
	ds_read_b128 v[162:165], v122
	ds_read_b128 v[166:169], v122 offset:1024
	ds_read_b128 v[170:173], v122 offset:2048
	ds_read_b128 v[174:177], v122 offset:3072
	ds_read_b128 v[186:189], v185 offset:32768
	ds_read_b128 v[190:193], v185 offset:33792
	ds_read_b128 v[194:197], v185 offset:34816
	ds_read_b128 v[198:201], v185 offset:35840
	ds_read_b128 v[202:205], v185 offset:36864
	ds_read_b128 v[206:209], v185 offset:37888
	ds_read_b128 v[210:213], v185 offset:38912
	ds_read_b128 v[214:217], v185 offset:39936
	s_add_u32 s62, s62, 0x20000
	s_addc_u32 s63, s63, 0
	s_add_i32 s83, s82, 0x4000
	s_mov_b32 m0, s83
	s_nop 0
	global_load_lds_dwordx4 v180, s[62:63]
	s_add_i32 s83, s82, 0x6000
	s_mov_b32 m0, s83
	s_nop 0
	global_load_lds_dwordx4 v181, s[62:63]
	s_waitcnt vmcnt(8)
	s_waitcnt lgkmcnt(0)
	s_barrier
	s_setprio 1
	s_waitcnt lgkmcnt(7)
	v_mfma_i32_16x16x64_i8 v[46:49], v[146:149], v[186:189], v[46:49]
	s_waitcnt lgkmcnt(6)
	v_mfma_i32_16x16x64_i8 v[142:145], v[150:153], v[190:193], v[46:49]
	v_mfma_i32_16x16x64_i8 v[46:49], v[154:157], v[186:189], v[54:57]
	v_mfma_i32_16x16x64_i8 v[138:141], v[158:161], v[190:193], v[46:49]
	s_waitcnt lgkmcnt(5)
	v_mfma_i32_16x16x64_i8 v[46:49], v[146:149], v[194:197], v[58:61]
	s_waitcnt lgkmcnt(4)
	v_mfma_i32_16x16x64_i8 v[126:129], v[150:153], v[198:201], v[46:49]
	v_mfma_i32_16x16x64_i8 v[46:49], v[154:157], v[194:197], v[66:69]
	v_mfma_i32_16x16x64_i8 v[122:125], v[158:161], v[198:201], v[46:49]
	s_waitcnt lgkmcnt(3)
	v_mfma_i32_16x16x64_i8 v[46:49], v[146:149], v[202:205], v[110:113]
	s_waitcnt lgkmcnt(2)
	v_mfma_i32_16x16x64_i8 v[110:113], v[150:153], v[206:209], v[46:49]
	v_mfma_i32_16x16x64_i8 v[46:49], v[154:157], v[202:205], v[106:109]
	v_mfma_i32_16x16x64_i8 v[106:109], v[158:161], v[206:209], v[46:49]
	s_waitcnt lgkmcnt(1)
	v_mfma_i32_16x16x64_i8 v[46:49], v[146:149], v[210:213], v[94:97]
	s_waitcnt lgkmcnt(0)
	v_mfma_i32_16x16x64_i8 v[94:97], v[150:153], v[214:217], v[46:49]
	v_mfma_i32_16x16x64_i8 v[46:49], v[154:157], v[210:213], v[90:93]
	v_mfma_i32_16x16x64_i8 v[90:93], v[158:161], v[214:217], v[46:49]
	v_mfma_i32_16x16x64_i8 v[46:49], v[162:165], v[186:189], v[134:137]
	v_mfma_i32_16x16x64_i8 v[134:137], v[166:169], v[190:193], v[46:49]
	v_mfma_i32_16x16x64_i8 v[46:49], v[170:173], v[186:189], v[130:133]
	v_mfma_i32_16x16x64_i8 v[130:133], v[174:177], v[190:193], v[46:49]
	v_mfma_i32_16x16x64_i8 v[46:49], v[162:165], v[194:197], v[118:121]
	v_mfma_i32_16x16x64_i8 v[118:121], v[166:169], v[198:201], v[46:49]
	v_mfma_i32_16x16x64_i8 v[46:49], v[170:173], v[194:197], v[114:117]
	v_mfma_i32_16x16x64_i8 v[114:117], v[174:177], v[198:201], v[46:49]
	v_mfma_i32_16x16x64_i8 v[46:49], v[162:165], v[202:205], v[102:105]
	v_mfma_i32_16x16x64_i8 v[102:105], v[166:169], v[206:209], v[46:49]
	v_mfma_i32_16x16x64_i8 v[46:49], v[170:173], v[202:205], v[98:101]
	v_mfma_i32_16x16x64_i8 v[98:101], v[174:177], v[206:209], v[46:49]
	v_mfma_i32_16x16x64_i8 v[46:49], v[162:165], v[210:213], v[86:89]
	v_mfma_i32_16x16x64_i8 v[86:89], v[166:169], v[214:217], v[46:49]
	v_mfma_i32_16x16x64_i8 v[46:49], v[170:173], v[210:213], v[82:85]
	v_mfma_i32_16x16x64_i8 v[82:85], v[174:177], v[214:217], v[46:49]
	s_setprio 0
	s_barrier
	s_nop 4
	ds_read_b128 v[46:49], v185 offset:49152
	ds_read_b128 v[54:57], v185 offset:50176
	ds_read_b128 v[58:61], v185 offset:51200
	ds_read_b128 v[66:69], v185 offset:52224
	ds_read_b128 v[186:189], v185 offset:53248
	ds_read_b128 v[190:193], v185 offset:54272
	ds_read_b128 v[194:197], v185 offset:55296
	ds_read_b128 v[198:201], v185 offset:56320
	s_add_i32 s62, s82, 0x18000
	s_mov_b32 m0, s62
	s_nop 0
	global_load_lds_dwordx4 v182, s[60:61]
	s_add_i32 s62, s82, 0x1a000
	s_mov_b32 m0, s62
	s_nop 0
	global_load_lds_dwordx4 v183, s[60:61]
	s_add_u32 s50, s50, 0x2080
	s_addc_u32 s51, s51, 0
	s_add_i32 s60, s82, 0x1c000
	s_mov_b32 m0, s60
	s_nop 0
	global_load_lds_dwordx4 v182, s[50:51]
	s_add_i32 s60, s82, 0x1e000
	s_mov_b32 m0, s60
	s_nop 0
	global_load_lds_dwordx4 v183, s[50:51]
	s_waitcnt vmcnt(6)
	s_waitcnt lgkmcnt(0)
	s_barrier
	s_setprio 1
	s_waitcnt lgkmcnt(7)
	v_mfma_i32_16x16x64_i8 v[78:81], v[146:149], v[46:49], v[78:81]
	v_mfma_i32_16x16x64_i8 v[74:77], v[154:157], v[46:49], v[74:77]
	s_waitcnt lgkmcnt(5)
	v_mfma_i32_16x16x64_i8 v[50:53], v[146:149], v[58:61], v[50:53]
	v_mfma_i32_16x16x64_i8 v[42:45], v[154:157], v[58:61], v[42:45]
	s_waitcnt lgkmcnt(3)
	v_mfma_i32_16x16x64_i8 v[30:33], v[146:149], v[186:189], v[30:33]
	v_mfma_i32_16x16x64_i8 v[26:29], v[154:157], v[186:189], v[26:29]
	s_waitcnt lgkmcnt(1)
	v_mfma_i32_16x16x64_i8 v[14:17], v[146:149], v[194:197], v[14:17]
	v_mfma_i32_16x16x64_i8 v[10:13], v[154:157], v[194:197], v[10:13]
	v_mfma_i32_16x16x64_i8 v[78:81], v[150:153], v[54:57], v[78:81]
	v_mfma_i32_16x16x64_i8 v[74:77], v[158:161], v[54:57], v[74:77]
	v_mfma_i32_16x16x64_i8 v[50:53], v[150:153], v[66:69], v[50:53]
	v_mfma_i32_16x16x64_i8 v[42:45], v[158:161], v[66:69], v[42:45]
	v_mfma_i32_16x16x64_i8 v[30:33], v[150:153], v[190:193], v[30:33]
	v_mfma_i32_16x16x64_i8 v[26:29], v[158:161], v[190:193], v[26:29]
	s_waitcnt lgkmcnt(0)
	v_mfma_i32_16x16x64_i8 v[14:17], v[150:153], v[198:201], v[14:17]
	v_mfma_i32_16x16x64_i8 v[10:13], v[158:161], v[198:201], v[10:13]
	v_mfma_i32_16x16x64_i8 v[70:73], v[162:165], v[46:49], v[70:73]
	v_mfma_i32_16x16x64_i8 v[46:49], v[170:173], v[46:49], v[62:65]
	v_mfma_i32_16x16x64_i8 v[38:41], v[162:165], v[58:61], v[38:41]
	v_mfma_i32_16x16x64_i8 v[34:37], v[170:173], v[58:61], v[34:37]
	v_mfma_i32_16x16x64_i8 v[22:25], v[162:165], v[186:189], v[22:25]
	v_mfma_i32_16x16x64_i8 v[18:21], v[170:173], v[186:189], v[18:21]
	v_mfma_i32_16x16x64_i8 v[6:9], v[162:165], v[194:197], v[6:9]
	v_mfma_i32_16x16x64_i8 v[2:5], v[170:173], v[194:197], v[2:5]
	v_mfma_i32_16x16x64_i8 v[70:73], v[166:169], v[54:57], v[70:73]
	v_mfma_i32_16x16x64_i8 v[62:65], v[174:177], v[54:57], v[46:49]
	v_mfma_i32_16x16x64_i8 v[38:41], v[166:169], v[66:69], v[38:41]
	v_mfma_i32_16x16x64_i8 v[34:37], v[174:177], v[66:69], v[34:37]
	v_mfma_i32_16x16x64_i8 v[22:25], v[166:169], v[190:193], v[22:25]
	v_mfma_i32_16x16x64_i8 v[18:21], v[174:177], v[190:193], v[18:21]
	v_mfma_i32_16x16x64_i8 v[6:9], v[166:169], v[198:201], v[6:9]
	v_mfma_i32_16x16x64_i8 v[2:5], v[174:177], v[198:201], v[2:5]
	s_setprio 0
	s_barrier
	s_add_i32 s79, s79, 2
	s_add_u32 s76, s76, 0x100
	s_addc_u32 s77, s77, 0
	s_add_u32 s2, s2, 0x100
	s_addc_u32 s3, s3, 0
	s_cmp_gt_u32 s79, 5
	s_branch .LBB0_214

; #define PG8_STAGE(bufoff, gbase, voff) do { PG8_GLDS((const char*)(gbase), (voff)[0], ldsb + (bufoff)); PG8_GLDS((const char*)(gbase), (voff)[1], ldsb + (bufoff) + 8192u); } while (0)
; #define PG8_STAGEA(bufoff, gbase, o0, o1) do { PG8_GLDS((const char*)(gbase), (o0), ldsb + (bufoff)); PG8_GLDS((const char*)(gbase), (o1), ldsb + (bufoff) + 8192u); } while (0)
; #define PG8_STAGEA1(bufoff, gbase) do { if constexpr (Sched::GATHER) { PG8_STAGEA(bufoff, gbase, vA2, vA3); } else { PG8_STAGEA(bufoff, (gbase) + hstep, vA0, vA1); } } while (0)
; #define PG8_LDA(dst, b, h) do { if constexpr (F8) { _Pragma("unroll") for (int m = 0; m < 4; ++m) dst##8[m] = PG8_LD32(lds + PG8_SA(b, h) + aoff + m * 2048); } else { \
;         _Pragma("unroll") for (int m = 0; m < 4; ++m) _Pragma("unroll") for (int k = 0; k < 2; ++k) dst[m][k] = *(const LAS bf16x8*)(lds + PG8_SA(b, h) + aoff + m * 2048 + k * 1024); } } while (0)
; #define PG8_LDB(dst, b, h) do { if constexpr (F8) { _Pragma("unroll") for (int n = 0; n < 2; ++n) dst##8[n] = PG8_LD32(lds + PG8_SB(b, h) + boff + n * 2048); } else { \
;         _Pragma("unroll") for (int n = 0; n < 2; ++n) _Pragma("unroll") for (int k = 0; k < 2; ++k) dst[n][k] = *(const LAS bf16x8*)(lds + PG8_SB(b, h) + boff + n * 2048 + k * 1024); } } while (0)
; template <class Epi, class Sched, bool F8 = false, bool PF = false, bool I8 = false, int PID = -1>
; __device__ __forceinline__ void gemm_phase(LAS unsigned char* lds, LAS unsigned char* xlds, const int RP, const int RPB, const int nt, const Sched& S, const Epi& E, const int stagger_ticks) {
;     ...
;             PG8_LDB(B0, 0, 0); PG8_LDB(B1, 0, 1); PG8_SCHED; PG8_LDA(At, 0, 0); PG8_STAGEA1(PG8_SA(1, 1), a1);
;             if (Sched::GATHER) { if (last) { const u32x4 nv = *nslot; vA0 = nv.x; vA1 = nv.y; vA2 = nv.z; vA3 = nv.w; } }
;             PG8_WAIT_VX(); PG8_WAIT_L(0); PG8_BAR; PG8_MMA(0, 0, At, B0); PG8_MMA(0, 1, At, B1); PG8_BAR; PG8_SCHED;
;             if constexpr (Epi::BIAS_DMA) { if (t == 0 && has_next) E.bias_dma(nxt, xlds + 8192 + ((ui + 1) & 1) * Epi::BIAS_STRIDE, wid, lane); }
;             PG8_LDA(At, 0, 1); PG8_STAGE(PG8_SB(0, 0), b2, voffB); PG8_STAGE(PG8_SB(0, 1), b2 + hstepB, voffB); PG8_STAGEA(PG8_SA(0, 0), a2, vA0, vA1);
;             PG8_WAIT_VX(); PG8_WAIT_L(0); PG8_BAR; PG8_MMA(1, 0, At, B0); PG8_MMA(1, 1, At, B1); PG8_BAR; PG8_SCHED;
.LBB0_546:
	s_mov_b64 s[36:37], s[10:11]
	s_add_u32 s20, s36, 0x100
	s_mov_b64 s[34:35], s[8:9]
	s_addc_u32 s45, s37, 0
	s_mov_b64 s[8:9], s[0:1]
	s_add_u32 s0, s34, 0x40080
	s_mov_b64 s[10:11], s[2:3]
	s_mov_b32 s15, s4
	s_mov_b32 s19, s6
	s_mov_b32 s6, s18
	s_mov_b32 s4, s14
	s_addc_u32 s1, s35, 0
	s_mov_b32 s46, -2
	s_mov_b32 s47, s5
	s_add_u32 s100, s0, 0xfffc0000
	s_addc_u32 s101, s1, -1
	s_add_i32 s48, s47, 0x8000
	s_mov_b32 m0, s48
	s_nop 0
	global_load_lds_dwordx4 v1, s[100:101]
	s_add_i32 s48, s47, 0xa000
	s_mov_b32 m0, s48
	s_nop 0
	global_load_lds_dwordx4 v192, s[100:101]
	v_add_u32_e32 v142, 0x10000, v195
	v_add_u32_e32 v158, 0x14000, v195
	ds_read_b128 v[130:133], v142
	ds_read_b128 v[134:137], v142 offset:1024
	ds_read_b128 v[138:141], v142 offset:2048
	ds_read_b128 v[142:145], v142 offset:3072
	ds_read_b128 v[146:149], v158
	ds_read_b128 v[150:153], v158 offset:1024
	ds_read_b128 v[154:157], v158 offset:2048
	ds_read_b128 v[158:161], v158 offset:3072
	s_add_u32 s2, s0, 0xfffc0080
	s_addc_u32 s3, s1, -1
	s_cmp_eq_u32 s46, 12
	s_cselect_b32 s36, s8, s2
	s_cselect_b32 s37, s9, s3
	s_cselect_b32 s34, s10, s20
	s_cselect_b32 s35, s11, s45
	s_add_u32 s2, s36, 0x80
	s_addc_u32 s3, s37, 0
	ds_read_b128 v[162:165], v196
	ds_read_b128 v[166:169], v196 offset:1024
	ds_read_b128 v[170:173], v196 offset:2048
	ds_read_b128 v[174:177], v196 offset:3072
	ds_read_b128 v[180:183], v196 offset:4096
	ds_read_b128 v[184:187], v196 offset:5120
	ds_read_b128 v[188:191], v196 offset:6144
	ds_read_b128 v[198:201], v196 offset:7168
	s_add_i32 s48, s47, 0xc000
	s_mov_b32 m0, s48
	s_nop 0
	global_load_lds_dwordx4 v1, s[0:1]
	s_add_i32 s48, s47, 0xe000
	s_mov_b32 m0, s48
	s_nop 0
	global_load_lds_dwordx4 v192, s[0:1]
	s_waitcnt vmcnt(8)
	s_waitcnt lgkmcnt(0)
	s_barrier
	s_setprio 1
	s_waitcnt lgkmcnt(7)
	v_mfma_f32_16x16x32_bf16 v[114:117], v[130:133], v[162:165], 0
	v_mfma_f32_16x16x32_bf16 v[118:121], v[138:141], v[162:165], 0
	s_waitcnt lgkmcnt(5)
	v_mfma_f32_16x16x32_bf16 v[110:113], v[130:133], v[170:173], 0
	v_mfma_f32_16x16x32_bf16 v[106:109], v[138:141], v[170:173], 0
	s_waitcnt lgkmcnt(3)
	v_mfma_f32_16x16x32_bf16 v[94:97], v[130:133], v[180:183], 0
	v_mfma_f32_16x16x32_bf16 v[90:93], v[138:141], v[180:183], 0
	s_waitcnt lgkmcnt(1)
	v_mfma_f32_16x16x32_bf16 v[78:81], v[130:133], v[188:191], 0
	v_mfma_f32_16x16x32_bf16 v[74:77], v[138:141], v[188:191], 0
	v_mfma_f32_16x16x32_bf16 v[114:117], v[134:137], v[166:169], v[114:117]
	v_mfma_f32_16x16x32_bf16 v[118:121], v[142:145], v[166:169], v[118:121]
	v_mfma_f32_16x16x32_bf16 v[110:113], v[134:137], v[174:177], v[110:113]
	v_mfma_f32_16x16x32_bf16 v[106:109], v[142:145], v[174:177], v[106:109]
	v_mfma_f32_16x16x32_bf16 v[94:97], v[134:137], v[184:187], v[94:97]
	v_mfma_f32_16x16x32_bf16 v[90:93], v[142:145], v[184:187], v[90:93]
	s_waitcnt lgkmcnt(0)
	v_mfma_f32_16x16x32_bf16 v[78:81], v[134:137], v[198:201], v[78:81]
	v_mfma_f32_16x16x32_bf16 v[74:77], v[142:145], v[198:201], v[74:77]
	v_mfma_f32_16x16x32_bf16 v[126:129], v[146:149], v[162:165], 0
	v_mfma_f32_16x16x32_bf16 v[122:125], v[154:157], v[162:165], 0
	v_mfma_f32_16x16x32_bf16 v[102:105], v[146:149], v[170:173], 0
	v_mfma_f32_16x16x32_bf16 v[98:101], v[154:157], v[170:173], 0
	v_mfma_f32_16x16x32_bf16 v[86:89], v[146:149], v[180:183], 0
	v_mfma_f32_16x16x32_bf16 v[82:85], v[154:157], v[180:183], 0
	v_mfma_f32_16x16x32_bf16 v[70:73], v[146:149], v[188:191], 0
	v_mfma_f32_16x16x32_bf16 v[66:69], v[154:157], v[188:191], 0
	v_mfma_f32_16x16x32_bf16 v[126:129], v[150:153], v[166:169], v[126:129]
	v_mfma_f32_16x16x32_bf16 v[122:125], v[158:161], v[166:169], v[122:125]
	v_mfma_f32_16x16x32_bf16 v[102:105], v[150:153], v[174:177], v[102:105]
	v_mfma_f32_16x16x32_bf16 v[98:101], v[158:161], v[174:177], v[98:101]
	v_mfma_f32_16x16x32_bf16 v[86:89], v[150:153], v[184:187], v[86:89]
	v_mfma_f32_16x16x32_bf16 v[82:85], v[158:161], v[184:187], v[82:85]
	v_mfma_f32_16x16x32_bf16 v[70:73], v[150:153], v[198:201], v[70:73]
	v_mfma_f32_16x16x32_bf16 v[66:69], v[158:161], v[198:201], v[66:69]
	s_setprio 0
	s_barrier
	ds_read_b128 v[162:165], v196 offset:16384
	ds_read_b128 v[166:169], v196 offset:17408
	ds_read_b128 v[170:173], v196 offset:18432
	ds_read_b128 v[174:177], v196 offset:19456
	ds_read_b128 v[180:183], v196 offset:20480
	ds_read_b128 v[184:187], v196 offset:21504
	ds_read_b128 v[188:191], v196 offset:22528
	ds_read_b128 v[198:201], v196 offset:23552
	s_add_i32 s48, s47, 0x10000
	s_mov_b32 m0, s48
	s_nop 0
	global_load_lds_dwordx4 v193, s[34:35]
	s_add_i32 s48, s47, 0x12000
	s_mov_b32 m0, s48
	s_nop 0
	global_load_lds_dwordx4 v194, s[34:35]
	s_add_u32 s48, s34, 0x4000
	s_addc_u32 s49, s35, 0
	s_add_i32 s50, s47, 0x14000
	s_mov_b32 m0, s50
	s_nop 0
	global_load_lds_dwordx4 v193, s[48:49]
	s_add_i32 s50, s47, 0x16000
	s_mov_b32 m0, s50
	s_nop 0
	global_load_lds_dwordx4 v194, s[48:49]
	s_waitcnt vmcnt(6)
	s_waitcnt lgkmcnt(0)
	s_barrier
; #define PG8_STAGEA1(bufoff, gbase) do { if constexpr (Sched::GATHER) { PG8_STAGEA(bufoff, gbase, vA2, vA3); } else { PG8_STAGEA(bufoff, (gbase) + hstep, vA0, vA1); } } while (0)
; #define PG8_LDA(dst, b, h) do { if constexpr (F8) { _Pragma("unroll") for (int m = 0; m < 4; ++m) dst##8[m] = PG8_LD32(lds + PG8_SA(b, h) + aoff + m * 2048); } else { \
;         _Pragma("unroll") for (int m = 0; m < 4; ++m) _Pragma("unroll") for (int k = 0; k < 2; ++k) dst[m][k] = *(const LAS bf16x8*)(lds + PG8_SA(b, h) + aoff + m * 2048 + k * 1024); } } while (0)
; #define PG8_LDB(dst, b, h) do { if constexpr (F8) { _Pragma("unroll") for (int n = 0; n < 2; ++n) dst##8[n] = PG8_LD32(lds + PG8_SB(b, h) + boff + n * 2048); } else { \
;         _Pragma("unroll") for (int n = 0; n < 2; ++n) _Pragma("unroll") for (int k = 0; k < 2; ++k) dst[n][k] = *(const LAS bf16x8*)(lds + PG8_SB(b, h) + boff + n * 2048 + k * 1024); } } while (0)
; #define PG8_WAIT_VR() PG8_WAIT_V(8)
; #define PG8_WAIT_VX() do { if (relax) asm volatile("s_waitcnt vmcnt(%0)" :: "n"(8 + Epi::RELAX) : "memory"); else PG8_WAIT_V(8); } while (0)
; #define PG8_WAIT_L(n) asm volatile("s_waitcnt lgkmcnt(" #n ")" ::: "memory")
; #define PG8_BAR __builtin_amdgcn_s_barrier()
; #define PG8_SCHED __builtin_amdgcn_sched_barrier(0)
; template <class Epi, class Sched, bool F8 = false, bool PF = false, bool I8 = false, int PID = -1>
; __device__ __forceinline__ void gemm_phase(LAS unsigned char* lds, LAS unsigned char* xlds, const int RP, const int RPB, const int nt, const Sched& S, const Epi& E, const int stagger_ticks) {
;     ...
;             PG8_WAIT_VX(); PG8_WAIT_L(0); PG8_BAR; PG8_MMA(1, 0, At, B0); PG8_MMA(1, 1, At, B1); PG8_BAR; PG8_SCHED;
;             PG8_LDB(B0, 1, 0); PG8_LDB(B1, 1, 1); PG8_SCHED; PG8_LDA(At, 1, 0); PG8_STAGEA1(PG8_SA(0, 1), a2);
;             PG8_WAIT_VR(); PG8_WAIT_L(0); PG8_BAR; PG8_MMA(0, 0, At, B0); PG8_MMA(0, 1, At, B1); PG8_BAR; PG8_SCHED;
	s_setprio 1
	s_waitcnt lgkmcnt(7)
	v_mfma_f32_16x16x32_bf16 v[50:53], v[130:133], v[162:165], 0
	v_mfma_f32_16x16x32_bf16 v[54:57], v[138:141], v[162:165], 0
	s_waitcnt lgkmcnt(5)
	v_mfma_f32_16x16x32_bf16 v[46:49], v[130:133], v[170:173], 0
	v_mfma_f32_16x16x32_bf16 v[42:45], v[138:141], v[170:173], 0
	s_waitcnt lgkmcnt(3)
	v_mfma_f32_16x16x32_bf16 v[30:33], v[130:133], v[180:183], 0
	v_mfma_f32_16x16x32_bf16 v[26:29], v[138:141], v[180:183], 0
	s_waitcnt lgkmcnt(1)
	v_mfma_f32_16x16x32_bf16 v[14:17], v[130:133], v[188:191], 0
	v_mfma_f32_16x16x32_bf16 v[10:13], v[138:141], v[188:191], 0
	v_mfma_f32_16x16x32_bf16 v[50:53], v[134:137], v[166:169], v[50:53]
	v_mfma_f32_16x16x32_bf16 v[54:57], v[142:145], v[166:169], v[54:57]
	v_mfma_f32_16x16x32_bf16 v[46:49], v[134:137], v[174:177], v[46:49]
	v_mfma_f32_16x16x32_bf16 v[42:45], v[142:145], v[174:177], v[42:45]
	v_mfma_f32_16x16x32_bf16 v[30:33], v[134:137], v[184:187], v[30:33]
	v_mfma_f32_16x16x32_bf16 v[26:29], v[142:145], v[184:187], v[26:29]
	s_waitcnt lgkmcnt(0)
	v_mfma_f32_16x16x32_bf16 v[14:17], v[134:137], v[198:201], v[14:17]
	v_mfma_f32_16x16x32_bf16 v[10:13], v[142:145], v[198:201], v[10:13]
	v_mfma_f32_16x16x32_bf16 v[58:61], v[146:149], v[162:165], 0
	v_mfma_f32_16x16x32_bf16 v[62:65], v[154:157], v[162:165], 0
	v_mfma_f32_16x16x32_bf16 v[38:41], v[146:149], v[170:173], 0
	v_mfma_f32_16x16x32_bf16 v[34:37], v[154:157], v[170:173], 0
	v_mfma_f32_16x16x32_bf16 v[22:25], v[146:149], v[180:183], 0
	v_mfma_f32_16x16x32_bf16 v[18:21], v[154:157], v[180:183], 0
	v_mfma_f32_16x16x32_bf16 v[6:9], v[146:149], v[188:191], 0
	v_mfma_f32_16x16x32_bf16 v[2:5], v[154:157], v[188:191], 0
	v_mfma_f32_16x16x32_bf16 v[58:61], v[150:153], v[166:169], v[58:61]
	v_mfma_f32_16x16x32_bf16 v[62:65], v[158:161], v[166:169], v[62:65]
	v_mfma_f32_16x16x32_bf16 v[38:41], v[150:153], v[174:177], v[38:41]
	v_mfma_f32_16x16x32_bf16 v[34:37], v[158:161], v[174:177], v[34:37]
	v_mfma_f32_16x16x32_bf16 v[22:25], v[150:153], v[184:187], v[22:25]
	v_mfma_f32_16x16x32_bf16 v[18:21], v[158:161], v[184:187], v[18:21]
	v_mfma_f32_16x16x32_bf16 v[6:9], v[150:153], v[198:201], v[6:9]
	v_mfma_f32_16x16x32_bf16 v[2:5], v[158:161], v[198:201], v[2:5]
	s_setprio 0
	s_barrier
	s_add_i32 s48, s47, 0x2000
	s_mov_b32 m0, s47
	s_nop 0
	global_load_lds_dwordx4 v1, s[36:37]
	s_nop 0
	s_mov_b32 m0, s48
	s_nop 0
	global_load_lds_dwordx4 v192, s[36:37]
	v_add_u32_e32 v142, 0x18000, v195
	v_add_u32_e32 v158, 0x1c000, v195
	ds_read_b128 v[130:133], v142
	ds_read_b128 v[134:137], v142 offset:1024
	ds_read_b128 v[138:141], v142 offset:2048
	ds_read_b128 v[142:145], v142 offset:3072
	ds_read_b128 v[146:149], v158
	ds_read_b128 v[150:153], v158 offset:1024
	ds_read_b128 v[154:157], v158 offset:2048
	ds_read_b128 v[158:161], v158 offset:3072
	ds_read_b128 v[162:165], v196 offset:32768
	ds_read_b128 v[166:169], v196 offset:33792
	ds_read_b128 v[170:173], v196 offset:34816
	ds_read_b128 v[174:177], v196 offset:35840
	ds_read_b128 v[180:183], v196 offset:36864
	ds_read_b128 v[184:187], v196 offset:37888
	ds_read_b128 v[188:191], v196 offset:38912
	ds_read_b128 v[198:201], v196 offset:39936
	s_add_u32 s36, s36, 0x40000
	s_addc_u32 s37, s37, 0
	s_add_i32 s48, s47, 0x4000
	s_mov_b32 m0, s48
	s_nop 0
	global_load_lds_dwordx4 v1, s[36:37]
	s_add_i32 s48, s47, 0x6000
	s_mov_b32 m0, s48
	s_nop 0
	global_load_lds_dwordx4 v192, s[36:37]
	s_waitcnt vmcnt(8)
	s_waitcnt lgkmcnt(0)
	s_barrier
	s_setprio 1
	s_waitcnt lgkmcnt(7)
	v_mfma_f32_16x16x32_bf16 v[114:117], v[130:133], v[162:165], v[114:117]
	v_mfma_f32_16x16x32_bf16 v[118:121], v[138:141], v[162:165], v[118:121]
	s_waitcnt lgkmcnt(5)
	v_mfma_f32_16x16x32_bf16 v[110:113], v[130:133], v[170:173], v[110:113]
	v_mfma_f32_16x16x32_bf16 v[106:109], v[138:141], v[170:173], v[106:109]
	s_waitcnt lgkmcnt(3)
	v_mfma_f32_16x16x32_bf16 v[94:97], v[130:133], v[180:183], v[94:97]
	v_mfma_f32_16x16x32_bf16 v[90:93], v[138:141], v[180:183], v[90:93]
	s_waitcnt lgkmcnt(1)
	v_mfma_f32_16x16x32_bf16 v[78:81], v[130:133], v[188:191], v[78:81]
	v_mfma_f32_16x16x32_bf16 v[74:77], v[138:141], v[188:191], v[74:77]
	v_mfma_f32_16x16x32_bf16 v[114:117], v[134:137], v[166:169], v[114:117]
	v_mfma_f32_16x16x32_bf16 v[118:121], v[142:145], v[166:169], v[118:121]
	v_mfma_f32_16x16x32_bf16 v[110:113], v[134:137], v[174:177], v[110:113]
	v_mfma_f32_16x16x32_bf16 v[106:109], v[142:145], v[174:177], v[106:109]
	v_mfma_f32_16x16x32_bf16 v[94:97], v[134:137], v[184:187], v[94:97]
	v_mfma_f32_16x16x32_bf16 v[90:93], v[142:145], v[184:187], v[90:93]
	s_waitcnt lgkmcnt(0)
	v_mfma_f32_16x16x32_bf16 v[78:81], v[134:137], v[198:201], v[78:81]
	v_mfma_f32_16x16x32_bf16 v[74:77], v[142:145], v[198:201], v[74:77]
	v_mfma_f32_16x16x32_bf16 v[126:129], v[146:149], v[162:165], v[126:129]
	v_mfma_f32_16x16x32_bf16 v[122:125], v[154:157], v[162:165], v[122:125]
	v_mfma_f32_16x16x32_bf16 v[102:105], v[146:149], v[170:173], v[102:105]
	v_mfma_f32_16x16x32_bf16 v[98:101], v[154:157], v[170:173], v[98:101]
	v_mfma_f32_16x16x32_bf16 v[86:89], v[146:149], v[180:183], v[86:89]
	v_mfma_f32_16x16x32_bf16 v[82:85], v[154:157], v[180:183], v[82:85]
	v_mfma_f32_16x16x32_bf16 v[70:73], v[146:149], v[188:191], v[70:73]
	v_mfma_f32_16x16x32_bf16 v[66:69], v[154:157], v[188:191], v[66:69]
	v_mfma_f32_16x16x32_bf16 v[126:129], v[150:153], v[166:169], v[126:129]
	v_mfma_f32_16x16x32_bf16 v[122:125], v[158:161], v[166:169], v[122:125]
	v_mfma_f32_16x16x32_bf16 v[102:105], v[150:153], v[174:177], v[102:105]
	v_mfma_f32_16x16x32_bf16 v[98:101], v[158:161], v[174:177], v[98:101]
	v_mfma_f32_16x16x32_bf16 v[86:89], v[150:153], v[184:187], v[86:89]
	v_mfma_f32_16x16x32_bf16 v[82:85], v[158:161], v[184:187], v[82:85]
	v_mfma_f32_16x16x32_bf16 v[70:73], v[150:153], v[198:201], v[70:73]
	v_mfma_f32_16x16x32_bf16 v[66:69], v[158:161], v[198:201], v[66:69]
	s_setprio 0
	s_barrier
; #define PG8_STAGE(bufoff, gbase, voff) do { PG8_GLDS((const char*)(gbase), (voff)[0], ldsb + (bufoff)); PG8_GLDS((const char*)(gbase), (voff)[1], ldsb + (bufoff) + 8192u); } while (0)
; #define PG8_STAGEA(bufoff, gbase, o0, o1) do { PG8_GLDS((const char*)(gbase), (o0), ldsb + (bufoff)); PG8_GLDS((const char*)(gbase), (o1), ldsb + (bufoff) + 8192u); } while (0)
; #define PG8_STAGEA1(bufoff, gbase) do { if constexpr (Sched::GATHER) { PG8_STAGEA(bufoff, gbase, vA2, vA3); } else { PG8_STAGEA(bufoff, (gbase) + hstep, vA0, vA1); } } while (0)
; #define PG8_WAIT_VR() PG8_WAIT_V(8)
; #define PG8_WAIT_VX() do { if (relax) asm volatile("s_waitcnt vmcnt(%0)" :: "n"(8 + Epi::RELAX) : "memory"); else PG8_WAIT_V(8); } while (0)
; #define PG8_WAIT_L(n) asm volatile("s_waitcnt lgkmcnt(" #n ")" ::: "memory")
; template <class Epi, class Sched, bool F8 = false, bool PF = false, bool I8 = false, int PID = -1>
; __device__ __forceinline__ void gemm_phase(LAS unsigned char* lds, LAS unsigned char* xlds, const int RP, const int RPB, const int nt, const Sched& S, const Epi& E, const int stagger_ticks) {
;     ...
;             PG8_LDB(B0, 0, 0); PG8_LDB(B1, 0, 1); PG8_SCHED; PG8_LDA(At, 0, 0); PG8_STAGEA1(PG8_SA(1, 1), a1);
;             if (Sched::GATHER) { if (last) { const u32x4 nv = *nslot; vA0 = nv.x; vA1 = nv.y; vA2 = nv.z; vA3 = nv.w; } }
;             PG8_WAIT_VX(); PG8_WAIT_L(0); PG8_BAR; PG8_MMA(0, 0, At, B0); PG8_MMA(0, 1, At, B1); PG8_BAR; PG8_SCHED;
;             if constexpr (Epi::BIAS_DMA) { if (t == 0 && has_next) E.bias_dma(nxt, xlds + 8192 + ((ui + 1) & 1) * Epi::BIAS_STRIDE, wid, lane); }
;             PG8_LDA(At, 0, 1); PG8_STAGE(PG8_SB(0, 0), b2, voffB); PG8_STAGE(PG8_SB(0, 1), b2 + hstepB, voffB); PG8_STAGEA(PG8_SA(0, 0), a2, vA0, vA1);
;             PG8_WAIT_VX(); PG8_WAIT_L(0); PG8_BAR; PG8_MMA(1, 0, At, B0); PG8_MMA(1, 1, At, B1); PG8_BAR; PG8_SCHED;
;             PG8_LDB(B0, 1, 0); PG8_LDB(B1, 1, 1); PG8_SCHED; PG8_LDA(At, 1, 0); PG8_STAGEA1(PG8_SA(0, 1), a2);
;             PG8_WAIT_VR(); PG8_WAIT_L(0); PG8_BAR; PG8_MMA(0, 0, At, B0); PG8_MMA(0, 1, At, B1); PG8_BAR; PG8_SCHED;
;             PG8_LDA(At, 1, 1); PG8_STAGE(PG8_SB(1, 0), b3, voffB); PG8_STAGE(PG8_SB(1, 1), b3 + hstepB, voffB); PG8_STAGEA(PG8_SA(1, 0), a3, vA0, vA1);
;             PG8_WAIT_VR(); PG8_WAIT_L(0); PG8_BAR; PG8_MMA(1, 0, At, B0); PG8_MMA(1, 1, At, B1); PG8_BAR; PG8_SCHED;
	s_add_u32 s36, s34, 0x80
	ds_read_b128 v[162:165], v196 offset:49152
	ds_read_b128 v[166:169], v196 offset:50176
	ds_read_b128 v[170:173], v196 offset:51200
	ds_read_b128 v[174:177], v196 offset:52224
	ds_read_b128 v[180:183], v196 offset:53248
	ds_read_b128 v[184:187], v196 offset:54272
	ds_read_b128 v[188:191], v196 offset:55296
	ds_read_b128 v[198:201], v196 offset:56320
	s_addc_u32 s37, s35, 0
	s_add_i32 s48, s47, 0x18000
	s_mov_b32 m0, s48
	s_nop 0
	global_load_lds_dwordx4 v193, s[36:37]
	s_add_i32 s48, s47, 0x1a000
	s_mov_b32 m0, s48
	s_nop 0
	global_load_lds_dwordx4 v194, s[36:37]
	s_add_u32 s34, s34, 0x4080
	s_addc_u32 s35, s35, 0
	s_add_i32 s36, s47, 0x1c000
	s_mov_b32 m0, s36
	s_nop 0
	global_load_lds_dwordx4 v193, s[34:35]
	s_add_i32 s36, s47, 0x1e000
	s_mov_b32 m0, s36
	s_nop 0
	global_load_lds_dwordx4 v194, s[34:35]
	s_waitcnt vmcnt(6)
	s_waitcnt lgkmcnt(0)
	s_barrier
	s_setprio 1
	s_waitcnt lgkmcnt(7)
	v_mfma_f32_16x16x32_bf16 v[50:53], v[130:133], v[162:165], v[50:53]
	v_mfma_f32_16x16x32_bf16 v[54:57], v[138:141], v[162:165], v[54:57]
	s_waitcnt lgkmcnt(5)
	v_mfma_f32_16x16x32_bf16 v[46:49], v[130:133], v[170:173], v[46:49]
	v_mfma_f32_16x16x32_bf16 v[42:45], v[138:141], v[170:173], v[42:45]
	s_waitcnt lgkmcnt(3)
	v_mfma_f32_16x16x32_bf16 v[30:33], v[130:133], v[180:183], v[30:33]
	v_mfma_f32_16x16x32_bf16 v[26:29], v[138:141], v[180:183], v[26:29]
	s_waitcnt lgkmcnt(1)
	v_mfma_f32_16x16x32_bf16 v[14:17], v[130:133], v[188:191], v[14:17]
	v_mfma_f32_16x16x32_bf16 v[10:13], v[138:141], v[188:191], v[10:13]
	v_mfma_f32_16x16x32_bf16 v[50:53], v[134:137], v[166:169], v[50:53]
	v_mfma_f32_16x16x32_bf16 v[54:57], v[142:145], v[166:169], v[54:57]
	v_mfma_f32_16x16x32_bf16 v[46:49], v[134:137], v[174:177], v[46:49]
	v_mfma_f32_16x16x32_bf16 v[42:45], v[142:145], v[174:177], v[42:45]
	v_mfma_f32_16x16x32_bf16 v[30:33], v[134:137], v[184:187], v[30:33]
	v_mfma_f32_16x16x32_bf16 v[26:29], v[142:145], v[184:187], v[26:29]
	s_waitcnt lgkmcnt(0)
	v_mfma_f32_16x16x32_bf16 v[14:17], v[134:137], v[198:201], v[14:17]
	v_mfma_f32_16x16x32_bf16 v[10:13], v[142:145], v[198:201], v[10:13]
	v_mfma_f32_16x16x32_bf16 v[58:61], v[146:149], v[162:165], v[58:61]
	v_mfma_f32_16x16x32_bf16 v[62:65], v[154:157], v[162:165], v[62:65]
	v_mfma_f32_16x16x32_bf16 v[38:41], v[146:149], v[170:173], v[38:41]
	v_mfma_f32_16x16x32_bf16 v[34:37], v[154:157], v[170:173], v[34:37]
	v_mfma_f32_16x16x32_bf16 v[22:25], v[146:149], v[180:183], v[22:25]
	v_mfma_f32_16x16x32_bf16 v[18:21], v[154:157], v[180:183], v[18:21]
	v_mfma_f32_16x16x32_bf16 v[6:9], v[146:149], v[188:191], v[6:9]
	v_mfma_f32_16x16x32_bf16 v[2:5], v[154:157], v[188:191], v[2:5]
	v_mfma_f32_16x16x32_bf16 v[58:61], v[150:153], v[166:169], v[58:61]
	v_mfma_f32_16x16x32_bf16 v[62:65], v[158:161], v[166:169], v[62:65]
	v_mfma_f32_16x16x32_bf16 v[38:41], v[150:153], v[174:177], v[38:41]
	v_mfma_f32_16x16x32_bf16 v[34:37], v[158:161], v[174:177], v[34:37]
	v_mfma_f32_16x16x32_bf16 v[22:25], v[150:153], v[184:187], v[22:25]
	v_mfma_f32_16x16x32_bf16 v[18:21], v[158:161], v[184:187], v[18:21]
	v_mfma_f32_16x16x32_bf16 v[6:9], v[150:153], v[198:201], v[6:9]
	v_mfma_f32_16x16x32_bf16 v[2:5], v[158:161], v[198:201], v[2:5]
	s_setprio 0
	s_barrier
	s_add_i32 s46, s46, 2
	s_add_u32 s20, s20, 0x100
	s_addc_u32 s45, s45, 0
	s_add_u32 s0, s0, 0x100
	s_addc_u32 s1, s1, 0
	s_cmp_gt_u32 s46, 13
.LBB0_547:
	s_mov_b32 s47, s5
	s_add_u32 s100, s0, 0xfffc0000
	s_addc_u32 s101, s1, -1
	s_add_i32 s48, s47, 0x8000
	s_mov_b32 m0, s48
	s_nop 0
	global_load_lds_dwordx4 v1, s[100:101]
	s_add_i32 s48, s47, 0xa000
	s_mov_b32 m0, s48
	s_nop 0
	global_load_lds_dwordx4 v192, s[100:101]
	v_add_u32_e32 v142, 0x10000, v195
	v_add_u32_e32 v158, 0x14000, v195
	ds_read_b128 v[130:133], v142
	ds_read_b128 v[134:137], v142 offset:1024
	ds_read_b128 v[138:141], v142 offset:2048
	ds_read_b128 v[142:145], v142 offset:3072
	ds_read_b128 v[146:149], v158
	ds_read_b128 v[150:153], v158 offset:1024
	ds_read_b128 v[154:157], v158 offset:2048
	ds_read_b128 v[158:161], v158 offset:3072
	s_add_u32 s2, s0, 0xfffc0080
	s_addc_u32 s3, s1, -1
	s_cmp_eq_u32 s46, 12
	s_cselect_b32 s36, s8, s2
	s_cselect_b32 s37, s9, s3
	s_cselect_b32 s34, s10, s20
	s_cselect_b32 s35, s11, s45
	s_add_u32 s2, s36, 0x80
	s_addc_u32 s3, s37, 0
	ds_read_b128 v[162:165], v196
	ds_read_b128 v[166:169], v196 offset:1024
	ds_read_b128 v[170:173], v196 offset:2048
	ds_read_b128 v[174:177], v196 offset:3072
	ds_read_b128 v[180:183], v196 offset:4096
	ds_read_b128 v[184:187], v196 offset:5120
	ds_read_b128 v[188:191], v196 offset:6144
	ds_read_b128 v[198:201], v196 offset:7168
	s_add_i32 s48, s47, 0xc000
	s_mov_b32 m0, s48
	s_nop 0
	global_load_lds_dwordx4 v1, s[0:1]
	s_add_i32 s48, s47, 0xe000
	s_mov_b32 m0, s48
	s_nop 0
	global_load_lds_dwordx4 v192, s[0:1]
	s_waitcnt vmcnt(8)
	s_waitcnt lgkmcnt(0)
	s_barrier
; #define PG8_STAGE(bufoff, gbase, voff) do { PG8_GLDS((const char*)(gbase), (voff)[0], ldsb + (bufoff)); PG8_GLDS((const char*)(gbase), (voff)[1], ldsb + (bufoff) + 8192u); } while (0)
; #define PG8_STAGEA(bufoff, gbase, o0, o1) do { PG8_GLDS((const char*)(gbase), (o0), ldsb + (bufoff)); PG8_GLDS((const char*)(gbase), (o1), ldsb + (bufoff) + 8192u); } while (0)
; #define PG8_LDA(dst, b, h) do { if constexpr (F8) { _Pragma("unroll") for (int m = 0; m < 4; ++m) dst##8[m] = PG8_LD32(lds + PG8_SA(b, h) + aoff + m * 2048); } else { \
;         _Pragma("unroll") for (int m = 0; m < 4; ++m) _Pragma("unroll") for (int k = 0; k < 2; ++k) dst[m][k] = *(const LAS bf16x8*)(lds + PG8_SA(b, h) + aoff + m * 2048 + k * 1024); } } while (0)
; #define PG8_WAIT_VX() do { if (relax) asm volatile("s_waitcnt vmcnt(%0)" :: "n"(8 + Epi::RELAX) : "memory"); else PG8_WAIT_V(8); } while (0)
; #define PG8_WAIT_L(n) asm volatile("s_waitcnt lgkmcnt(" #n ")" ::: "memory")
; #define PG8_BAR __builtin_amdgcn_s_barrier()
; #define PG8_SCHED __builtin_amdgcn_sched_barrier(0)
; template <class Epi, class Sched, bool F8 = false, bool PF = false, bool I8 = false, int PID = -1>
; __device__ __forceinline__ void gemm_phase(LAS unsigned char* lds, LAS unsigned char* xlds, const int RP, const int RPB, const int nt, const Sched& S, const Epi& E, const int stagger_ticks) {
;     ...
;             PG8_WAIT_VX(); PG8_WAIT_L(0); PG8_BAR; PG8_MMA(0, 0, At, B0); PG8_MMA(0, 1, At, B1); PG8_BAR; PG8_SCHED;
;             if constexpr (Epi::BIAS_DMA) { if (t == 0 && has_next) E.bias_dma(nxt, xlds + 8192 + ((ui + 1) & 1) * Epi::BIAS_STRIDE, wid, lane); }
;             PG8_LDA(At, 0, 1); PG8_STAGE(PG8_SB(0, 0), b2, voffB); PG8_STAGE(PG8_SB(0, 1), b2 + hstepB, voffB); PG8_STAGEA(PG8_SA(0, 0), a2, vA0, vA1);
;             PG8_WAIT_VX(); PG8_WAIT_L(0); PG8_BAR; PG8_MMA(1, 0, At, B0); PG8_MMA(1, 1, At, B1); PG8_BAR; PG8_SCHED;
	s_setprio 1
	s_waitcnt lgkmcnt(7)
	v_mfma_f32_16x16x32_bf16 v[114:117], v[130:133], v[162:165], v[114:117]
	v_mfma_f32_16x16x32_bf16 v[118:121], v[138:141], v[162:165], v[118:121]
	s_waitcnt lgkmcnt(5)
	v_mfma_f32_16x16x32_bf16 v[110:113], v[130:133], v[170:173], v[110:113]
	v_mfma_f32_16x16x32_bf16 v[106:109], v[138:141], v[170:173], v[106:109]
	s_waitcnt lgkmcnt(3)
	v_mfma_f32_16x16x32_bf16 v[94:97], v[130:133], v[180:183], v[94:97]
	v_mfma_f32_16x16x32_bf16 v[90:93], v[138:141], v[180:183], v[90:93]
	s_waitcnt lgkmcnt(1)
	v_mfma_f32_16x16x32_bf16 v[78:81], v[130:133], v[188:191], v[78:81]
	v_mfma_f32_16x16x32_bf16 v[74:77], v[138:141], v[188:191], v[74:77]
	v_mfma_f32_16x16x32_bf16 v[114:117], v[134:137], v[166:169], v[114:117]
	v_mfma_f32_16x16x32_bf16 v[118:121], v[142:145], v[166:169], v[118:121]
	v_mfma_f32_16x16x32_bf16 v[110:113], v[134:137], v[174:177], v[110:113]
	v_mfma_f32_16x16x32_bf16 v[106:109], v[142:145], v[174:177], v[106:109]
	v_mfma_f32_16x16x32_bf16 v[94:97], v[134:137], v[184:187], v[94:97]
	v_mfma_f32_16x16x32_bf16 v[90:93], v[142:145], v[184:187], v[90:93]
	s_waitcnt lgkmcnt(0)
	v_mfma_f32_16x16x32_bf16 v[78:81], v[134:137], v[198:201], v[78:81]
	v_mfma_f32_16x16x32_bf16 v[74:77], v[142:145], v[198:201], v[74:77]
	v_mfma_f32_16x16x32_bf16 v[126:129], v[146:149], v[162:165], v[126:129]
	v_mfma_f32_16x16x32_bf16 v[122:125], v[154:157], v[162:165], v[122:125]
	v_mfma_f32_16x16x32_bf16 v[102:105], v[146:149], v[170:173], v[102:105]
	v_mfma_f32_16x16x32_bf16 v[98:101], v[154:157], v[170:173], v[98:101]
	v_mfma_f32_16x16x32_bf16 v[86:89], v[146:149], v[180:183], v[86:89]
	v_mfma_f32_16x16x32_bf16 v[82:85], v[154:157], v[180:183], v[82:85]
	v_mfma_f32_16x16x32_bf16 v[70:73], v[146:149], v[188:191], v[70:73]
	v_mfma_f32_16x16x32_bf16 v[66:69], v[154:157], v[188:191], v[66:69]
	v_mfma_f32_16x16x32_bf16 v[126:129], v[150:153], v[166:169], v[126:129]
	v_mfma_f32_16x16x32_bf16 v[122:125], v[158:161], v[166:169], v[122:125]
	v_mfma_f32_16x16x32_bf16 v[102:105], v[150:153], v[174:177], v[102:105]
	v_mfma_f32_16x16x32_bf16 v[98:101], v[158:161], v[174:177], v[98:101]
	v_mfma_f32_16x16x32_bf16 v[86:89], v[150:153], v[184:187], v[86:89]
	v_mfma_f32_16x16x32_bf16 v[82:85], v[158:161], v[184:187], v[82:85]
	v_mfma_f32_16x16x32_bf16 v[70:73], v[150:153], v[198:201], v[70:73]
	v_mfma_f32_16x16x32_bf16 v[66:69], v[158:161], v[198:201], v[66:69]
	s_setprio 0
	s_barrier
	ds_read_b128 v[162:165], v196 offset:16384
	ds_read_b128 v[166:169], v196 offset:17408
	ds_read_b128 v[170:173], v196 offset:18432
	ds_read_b128 v[174:177], v196 offset:19456
	ds_read_b128 v[180:183], v196 offset:20480
	ds_read_b128 v[184:187], v196 offset:21504
	ds_read_b128 v[188:191], v196 offset:22528
	ds_read_b128 v[198:201], v196 offset:23552
	s_add_i32 s48, s47, 0x10000
	s_mov_b32 m0, s48
	s_nop 0
	global_load_lds_dwordx4 v193, s[34:35]
	s_add_i32 s48, s47, 0x12000
	s_mov_b32 m0, s48
	s_nop 0
	global_load_lds_dwordx4 v194, s[34:35]
	s_add_u32 s48, s34, 0x4000
	s_addc_u32 s49, s35, 0
	s_add_i32 s50, s47, 0x14000
	s_mov_b32 m0, s50
	s_nop 0
	global_load_lds_dwordx4 v193, s[48:49]
	s_add_i32 s50, s47, 0x16000
	s_mov_b32 m0, s50
	s_nop 0
	global_load_lds_dwordx4 v194, s[48:49]
	s_waitcnt vmcnt(6)
	s_waitcnt lgkmcnt(0)
	s_barrier
	s_setprio 1
	s_waitcnt lgkmcnt(7)
	v_mfma_f32_16x16x32_bf16 v[50:53], v[130:133], v[162:165], v[50:53]
	v_mfma_f32_16x16x32_bf16 v[54:57], v[138:141], v[162:165], v[54:57]
	s_waitcnt lgkmcnt(5)
	v_mfma_f32_16x16x32_bf16 v[46:49], v[130:133], v[170:173], v[46:49]
	v_mfma_f32_16x16x32_bf16 v[42:45], v[138:141], v[170:173], v[42:45]
	s_waitcnt lgkmcnt(3)
	v_mfma_f32_16x16x32_bf16 v[30:33], v[130:133], v[180:183], v[30:33]
	v_mfma_f32_16x16x32_bf16 v[26:29], v[138:141], v[180:183], v[26:29]
	s_waitcnt lgkmcnt(1)
	v_mfma_f32_16x16x32_bf16 v[14:17], v[130:133], v[188:191], v[14:17]
	v_mfma_f32_16x16x32_bf16 v[10:13], v[138:141], v[188:191], v[10:13]
	v_mfma_f32_16x16x32_bf16 v[50:53], v[134:137], v[166:169], v[50:53]
	v_mfma_f32_16x16x32_bf16 v[54:57], v[142:145], v[166:169], v[54:57]
	v_mfma_f32_16x16x32_bf16 v[46:49], v[134:137], v[174:177], v[46:49]
	v_mfma_f32_16x16x32_bf16 v[42:45], v[142:145], v[174:177], v[42:45]
	v_mfma_f32_16x16x32_bf16 v[30:33], v[134:137], v[184:187], v[30:33]
	v_mfma_f32_16x16x32_bf16 v[26:29], v[142:145], v[184:187], v[26:29]
	s_waitcnt lgkmcnt(0)
	v_mfma_f32_16x16x32_bf16 v[14:17], v[134:137], v[198:201], v[14:17]
	v_mfma_f32_16x16x32_bf16 v[10:13], v[142:145], v[198:201], v[10:13]
	v_mfma_f32_16x16x32_bf16 v[58:61], v[146:149], v[162:165], v[58:61]
	v_mfma_f32_16x16x32_bf16 v[62:65], v[154:157], v[162:165], v[62:65]
	v_mfma_f32_16x16x32_bf16 v[38:41], v[146:149], v[170:173], v[38:41]
	v_mfma_f32_16x16x32_bf16 v[34:37], v[154:157], v[170:173], v[34:37]
	v_mfma_f32_16x16x32_bf16 v[22:25], v[146:149], v[180:183], v[22:25]
	v_mfma_f32_16x16x32_bf16 v[18:21], v[154:157], v[180:183], v[18:21]
	v_mfma_f32_16x16x32_bf16 v[6:9], v[146:149], v[188:191], v[6:9]
	v_mfma_f32_16x16x32_bf16 v[2:5], v[154:157], v[188:191], v[2:5]
	v_mfma_f32_16x16x32_bf16 v[58:61], v[150:153], v[166:169], v[58:61]
	v_mfma_f32_16x16x32_bf16 v[62:65], v[158:161], v[166:169], v[62:65]
	v_mfma_f32_16x16x32_bf16 v[38:41], v[150:153], v[174:177], v[38:41]
	v_mfma_f32_16x16x32_bf16 v[34:37], v[158:161], v[174:177], v[34:37]
	v_mfma_f32_16x16x32_bf16 v[22:25], v[150:153], v[184:187], v[22:25]
	v_mfma_f32_16x16x32_bf16 v[18:21], v[158:161], v[184:187], v[18:21]
	v_mfma_f32_16x16x32_bf16 v[6:9], v[150:153], v[198:201], v[6:9]
	v_mfma_f32_16x16x32_bf16 v[2:5], v[158:161], v[198:201], v[2:5]
	s_setprio 0
	s_barrier
; #define PG8_STAGEA1(bufoff, gbase) do { if constexpr (Sched::GATHER) { PG8_STAGEA(bufoff, gbase, vA2, vA3); } else { PG8_STAGEA(bufoff, (gbase) + hstep, vA0, vA1); } } while (0)
; #define PG8_LDA(dst, b, h) do { if constexpr (F8) { _Pragma("unroll") for (int m = 0; m < 4; ++m) dst##8[m] = PG8_LD32(lds + PG8_SA(b, h) + aoff + m * 2048); } else { \
;         _Pragma("unroll") for (int m = 0; m < 4; ++m) _Pragma("unroll") for (int k = 0; k < 2; ++k) dst[m][k] = *(const LAS bf16x8*)(lds + PG8_SA(b, h) + aoff + m * 2048 + k * 1024); } } while (0)
; #define PG8_LDB(dst, b, h) do { if constexpr (F8) { _Pragma("unroll") for (int n = 0; n < 2; ++n) dst##8[n] = PG8_LD32(lds + PG8_SB(b, h) + boff + n * 2048); } else { \
;         _Pragma("unroll") for (int n = 0; n < 2; ++n) _Pragma("unroll") for (int k = 0; k < 2; ++k) dst[n][k] = *(const LAS bf16x8*)(lds + PG8_SB(b, h) + boff + n * 2048 + k * 1024); } } while (0)
; #define PG8_WAIT_VR() PG8_WAIT_V(8)
; #define PG8_WAIT_L(n) asm volatile("s_waitcnt lgkmcnt(" #n ")" ::: "memory")
; #define PG8_BAR __builtin_amdgcn_s_barrier()
; #define PG8_SCHED __builtin_amdgcn_sched_barrier(0)
; template <class Epi, class Sched, bool F8 = false, bool PF = false, bool I8 = false, int PID = -1>
; __device__ __forceinline__ void gemm_phase(LAS unsigned char* lds, LAS unsigned char* xlds, const int RP, const int RPB, const int nt, const Sched& S, const Epi& E, const int stagger_ticks) {
;     ...
;             PG8_LDB(B0, 1, 0); PG8_LDB(B1, 1, 1); PG8_SCHED; PG8_LDA(At, 1, 0); PG8_STAGEA1(PG8_SA(0, 1), a2);
;             PG8_WAIT_VR(); PG8_WAIT_L(0); PG8_BAR; PG8_MMA(0, 0, At, B0); PG8_MMA(0, 1, At, B1); PG8_BAR; PG8_SCHED;
	s_add_i32 s48, s47, 0x2000
	s_mov_b32 m0, s47
	s_nop 0
	global_load_lds_dwordx4 v1, s[36:37]
	s_nop 0
	s_mov_b32 m0, s48
	s_nop 0
	global_load_lds_dwordx4 v192, s[36:37]
	v_add_u32_e32 v142, 0x18000, v195
	v_add_u32_e32 v158, 0x1c000, v195
	ds_read_b128 v[130:133], v142
	ds_read_b128 v[134:137], v142 offset:1024
	ds_read_b128 v[138:141], v142 offset:2048
	ds_read_b128 v[142:145], v142 offset:3072
	ds_read_b128 v[146:149], v158
	ds_read_b128 v[150:153], v158 offset:1024
	ds_read_b128 v[154:157], v158 offset:2048
	ds_read_b128 v[158:161], v158 offset:3072
	ds_read_b128 v[162:165], v196 offset:32768
	ds_read_b128 v[166:169], v196 offset:33792
	ds_read_b128 v[170:173], v196 offset:34816
	ds_read_b128 v[174:177], v196 offset:35840
	ds_read_b128 v[180:183], v196 offset:36864
	ds_read_b128 v[184:187], v196 offset:37888
	ds_read_b128 v[188:191], v196 offset:38912
	ds_read_b128 v[198:201], v196 offset:39936
	s_add_u32 s36, s36, 0x40000
	s_addc_u32 s37, s37, 0
	s_add_i32 s48, s47, 0x4000
	s_mov_b32 m0, s48
	s_nop 0
	global_load_lds_dwordx4 v1, s[36:37]
	s_add_i32 s48, s47, 0x6000
	s_mov_b32 m0, s48
	s_nop 0
	global_load_lds_dwordx4 v192, s[36:37]
	s_waitcnt vmcnt(8)
	s_waitcnt lgkmcnt(0)
	s_barrier
	s_setprio 1
	s_waitcnt lgkmcnt(7)
	v_mfma_f32_16x16x32_bf16 v[114:117], v[130:133], v[162:165], v[114:117]
	v_mfma_f32_16x16x32_bf16 v[118:121], v[138:141], v[162:165], v[118:121]
	s_waitcnt lgkmcnt(5)
	v_mfma_f32_16x16x32_bf16 v[110:113], v[130:133], v[170:173], v[110:113]
	v_mfma_f32_16x16x32_bf16 v[106:109], v[138:141], v[170:173], v[106:109]
	s_waitcnt lgkmcnt(3)
	v_mfma_f32_16x16x32_bf16 v[94:97], v[130:133], v[180:183], v[94:97]
	v_mfma_f32_16x16x32_bf16 v[90:93], v[138:141], v[180:183], v[90:93]
	s_waitcnt lgkmcnt(1)
	v_mfma_f32_16x16x32_bf16 v[78:81], v[130:133], v[188:191], v[78:81]
	v_mfma_f32_16x16x32_bf16 v[74:77], v[138:141], v[188:191], v[74:77]
	v_mfma_f32_16x16x32_bf16 v[114:117], v[134:137], v[166:169], v[114:117]
	v_mfma_f32_16x16x32_bf16 v[118:121], v[142:145], v[166:169], v[118:121]
	v_mfma_f32_16x16x32_bf16 v[110:113], v[134:137], v[174:177], v[110:113]
	v_mfma_f32_16x16x32_bf16 v[106:109], v[142:145], v[174:177], v[106:109]
	v_mfma_f32_16x16x32_bf16 v[94:97], v[134:137], v[184:187], v[94:97]
	v_mfma_f32_16x16x32_bf16 v[90:93], v[142:145], v[184:187], v[90:93]
	s_waitcnt lgkmcnt(0)
	v_mfma_f32_16x16x32_bf16 v[78:81], v[134:137], v[198:201], v[78:81]
	v_mfma_f32_16x16x32_bf16 v[74:77], v[142:145], v[198:201], v[74:77]
	v_mfma_f32_16x16x32_bf16 v[126:129], v[146:149], v[162:165], v[126:129]
	v_mfma_f32_16x16x32_bf16 v[122:125], v[154:157], v[162:165], v[122:125]
	v_mfma_f32_16x16x32_bf16 v[102:105], v[146:149], v[170:173], v[102:105]
	v_mfma_f32_16x16x32_bf16 v[98:101], v[154:157], v[170:173], v[98:101]
	v_mfma_f32_16x16x32_bf16 v[86:89], v[146:149], v[180:183], v[86:89]
	v_mfma_f32_16x16x32_bf16 v[82:85], v[154:157], v[180:183], v[82:85]
	v_mfma_f32_16x16x32_bf16 v[70:73], v[146:149], v[188:191], v[70:73]
	v_mfma_f32_16x16x32_bf16 v[66:69], v[154:157], v[188:191], v[66:69]
	v_mfma_f32_16x16x32_bf16 v[126:129], v[150:153], v[166:169], v[126:129]
	v_mfma_f32_16x16x32_bf16 v[122:125], v[158:161], v[166:169], v[122:125]
	v_mfma_f32_16x16x32_bf16 v[102:105], v[150:153], v[174:177], v[102:105]
	v_mfma_f32_16x16x32_bf16 v[98:101], v[158:161], v[174:177], v[98:101]
	v_mfma_f32_16x16x32_bf16 v[86:89], v[150:153], v[184:187], v[86:89]
	v_mfma_f32_16x16x32_bf16 v[82:85], v[158:161], v[184:187], v[82:85]
	v_mfma_f32_16x16x32_bf16 v[70:73], v[150:153], v[198:201], v[70:73]
	v_mfma_f32_16x16x32_bf16 v[66:69], v[158:161], v[198:201], v[66:69]
	s_setprio 0
	s_barrier
; #define PG8_STAGE(bufoff, gbase, voff) do { PG8_GLDS((const char*)(gbase), (voff)[0], ldsb + (bufoff)); PG8_GLDS((const char*)(gbase), (voff)[1], ldsb + (bufoff) + 8192u); } while (0)
; #define PG8_STAGEA(bufoff, gbase, o0, o1) do { PG8_GLDS((const char*)(gbase), (o0), ldsb + (bufoff)); PG8_GLDS((const char*)(gbase), (o1), ldsb + (bufoff) + 8192u); } while (0)
; #define PG8_LDA(dst, b, h) do { if constexpr (F8) { _Pragma("unroll") for (int m = 0; m < 4; ++m) dst##8[m] = PG8_LD32(lds + PG8_SA(b, h) + aoff + m * 2048); } else { \
;         _Pragma("unroll") for (int m = 0; m < 4; ++m) _Pragma("unroll") for (int k = 0; k < 2; ++k) dst[m][k] = *(const LAS bf16x8*)(lds + PG8_SA(b, h) + aoff + m * 2048 + k * 1024); } } while (0)
; #define PG8_WAIT_VR() PG8_WAIT_V(8)
; #define PG8_WAIT_L(n) asm volatile("s_waitcnt lgkmcnt(" #n ")" ::: "memory")
; #define PG8_BAR __builtin_amdgcn_s_barrier()
; #define PG8_SCHED __builtin_amdgcn_sched_barrier(0)
; #define PROF_BEGIN(sel) do { if constexpr (PROF && PROF_SEL == (sel)) prof_t0 = (unsigned)__builtin_amdgcn_s_memrealtime(); } while (0)
; #define PROF_END(sel) do { if constexpr (PROF && PROF_SEL == (sel)) prof_acc += (unsigned)__builtin_amdgcn_s_memrealtime() - prof_t0; } while (0)
; template <class Epi, class Sched, bool F8 = false, bool PF = false, bool I8 = false, int PID = -1>
; __device__ __forceinline__ void gemm_phase(LAS unsigned char* lds, LAS unsigned char* xlds, const int RP, const int RPB, const int nt, const Sched& S, const Epi& E, const int stagger_ticks) {
;     ...
;             PG8_LDA(At, 1, 1); PG8_STAGE(PG8_SB(1, 0), b3, voffB); PG8_STAGE(PG8_SB(1, 1), b3 + hstepB, voffB); PG8_STAGEA(PG8_SA(1, 0), a3, vA0, vA1);
;             PG8_WAIT_VR(); PG8_WAIT_L(0); PG8_BAR; PG8_MMA(1, 0, At, B0); PG8_MMA(1, 1, At, B1); PG8_BAR; PG8_SCHED;
;         }
;         PROF_END(1); PROF_BEGIN(3);
;         if (wr == 0) PG8_BAR;
	s_add_u32 s36, s34, 0x80
	ds_read_b128 v[162:165], v196 offset:49152
	ds_read_b128 v[166:169], v196 offset:50176
	ds_read_b128 v[170:173], v196 offset:51200
	ds_read_b128 v[174:177], v196 offset:52224
	ds_read_b128 v[180:183], v196 offset:53248
	ds_read_b128 v[184:187], v196 offset:54272
	ds_read_b128 v[188:191], v196 offset:55296
	ds_read_b128 v[198:201], v196 offset:56320
	s_addc_u32 s37, s35, 0
	s_add_i32 s48, s47, 0x18000
	s_mov_b32 m0, s48
	s_nop 0
	global_load_lds_dwordx4 v193, s[36:37]
	s_add_i32 s48, s47, 0x1a000
	s_mov_b32 m0, s48
	s_nop 0
	global_load_lds_dwordx4 v194, s[36:37]
	s_add_u32 s34, s34, 0x4080
	s_addc_u32 s35, s35, 0
	s_add_i32 s36, s47, 0x1c000
	s_mov_b32 m0, s36
	s_nop 0
	global_load_lds_dwordx4 v193, s[34:35]
	s_add_i32 s36, s47, 0x1e000
	s_mov_b32 m0, s36
	s_nop 0
	global_load_lds_dwordx4 v194, s[34:35]
	s_waitcnt vmcnt(6)
	s_waitcnt lgkmcnt(0)
	s_barrier
	s_setprio 1
	s_waitcnt lgkmcnt(7)
	v_mfma_f32_16x16x32_bf16 v[50:53], v[130:133], v[162:165], v[50:53]
	v_mfma_f32_16x16x32_bf16 v[54:57], v[138:141], v[162:165], v[54:57]
	s_waitcnt lgkmcnt(5)
	v_mfma_f32_16x16x32_bf16 v[46:49], v[130:133], v[170:173], v[46:49]
	v_mfma_f32_16x16x32_bf16 v[42:45], v[138:141], v[170:173], v[42:45]
	s_waitcnt lgkmcnt(3)
	v_mfma_f32_16x16x32_bf16 v[30:33], v[130:133], v[180:183], v[30:33]
	v_mfma_f32_16x16x32_bf16 v[26:29], v[138:141], v[180:183], v[26:29]
	s_waitcnt lgkmcnt(1)
	v_mfma_f32_16x16x32_bf16 v[14:17], v[130:133], v[188:191], v[14:17]
	v_mfma_f32_16x16x32_bf16 v[10:13], v[138:141], v[188:191], v[10:13]
	v_mfma_f32_16x16x32_bf16 v[50:53], v[134:137], v[166:169], v[50:53]
	v_mfma_f32_16x16x32_bf16 v[54:57], v[142:145], v[166:169], v[54:57]
	v_mfma_f32_16x16x32_bf16 v[46:49], v[134:137], v[174:177], v[46:49]
	v_mfma_f32_16x16x32_bf16 v[42:45], v[142:145], v[174:177], v[42:45]
	v_mfma_f32_16x16x32_bf16 v[30:33], v[134:137], v[184:187], v[30:33]
	v_mfma_f32_16x16x32_bf16 v[26:29], v[142:145], v[184:187], v[26:29]
	s_waitcnt lgkmcnt(0)
	v_mfma_f32_16x16x32_bf16 v[14:17], v[134:137], v[198:201], v[14:17]
	v_mfma_f32_16x16x32_bf16 v[10:13], v[142:145], v[198:201], v[10:13]
	v_mfma_f32_16x16x32_bf16 v[58:61], v[146:149], v[162:165], v[58:61]
	v_mfma_f32_16x16x32_bf16 v[62:65], v[154:157], v[162:165], v[62:65]
	v_mfma_f32_16x16x32_bf16 v[38:41], v[146:149], v[170:173], v[38:41]
	v_mfma_f32_16x16x32_bf16 v[34:37], v[154:157], v[170:173], v[34:37]
	v_mfma_f32_16x16x32_bf16 v[22:25], v[146:149], v[180:183], v[22:25]
	v_mfma_f32_16x16x32_bf16 v[18:21], v[154:157], v[180:183], v[18:21]
	v_mfma_f32_16x16x32_bf16 v[6:9], v[146:149], v[188:191], v[6:9]
	v_mfma_f32_16x16x32_bf16 v[2:5], v[154:157], v[188:191], v[2:5]
	v_mfma_f32_16x16x32_bf16 v[58:61], v[150:153], v[166:169], v[58:61]
	v_mfma_f32_16x16x32_bf16 v[62:65], v[158:161], v[166:169], v[62:65]
	v_mfma_f32_16x16x32_bf16 v[38:41], v[150:153], v[174:177], v[38:41]
	v_mfma_f32_16x16x32_bf16 v[34:37], v[158:161], v[174:177], v[34:37]
	v_mfma_f32_16x16x32_bf16 v[22:25], v[150:153], v[184:187], v[22:25]
	v_mfma_f32_16x16x32_bf16 v[18:21], v[158:161], v[184:187], v[18:21]
	v_mfma_f32_16x16x32_bf16 v[6:9], v[150:153], v[198:201], v[6:9]
	v_mfma_f32_16x16x32_bf16 v[2:5], v[158:161], v[198:201], v[2:5]
	s_setprio 0
	s_barrier
	s_add_i32 s46, s46, 2
	s_add_u32 s20, s20, 0x100
	s_addc_u32 s45, s45, 0
	s_add_u32 s0, s0, 0x100
	s_addc_u32 s1, s1, 0
	s_cmp_gt_u32 s46, 13
	s_cbranch_scc0 .LBB0_547
	s_and_b64 vcc, exec, s[30:31]
	s_cbranch_vccz .LBB0_550
	s_barrier

; #define PG8_STAGE(bufoff, gbase, voff) do { PG8_GLDS((const char*)(gbase), (voff)[0], ldsb + (bufoff)); PG8_GLDS((const char*)(gbase), (voff)[1], ldsb + (bufoff) + 8192u); } while (0)
; #define PG8_STAGEA(bufoff, gbase, o0, o1) do { PG8_GLDS((const char*)(gbase), (o0), ldsb + (bufoff)); PG8_GLDS((const char*)(gbase), (o1), ldsb + (bufoff) + 8192u); } while (0)
; #define PG8_STAGEA1(bufoff, gbase) do { if constexpr (Sched::GATHER) { PG8_STAGEA(bufoff, gbase, vA2, vA3); } else { PG8_STAGEA(bufoff, (gbase) + hstep, vA0, vA1); } } while (0)
; #define PG8_LDA(dst, b, h) do { if constexpr (F8) { _Pragma("unroll") for (int m = 0; m < 4; ++m) dst##8[m] = PG8_LD32(lds + PG8_SA(b, h) + aoff + m * 2048); } else { \
;         _Pragma("unroll") for (int m = 0; m < 4; ++m) _Pragma("unroll") for (int k = 0; k < 2; ++k) dst[m][k] = *(const LAS bf16x8*)(lds + PG8_SA(b, h) + aoff + m * 2048 + k * 1024); } } while (0)
; #define PG8_WAIT_VR() PG8_WAIT_V(8)
; #define PG8_WAIT_VX() do { if (relax) asm volatile("s_waitcnt vmcnt(%0)" :: "n"(8 + Epi::RELAX) : "memory"); else PG8_WAIT_V(8); } while (0)
; template <class Epi, class Sched, bool F8 = false, bool PF = false, bool I8 = false, int PID = -1>
; __device__ __forceinline__ void gemm_phase(LAS unsigned char* lds, LAS unsigned char* xlds, const int RP, const int RPB, const int nt, const Sched& S, const Epi& E, const int stagger_ticks) {
;     ...
;             PG8_LDB(B0, 0, 0); PG8_LDB(B1, 0, 1); PG8_SCHED; PG8_LDA(At, 0, 0); PG8_STAGEA1(PG8_SA(1, 1), a1);
;             if (Sched::GATHER) { if (last) { const u32x4 nv = *nslot; vA0 = nv.x; vA1 = nv.y; vA2 = nv.z; vA3 = nv.w; } }
;             PG8_WAIT_VX(); PG8_WAIT_L(0); PG8_BAR; PG8_MMA(0, 0, At, B0); PG8_MMA(0, 1, At, B1); PG8_BAR; PG8_SCHED;
;             if constexpr (Epi::BIAS_DMA) { if (t == 0 && has_next) E.bias_dma(nxt, xlds + 8192 + ((ui + 1) & 1) * Epi::BIAS_STRIDE, wid, lane); }
;             PG8_LDA(At, 0, 1); PG8_STAGE(PG8_SB(0, 0), b2, voffB); PG8_STAGE(PG8_SB(0, 1), b2 + hstepB, voffB); PG8_STAGEA(PG8_SA(0, 0), a2, vA0, vA1);
;             PG8_WAIT_VX(); PG8_WAIT_L(0); PG8_BAR; PG8_MMA(1, 0, At, B0); PG8_MMA(1, 1, At, B1); PG8_BAR; PG8_SCHED;
;             PG8_LDB(B0, 1, 0); PG8_LDB(B1, 1, 1); PG8_SCHED; PG8_LDA(At, 1, 0); PG8_STAGEA1(PG8_SA(0, 1), a2);
;             PG8_WAIT_VR(); PG8_WAIT_L(0); PG8_BAR; PG8_MMA(0, 0, At, B0); PG8_MMA(0, 1, At, B1); PG8_BAR; PG8_SCHED;
.LBB0_640:
	s_mov_b64 s[24:25], s[10:11]
	s_add_u32 s42, s24, 0x100
	s_mov_b64 s[4:5], s[8:9]
	s_addc_u32 s43, s25, 0
	s_mov_b64 s[8:9], s[0:1]
	s_add_u32 s0, s4, 0x20080
	s_mov_b64 s[10:11], s[2:3]
	s_mov_b32 s15, s26
	s_mov_b32 s41, s6
	s_mov_b32 s6, s14
	s_mov_b32 s26, s7
	s_addc_u32 s1, s5, 0
	s_mov_b32 s44, -2
	s_mov_b32 s45, s29
	s_add_u32 s100, s0, 0xfffe0000
	s_addc_u32 s101, s1, -1
	s_add_i32 s46, s45, 0x8000
	s_mov_b32 m0, s46
	s_nop 0
	global_load_lds_dwordx4 v1, s[100:101]
	s_add_i32 s46, s45, 0xa000
	s_mov_b32 m0, s46
	s_nop 0
	global_load_lds_dwordx4 v194, s[100:101]
	v_add_u32_e32 v131, 0x10000, v197
	ds_read_b128 v[132:135], v131
	ds_read_b128 v[136:139], v131 offset:1024
	ds_read_b128 v[140:143], v131 offset:2048
	ds_read_b128 v[144:147], v131 offset:3072
	v_add_u32_e32 v131, 0x14000, v197
	ds_read_b128 v[148:151], v131
	ds_read_b128 v[152:155], v131 offset:1024
	ds_read_b128 v[156:159], v131 offset:2048
	ds_read_b128 v[160:163], v131 offset:3072
	s_add_u32 s2, s0, 0xfffe0080
	s_addc_u32 s3, s1, -1
	s_cmp_eq_u32 s44, 4
	s_cselect_b32 s24, s8, s2
	s_cselect_b32 s25, s9, s3
	s_cselect_b32 s4, s10, s42
	s_cselect_b32 s5, s11, s43
	s_add_u32 s2, s24, 0x80
	s_addc_u32 s3, s25, 0
	ds_read_b128 v[164:167], v198
	ds_read_b128 v[168:171], v198 offset:1024
	ds_read_b128 v[172:175], v198 offset:2048
	ds_read_b128 v[176:179], v198 offset:3072
	ds_read_b128 v[180:183], v198 offset:4096
	ds_read_b128 v[184:187], v198 offset:5120
	ds_read_b128 v[202:205], v198 offset:6144
	ds_read_b128 v[206:209], v198 offset:7168
	s_add_i32 s46, s45, 0xc000
	s_mov_b32 m0, s46
	s_nop 0
	global_load_lds_dwordx4 v1, s[0:1]
	s_add_i32 s46, s45, 0xe000
	s_mov_b32 m0, s46
	s_nop 0
	global_load_lds_dwordx4 v194, s[0:1]
	s_waitcnt vmcnt(8)
	s_waitcnt lgkmcnt(0)
	s_barrier
	s_setprio 1
	s_waitcnt lgkmcnt(6)
	v_mfma_f32_16x16x128_f8f6f4 v[114:117], v[132:139], v[164:171], 0
	v_mfma_f32_16x16x128_f8f6f4 v[118:121], v[140:147], v[164:171], 0
	s_waitcnt lgkmcnt(4)
	v_mfma_f32_16x16x128_f8f6f4 v[102:105], v[132:139], v[172:179], 0
	v_mfma_f32_16x16x128_f8f6f4 v[98:101], v[140:147], v[172:179], 0
	s_waitcnt lgkmcnt(2)
	v_mfma_f32_16x16x128_f8f6f4 v[188:191], v[132:139], v[180:187], 0
	v_mfma_f32_16x16x128_f8f6f4 v[210:213], v[140:147], v[180:187], 0
	s_waitcnt lgkmcnt(0)
	v_mfma_f32_16x16x128_f8f6f4 v[214:217], v[132:139], v[202:209], 0
	v_mfma_f32_16x16x128_f8f6f4 v[218:221], v[140:147], v[202:209], 0
	v_mfma_f32_16x16x128_f8f6f4 v[122:125], v[148:155], v[164:171], 0
	v_mfma_f32_16x16x128_f8f6f4 v[126:129], v[156:163], v[164:171], 0
	v_mfma_f32_16x16x128_f8f6f4 v[110:113], v[148:155], v[172:179], 0
	v_mfma_f32_16x16x128_f8f6f4 v[106:109], v[156:163], v[172:179], 0
	v_mfma_f32_16x16x128_f8f6f4 v[164:167], v[148:155], v[180:187], 0
	v_mfma_f32_16x16x128_f8f6f4 v[168:171], v[156:163], v[180:187], 0
	v_mfma_f32_16x16x128_f8f6f4 v[172:175], v[148:155], v[202:209], 0
	v_mfma_f32_16x16x128_f8f6f4 v[176:179], v[156:163], v[202:209], 0
	s_setprio 0
	s_barrier
	ds_read_b128 v[66:69], v198 offset:16384
	ds_read_b128 v[70:73], v198 offset:17408
	s_nop 2
	ds_read_b128 v[74:77], v198 offset:18432
	ds_read_b128 v[78:81], v198 offset:19456
	ds_read_b128 v[82:85], v198 offset:20480
	ds_read_b128 v[86:89], v198 offset:21504
	ds_read_b128 v[90:93], v198 offset:22528
	ds_read_b128 v[94:97], v198 offset:23552
	s_add_i32 s46, s45, 0x10000
	s_mov_b32 m0, s46
	s_nop 0
	global_load_lds_dwordx4 v195, s[4:5]
	s_add_i32 s46, s45, 0x12000
	s_mov_b32 m0, s46
	s_nop 0
	global_load_lds_dwordx4 v196, s[4:5]
	s_add_u32 s46, s4, 0x2000
	s_addc_u32 s47, s5, 0
	s_add_i32 s48, s45, 0x14000
	s_mov_b32 m0, s48
	s_nop 0
	global_load_lds_dwordx4 v195, s[46:47]
	s_add_i32 s48, s45, 0x16000
	s_mov_b32 m0, s48
	s_nop 0
	global_load_lds_dwordx4 v196, s[46:47]
	s_waitcnt vmcnt(6)
	s_waitcnt lgkmcnt(0)
	s_barrier
	s_setprio 1
	s_waitcnt lgkmcnt(6)
	v_mfma_f32_16x16x128_f8f6f4 v[54:57], v[132:139], v[66:73], 0
	v_mfma_f32_16x16x128_f8f6f4 v[50:53], v[140:147], v[66:73], 0
	s_waitcnt lgkmcnt(4)
	v_mfma_f32_16x16x128_f8f6f4 v[180:183], v[132:139], v[74:81], 0
	v_mfma_f32_16x16x128_f8f6f4 v[184:187], v[140:147], v[74:81], 0
	s_waitcnt lgkmcnt(2)
	v_mfma_f32_16x16x128_f8f6f4 v[202:205], v[132:139], v[82:89], 0
	v_mfma_f32_16x16x128_f8f6f4 v[206:209], v[140:147], v[82:89], 0
	s_waitcnt lgkmcnt(0)
	v_mfma_f32_16x16x128_f8f6f4 v[222:225], v[132:139], v[90:97], 0
	v_mfma_f32_16x16x128_f8f6f4 v[226:229], v[140:147], v[90:97], 0
	v_mfma_f32_16x16x128_f8f6f4 v[62:65], v[148:155], v[66:73], 0
	v_mfma_f32_16x16x128_f8f6f4 v[58:61], v[156:163], v[66:73], 0
	v_mfma_f32_16x16x128_f8f6f4 v[230:233], v[148:155], v[74:81], 0
	v_mfma_f32_16x16x128_f8f6f4 v[234:237], v[156:163], v[74:81], 0
	v_mfma_f32_16x16x128_f8f6f4 v[238:241], v[148:155], v[82:89], 0
	v_mfma_f32_16x16x128_f8f6f4 v[242:245], v[156:163], v[82:89], 0
	v_mfma_f32_16x16x128_f8f6f4 v[246:249], v[148:155], v[90:97], 0
	v_mfma_f32_16x16x128_f8f6f4 v[250:253], v[156:163], v[90:97], 0
	s_setprio 0
	s_barrier
	s_add_i32 s46, s45, 0x2000
	s_mov_b32 m0, s45
	s_nop 0
	global_load_lds_dwordx4 v1, s[24:25]
	s_nop 0
	s_mov_b32 m0, s46
	s_nop 0
	global_load_lds_dwordx4 v194, s[24:25]
	s_nop 3
	v_add_u32_e32 v14, 0x18000, v197
	v_add_u32_e32 v18, 0x1c000, v197
	ds_read_b128 v[2:5], v14
	ds_read_b128 v[6:9], v14 offset:1024
	ds_read_b128 v[10:13], v14 offset:2048
	ds_read_b128 v[14:17], v14 offset:3072
	ds_read_b128 v[132:135], v18
	ds_read_b128 v[136:139], v18 offset:1024
	ds_read_b128 v[140:143], v18 offset:2048
	ds_read_b128 v[144:147], v18 offset:3072
	ds_read_b128 v[18:21], v198 offset:32768
	ds_read_b128 v[22:25], v198 offset:33792
	ds_read_b128 v[26:29], v198 offset:34816
	ds_read_b128 v[30:33], v198 offset:35840
	ds_read_b128 v[34:37], v198 offset:36864
	ds_read_b128 v[38:41], v198 offset:37888
	ds_read_b128 v[42:45], v198 offset:38912
	ds_read_b128 v[46:49], v198 offset:39936
	s_add_u32 s24, s24, 0x20000
	s_addc_u32 s25, s25, 0
	s_add_i32 s46, s45, 0x4000
	s_mov_b32 m0, s46
	s_nop 0
	global_load_lds_dwordx4 v1, s[24:25]
	s_add_i32 s46, s45, 0x6000
	s_mov_b32 m0, s46
	s_nop 0
	global_load_lds_dwordx4 v194, s[24:25]
	s_waitcnt vmcnt(8)
	s_waitcnt lgkmcnt(0)
	s_barrier
; #define PG8_STAGE(bufoff, gbase, voff) do { PG8_GLDS((const char*)(gbase), (voff)[0], ldsb + (bufoff)); PG8_GLDS((const char*)(gbase), (voff)[1], ldsb + (bufoff) + 8192u); } while (0)
; #define PG8_STAGEA(bufoff, gbase, o0, o1) do { PG8_GLDS((const char*)(gbase), (o0), ldsb + (bufoff)); PG8_GLDS((const char*)(gbase), (o1), ldsb + (bufoff) + 8192u); } while (0)
; #define PG8_STAGEA1(bufoff, gbase) do { if constexpr (Sched::GATHER) { PG8_STAGEA(bufoff, gbase, vA2, vA3); } else { PG8_STAGEA(bufoff, (gbase) + hstep, vA0, vA1); } } while (0)
; #define PG8_WAIT_VR() PG8_WAIT_V(8)
; #define PG8_WAIT_VX() do { if (relax) asm volatile("s_waitcnt vmcnt(%0)" :: "n"(8 + Epi::RELAX) : "memory"); else PG8_WAIT_V(8); } while (0)
; #define PG8_WAIT_L(n) asm volatile("s_waitcnt lgkmcnt(" #n ")" ::: "memory")
; template <class Epi, class Sched, bool F8 = false, bool PF = false, bool I8 = false, int PID = -1>
; __device__ __forceinline__ void gemm_phase(LAS unsigned char* lds, LAS unsigned char* xlds, const int RP, const int RPB, const int nt, const Sched& S, const Epi& E, const int stagger_ticks) {
;     ...
;             PG8_LDB(B0, 0, 0); PG8_LDB(B1, 0, 1); PG8_SCHED; PG8_LDA(At, 0, 0); PG8_STAGEA1(PG8_SA(1, 1), a1);
;             if (Sched::GATHER) { if (last) { const u32x4 nv = *nslot; vA0 = nv.x; vA1 = nv.y; vA2 = nv.z; vA3 = nv.w; } }
;             PG8_WAIT_VX(); PG8_WAIT_L(0); PG8_BAR; PG8_MMA(0, 0, At, B0); PG8_MMA(0, 1, At, B1); PG8_BAR; PG8_SCHED;
;             if constexpr (Epi::BIAS_DMA) { if (t == 0 && has_next) E.bias_dma(nxt, xlds + 8192 + ((ui + 1) & 1) * Epi::BIAS_STRIDE, wid, lane); }
;             PG8_LDA(At, 0, 1); PG8_STAGE(PG8_SB(0, 0), b2, voffB); PG8_STAGE(PG8_SB(0, 1), b2 + hstepB, voffB); PG8_STAGEA(PG8_SA(0, 0), a2, vA0, vA1);
;             PG8_WAIT_VX(); PG8_WAIT_L(0); PG8_BAR; PG8_MMA(1, 0, At, B0); PG8_MMA(1, 1, At, B1); PG8_BAR; PG8_SCHED;
;             PG8_LDB(B0, 1, 0); PG8_LDB(B1, 1, 1); PG8_SCHED; PG8_LDA(At, 1, 0); PG8_STAGEA1(PG8_SA(0, 1), a2);
;             PG8_WAIT_VR(); PG8_WAIT_L(0); PG8_BAR; PG8_MMA(0, 0, At, B0); PG8_MMA(0, 1, At, B1); PG8_BAR; PG8_SCHED;
;             PG8_LDA(At, 1, 1); PG8_STAGE(PG8_SB(1, 0), b3, voffB); PG8_STAGE(PG8_SB(1, 1), b3 + hstepB, voffB); PG8_STAGEA(PG8_SA(1, 0), a3, vA0, vA1);
;             PG8_WAIT_VR(); PG8_WAIT_L(0); PG8_BAR; PG8_MMA(1, 0, At, B0); PG8_MMA(1, 1, At, B1); PG8_BAR; PG8_SCHED;
	s_setprio 1
	s_waitcnt lgkmcnt(6)
	v_mfma_f32_16x16x128_f8f6f4 v[114:117], v[2:9], v[18:25], v[114:117]
	v_mfma_f32_16x16x128_f8f6f4 v[118:121], v[10:17], v[18:25], v[118:121]
	s_waitcnt lgkmcnt(4)
	v_mfma_f32_16x16x128_f8f6f4 v[102:105], v[2:9], v[26:33], v[102:105]
	v_mfma_f32_16x16x128_f8f6f4 v[98:101], v[10:17], v[26:33], v[98:101]
	s_waitcnt lgkmcnt(2)
	v_mfma_f32_16x16x128_f8f6f4 v[86:89], v[2:9], v[34:41], v[188:191]
	v_mfma_f32_16x16x128_f8f6f4 v[82:85], v[10:17], v[34:41], v[210:213]
	s_waitcnt lgkmcnt(0)
	v_mfma_f32_16x16x128_f8f6f4 v[70:73], v[2:9], v[42:49], v[214:217]
	v_mfma_f32_16x16x128_f8f6f4 v[66:69], v[10:17], v[42:49], v[218:221]
	v_mfma_f32_16x16x128_f8f6f4 v[122:125], v[132:139], v[18:25], v[122:125]
	v_mfma_f32_16x16x128_f8f6f4 v[126:129], v[140:147], v[18:25], v[126:129]
	v_mfma_f32_16x16x128_f8f6f4 v[110:113], v[132:139], v[26:33], v[110:113]
	v_mfma_f32_16x16x128_f8f6f4 v[106:109], v[140:147], v[26:33], v[106:109]
	v_mfma_f32_16x16x128_f8f6f4 v[94:97], v[132:139], v[34:41], v[164:167]
	v_mfma_f32_16x16x128_f8f6f4 v[90:93], v[140:147], v[34:41], v[168:171]
	v_mfma_f32_16x16x128_f8f6f4 v[78:81], v[132:139], v[42:49], v[172:175]
	v_mfma_f32_16x16x128_f8f6f4 v[74:77], v[140:147], v[42:49], v[176:179]
	s_setprio 0
	s_barrier
	s_add_u32 s24, s4, 0x80
	ds_read_b128 v[26:29], v198 offset:49152
	ds_read_b128 v[30:33], v198 offset:50176
	ds_read_b128 v[148:151], v198 offset:51200
	ds_read_b128 v[152:155], v198 offset:52224
	ds_read_b128 v[156:159], v198 offset:53248
	ds_read_b128 v[160:163], v198 offset:54272
	ds_read_b128 v[164:167], v198 offset:55296
	ds_read_b128 v[168:171], v198 offset:56320
	s_addc_u32 s25, s5, 0
	s_add_i32 s46, s45, 0x18000
	s_mov_b32 m0, s46
	s_nop 0
	global_load_lds_dwordx4 v195, s[24:25]
	s_add_i32 s46, s45, 0x1a000
	s_mov_b32 m0, s46
	s_nop 0
	global_load_lds_dwordx4 v196, s[24:25]
	s_add_u32 s4, s4, 0x2080
	s_addc_u32 s5, s5, 0
	s_add_i32 s24, s45, 0x1c000
	s_mov_b32 m0, s24
	s_nop 0
	global_load_lds_dwordx4 v195, s[4:5]
	s_add_i32 s24, s45, 0x1e000
	s_mov_b32 m0, s24
	s_nop 0
	global_load_lds_dwordx4 v196, s[4:5]
	s_waitcnt vmcnt(6)
	s_waitcnt lgkmcnt(0)
	s_barrier
	s_setprio 1
	s_waitcnt lgkmcnt(6)
	v_mfma_f32_16x16x128_f8f6f4 v[54:57], v[2:9], v[26:33], v[54:57]
	v_mfma_f32_16x16x128_f8f6f4 v[50:53], v[10:17], v[26:33], v[50:53]
	s_waitcnt lgkmcnt(4)
	v_mfma_f32_16x16x128_f8f6f4 v[38:41], v[2:9], v[148:155], v[180:183]
	v_mfma_f32_16x16x128_f8f6f4 v[34:37], v[10:17], v[148:155], v[184:187]
	s_waitcnt lgkmcnt(2)
	v_mfma_f32_16x16x128_f8f6f4 v[22:25], v[2:9], v[156:163], v[202:205]
	v_mfma_f32_16x16x128_f8f6f4 v[18:21], v[10:17], v[156:163], v[206:209]
	s_waitcnt lgkmcnt(0)
	v_mfma_f32_16x16x128_f8f6f4 v[6:9], v[2:9], v[164:171], v[222:225]
	v_mfma_f32_16x16x128_f8f6f4 v[2:5], v[10:17], v[164:171], v[226:229]
	v_mfma_f32_16x16x128_f8f6f4 v[62:65], v[132:139], v[26:33], v[62:65]
	v_mfma_f32_16x16x128_f8f6f4 v[58:61], v[140:147], v[26:33], v[58:61]
	v_mfma_f32_16x16x128_f8f6f4 v[46:49], v[132:139], v[148:155], v[230:233]
	v_mfma_f32_16x16x128_f8f6f4 v[42:45], v[140:147], v[148:155], v[234:237]
	v_mfma_f32_16x16x128_f8f6f4 v[30:33], v[132:139], v[156:163], v[238:241]
	v_mfma_f32_16x16x128_f8f6f4 v[26:29], v[140:147], v[156:163], v[242:245]
	v_mfma_f32_16x16x128_f8f6f4 v[14:17], v[132:139], v[164:171], v[246:249]
	v_mfma_f32_16x16x128_f8f6f4 v[10:13], v[140:147], v[164:171], v[250:253]
	s_setprio 0
	s_barrier
	s_add_i32 s44, s44, 2
	s_add_u32 s42, s42, 0x100
	s_addc_u32 s43, s43, 0
	s_add_u32 s0, s0, 0x100
	s_addc_u32 s1, s1, 0
	s_cmp_gt_u32 s44, 5
.LBB0_641:
	s_mov_b32 s45, s29
	s_add_u32 s100, s0, 0xfffe0000
	s_addc_u32 s101, s1, -1
	s_add_i32 s46, s45, 0x8000
	s_mov_b32 m0, s46
	s_nop 0
	global_load_lds_dwordx4 v1, s[100:101]
	s_add_i32 s46, s45, 0xa000
	s_mov_b32 m0, s46
	s_nop 0
	global_load_lds_dwordx4 v194, s[100:101]
	v_add_u32_e32 v131, 0x10000, v197
	ds_read_b128 v[132:135], v131
	ds_read_b128 v[136:139], v131 offset:1024
	ds_read_b128 v[140:143], v131 offset:2048
	ds_read_b128 v[144:147], v131 offset:3072
	v_add_u32_e32 v131, 0x14000, v197
	ds_read_b128 v[148:151], v131
	ds_read_b128 v[152:155], v131 offset:1024
	ds_read_b128 v[156:159], v131 offset:2048
	ds_read_b128 v[160:163], v131 offset:3072
	s_add_u32 s2, s0, 0xfffe0080
	s_addc_u32 s3, s1, -1
	s_cmp_eq_u32 s44, 4
	s_cselect_b32 s24, s8, s2
	s_cselect_b32 s25, s9, s3
	s_cselect_b32 s4, s10, s42
	s_cselect_b32 s5, s11, s43
	s_add_u32 s2, s24, 0x80
	s_addc_u32 s3, s25, 0
	ds_read_b128 v[164:167], v198
	ds_read_b128 v[168:171], v198 offset:1024
	ds_read_b128 v[172:175], v198 offset:2048
	ds_read_b128 v[176:179], v198 offset:3072
	ds_read_b128 v[180:183], v198 offset:4096
	ds_read_b128 v[184:187], v198 offset:5120
	ds_read_b128 v[202:205], v198 offset:6144
	ds_read_b128 v[206:209], v198 offset:7168
	s_add_i32 s46, s45, 0xc000
	s_mov_b32 m0, s46
	s_nop 0
	global_load_lds_dwordx4 v1, s[0:1]
	s_add_i32 s46, s45, 0xe000
	s_mov_b32 m0, s46
	s_nop 0
	global_load_lds_dwordx4 v194, s[0:1]
	s_waitcnt vmcnt(8)
	s_waitcnt lgkmcnt(0)
	s_barrier
; #define PG8_STAGE(bufoff, gbase, voff) do { PG8_GLDS((const char*)(gbase), (voff)[0], ldsb + (bufoff)); PG8_GLDS((const char*)(gbase), (voff)[1], ldsb + (bufoff) + 8192u); } while (0)
; #define PG8_STAGEA(bufoff, gbase, o0, o1) do { PG8_GLDS((const char*)(gbase), (o0), ldsb + (bufoff)); PG8_GLDS((const char*)(gbase), (o1), ldsb + (bufoff) + 8192u); } while (0)
; #define PG8_STAGEA1(bufoff, gbase) do { if constexpr (Sched::GATHER) { PG8_STAGEA(bufoff, gbase, vA2, vA3); } else { PG8_STAGEA(bufoff, (gbase) + hstep, vA0, vA1); } } while (0)
; #define PG8_LDA(dst, b, h) do { if constexpr (F8) { _Pragma("unroll") for (int m = 0; m < 4; ++m) dst##8[m] = PG8_LD32(lds + PG8_SA(b, h) + aoff + m * 2048); } else { \
;         _Pragma("unroll") for (int m = 0; m < 4; ++m) _Pragma("unroll") for (int k = 0; k < 2; ++k) dst[m][k] = *(const LAS bf16x8*)(lds + PG8_SA(b, h) + aoff + m * 2048 + k * 1024); } } while (0)
; #define PG8_LDB(dst, b, h) do { if constexpr (F8) { _Pragma("unroll") for (int n = 0; n < 2; ++n) dst##8[n] = PG8_LD32(lds + PG8_SB(b, h) + boff + n * 2048); } else { \
;         _Pragma("unroll") for (int n = 0; n < 2; ++n) _Pragma("unroll") for (int k = 0; k < 2; ++k) dst[n][k] = *(const LAS bf16x8*)(lds + PG8_SB(b, h) + boff + n * 2048 + k * 1024); } } while (0)
; #define PG8_WAIT_VR() PG8_WAIT_V(8)
; template <class Epi, class Sched, bool F8 = false, bool PF = false, bool I8 = false, int PID = -1>
; __device__ __forceinline__ void gemm_phase(LAS unsigned char* lds, LAS unsigned char* xlds, const int RP, const int RPB, const int nt, const Sched& S, const Epi& E, const int stagger_ticks) {
;     ...
;             PG8_WAIT_VX(); PG8_WAIT_L(0); PG8_BAR; PG8_MMA(0, 0, At, B0); PG8_MMA(0, 1, At, B1); PG8_BAR; PG8_SCHED;
;             if constexpr (Epi::BIAS_DMA) { if (t == 0 && has_next) E.bias_dma(nxt, xlds + 8192 + ((ui + 1) & 1) * Epi::BIAS_STRIDE, wid, lane); }
;             PG8_LDA(At, 0, 1); PG8_STAGE(PG8_SB(0, 0), b2, voffB); PG8_STAGE(PG8_SB(0, 1), b2 + hstepB, voffB); PG8_STAGEA(PG8_SA(0, 0), a2, vA0, vA1);
;             PG8_WAIT_VX(); PG8_WAIT_L(0); PG8_BAR; PG8_MMA(1, 0, At, B0); PG8_MMA(1, 1, At, B1); PG8_BAR; PG8_SCHED;
;             PG8_LDB(B0, 1, 0); PG8_LDB(B1, 1, 1); PG8_SCHED; PG8_LDA(At, 1, 0); PG8_STAGEA1(PG8_SA(0, 1), a2);
;             PG8_WAIT_VR(); PG8_WAIT_L(0); PG8_BAR; PG8_MMA(0, 0, At, B0); PG8_MMA(0, 1, At, B1); PG8_BAR; PG8_SCHED;
	s_setprio 1
	s_waitcnt lgkmcnt(6)
	v_mfma_f32_16x16x128_f8f6f4 v[114:117], v[132:139], v[164:171], v[114:117]
	v_mfma_f32_16x16x128_f8f6f4 v[118:121], v[140:147], v[164:171], v[118:121]
	s_waitcnt lgkmcnt(4)
	v_mfma_f32_16x16x128_f8f6f4 v[102:105], v[132:139], v[172:179], v[102:105]
	v_mfma_f32_16x16x128_f8f6f4 v[98:101], v[140:147], v[172:179], v[98:101]
	s_waitcnt lgkmcnt(2)
	v_mfma_f32_16x16x128_f8f6f4 v[188:191], v[132:139], v[180:187], v[86:89]
	v_mfma_f32_16x16x128_f8f6f4 v[210:213], v[140:147], v[180:187], v[82:85]
	s_waitcnt lgkmcnt(0)
	v_mfma_f32_16x16x128_f8f6f4 v[214:217], v[132:139], v[202:209], v[70:73]
	v_mfma_f32_16x16x128_f8f6f4 v[218:221], v[140:147], v[202:209], v[66:69]
	v_mfma_f32_16x16x128_f8f6f4 v[122:125], v[148:155], v[164:171], v[122:125]
	v_mfma_f32_16x16x128_f8f6f4 v[126:129], v[156:163], v[164:171], v[126:129]
	v_mfma_f32_16x16x128_f8f6f4 v[110:113], v[148:155], v[172:179], v[110:113]
	v_mfma_f32_16x16x128_f8f6f4 v[106:109], v[156:163], v[172:179], v[106:109]
	v_mfma_f32_16x16x128_f8f6f4 v[164:167], v[148:155], v[180:187], v[94:97]
	v_mfma_f32_16x16x128_f8f6f4 v[168:171], v[156:163], v[180:187], v[90:93]
	v_mfma_f32_16x16x128_f8f6f4 v[172:175], v[148:155], v[202:209], v[78:81]
	v_mfma_f32_16x16x128_f8f6f4 v[176:179], v[156:163], v[202:209], v[74:77]
	s_setprio 0
	s_barrier
	ds_read_b128 v[66:69], v198 offset:16384
	ds_read_b128 v[70:73], v198 offset:17408
	s_nop 2
	ds_read_b128 v[74:77], v198 offset:18432
	ds_read_b128 v[78:81], v198 offset:19456
	ds_read_b128 v[82:85], v198 offset:20480
	ds_read_b128 v[86:89], v198 offset:21504
	ds_read_b128 v[90:93], v198 offset:22528
	ds_read_b128 v[94:97], v198 offset:23552
	s_add_i32 s46, s45, 0x10000
	s_mov_b32 m0, s46
	s_nop 0
	global_load_lds_dwordx4 v195, s[4:5]
	s_add_i32 s46, s45, 0x12000
	s_mov_b32 m0, s46
	s_nop 0
	global_load_lds_dwordx4 v196, s[4:5]
	s_add_u32 s46, s4, 0x2000
	s_addc_u32 s47, s5, 0
	s_add_i32 s48, s45, 0x14000
	s_mov_b32 m0, s48
	s_nop 0
	global_load_lds_dwordx4 v195, s[46:47]
	s_add_i32 s48, s45, 0x16000
	s_mov_b32 m0, s48
	s_nop 0
	global_load_lds_dwordx4 v196, s[46:47]
	s_waitcnt vmcnt(6)
	s_waitcnt lgkmcnt(0)
	s_barrier
	s_setprio 1
	s_waitcnt lgkmcnt(6)
	v_mfma_f32_16x16x128_f8f6f4 v[54:57], v[132:139], v[66:73], v[54:57]
	v_mfma_f32_16x16x128_f8f6f4 v[50:53], v[140:147], v[66:73], v[50:53]
	s_waitcnt lgkmcnt(4)
	v_mfma_f32_16x16x128_f8f6f4 v[180:183], v[132:139], v[74:81], v[38:41]
	v_mfma_f32_16x16x128_f8f6f4 v[184:187], v[140:147], v[74:81], v[34:37]
	s_waitcnt lgkmcnt(2)
	v_mfma_f32_16x16x128_f8f6f4 v[202:205], v[132:139], v[82:89], v[22:25]
	v_mfma_f32_16x16x128_f8f6f4 v[206:209], v[140:147], v[82:89], v[18:21]
	s_waitcnt lgkmcnt(0)
	v_mfma_f32_16x16x128_f8f6f4 v[222:225], v[132:139], v[90:97], v[6:9]
	v_mfma_f32_16x16x128_f8f6f4 v[226:229], v[140:147], v[90:97], v[2:5]
	v_mfma_f32_16x16x128_f8f6f4 v[62:65], v[148:155], v[66:73], v[62:65]
	v_mfma_f32_16x16x128_f8f6f4 v[58:61], v[156:163], v[66:73], v[58:61]
	v_mfma_f32_16x16x128_f8f6f4 v[230:233], v[148:155], v[74:81], v[46:49]
	v_mfma_f32_16x16x128_f8f6f4 v[234:237], v[156:163], v[74:81], v[42:45]
	v_mfma_f32_16x16x128_f8f6f4 v[238:241], v[148:155], v[82:89], v[30:33]
	v_mfma_f32_16x16x128_f8f6f4 v[242:245], v[156:163], v[82:89], v[26:29]
	v_mfma_f32_16x16x128_f8f6f4 v[246:249], v[148:155], v[90:97], v[14:17]
	v_mfma_f32_16x16x128_f8f6f4 v[250:253], v[156:163], v[90:97], v[10:13]
	s_setprio 0
	s_barrier
	s_add_i32 s46, s45, 0x2000
	s_mov_b32 m0, s45
	s_nop 0
	global_load_lds_dwordx4 v1, s[24:25]
	s_nop 0
	s_mov_b32 m0, s46
	s_nop 0
	global_load_lds_dwordx4 v194, s[24:25]
	s_nop 3
	v_add_u32_e32 v14, 0x18000, v197
	v_add_u32_e32 v18, 0x1c000, v197
	ds_read_b128 v[2:5], v14
	ds_read_b128 v[6:9], v14 offset:1024
	ds_read_b128 v[10:13], v14 offset:2048
	ds_read_b128 v[14:17], v14 offset:3072
	ds_read_b128 v[132:135], v18
	ds_read_b128 v[136:139], v18 offset:1024
	ds_read_b128 v[140:143], v18 offset:2048
	ds_read_b128 v[144:147], v18 offset:3072
	ds_read_b128 v[18:21], v198 offset:32768
	ds_read_b128 v[22:25], v198 offset:33792
	ds_read_b128 v[26:29], v198 offset:34816
	ds_read_b128 v[30:33], v198 offset:35840
	ds_read_b128 v[34:37], v198 offset:36864
	ds_read_b128 v[38:41], v198 offset:37888
	ds_read_b128 v[42:45], v198 offset:38912
	ds_read_b128 v[46:49], v198 offset:39936
	s_add_u32 s24, s24, 0x20000
	s_addc_u32 s25, s25, 0
	s_add_i32 s46, s45, 0x4000
	s_mov_b32 m0, s46
	s_nop 0
	global_load_lds_dwordx4 v1, s[24:25]
	s_add_i32 s46, s45, 0x6000
	s_mov_b32 m0, s46
	s_nop 0
	global_load_lds_dwordx4 v194, s[24:25]
	s_waitcnt vmcnt(8)
	s_waitcnt lgkmcnt(0)
	s_barrier
; #define PG8_STAGE(bufoff, gbase, voff) do { PG8_GLDS((const char*)(gbase), (voff)[0], ldsb + (bufoff)); PG8_GLDS((const char*)(gbase), (voff)[1], ldsb + (bufoff) + 8192u); } while (0)
; #define PG8_STAGEA(bufoff, gbase, o0, o1) do { PG8_GLDS((const char*)(gbase), (o0), ldsb + (bufoff)); PG8_GLDS((const char*)(gbase), (o1), ldsb + (bufoff) + 8192u); } while (0)
; #define PG8_LDA(dst, b, h) do { if constexpr (F8) { _Pragma("unroll") for (int m = 0; m < 4; ++m) dst##8[m] = PG8_LD32(lds + PG8_SA(b, h) + aoff + m * 2048); } else { \
;         _Pragma("unroll") for (int m = 0; m < 4; ++m) _Pragma("unroll") for (int k = 0; k < 2; ++k) dst[m][k] = *(const LAS bf16x8*)(lds + PG8_SA(b, h) + aoff + m * 2048 + k * 1024); } } while (0)
; #define PG8_WAIT_VR() PG8_WAIT_V(8)
; #define PG8_WAIT_L(n) asm volatile("s_waitcnt lgkmcnt(" #n ")" ::: "memory")
; #define PG8_BAR __builtin_amdgcn_s_barrier()
; #define PG8_SCHED __builtin_amdgcn_sched_barrier(0)
; #define PROF_BEGIN(sel) do { if constexpr (PROF && PROF_SEL == (sel)) prof_t0 = (unsigned)__builtin_amdgcn_s_memrealtime(); } while (0)
; #define PROF_END(sel) do { if constexpr (PROF && PROF_SEL == (sel)) prof_acc += (unsigned)__builtin_amdgcn_s_memrealtime() - prof_t0; } while (0)
; template <class Epi, class Sched, bool F8 = false, bool PF = false, bool I8 = false, int PID = -1>
; __device__ __forceinline__ void gemm_phase(LAS unsigned char* lds, LAS unsigned char* xlds, const int RP, const int RPB, const int nt, const Sched& S, const Epi& E, const int stagger_ticks) {
;     ...
;             PG8_WAIT_VR(); PG8_WAIT_L(0); PG8_BAR; PG8_MMA(0, 0, At, B0); PG8_MMA(0, 1, At, B1); PG8_BAR; PG8_SCHED;
;             PG8_LDA(At, 1, 1); PG8_STAGE(PG8_SB(1, 0), b3, voffB); PG8_STAGE(PG8_SB(1, 1), b3 + hstepB, voffB); PG8_STAGEA(PG8_SA(1, 0), a3, vA0, vA1);
;             PG8_WAIT_VR(); PG8_WAIT_L(0); PG8_BAR; PG8_MMA(1, 0, At, B0); PG8_MMA(1, 1, At, B1); PG8_BAR; PG8_SCHED;
;         }
;         PROF_END(1); PROF_BEGIN(3);
;         if (wr == 0) PG8_BAR;
	s_setprio 1
	s_waitcnt lgkmcnt(6)
	v_mfma_f32_16x16x128_f8f6f4 v[114:117], v[2:9], v[18:25], v[114:117]
	v_mfma_f32_16x16x128_f8f6f4 v[118:121], v[10:17], v[18:25], v[118:121]
	s_waitcnt lgkmcnt(4)
	v_mfma_f32_16x16x128_f8f6f4 v[102:105], v[2:9], v[26:33], v[102:105]
	v_mfma_f32_16x16x128_f8f6f4 v[98:101], v[10:17], v[26:33], v[98:101]
	s_waitcnt lgkmcnt(2)
	v_mfma_f32_16x16x128_f8f6f4 v[86:89], v[2:9], v[34:41], v[188:191]
	v_mfma_f32_16x16x128_f8f6f4 v[82:85], v[10:17], v[34:41], v[210:213]
	s_waitcnt lgkmcnt(0)
	v_mfma_f32_16x16x128_f8f6f4 v[70:73], v[2:9], v[42:49], v[214:217]
	v_mfma_f32_16x16x128_f8f6f4 v[66:69], v[10:17], v[42:49], v[218:221]
	v_mfma_f32_16x16x128_f8f6f4 v[122:125], v[132:139], v[18:25], v[122:125]
	v_mfma_f32_16x16x128_f8f6f4 v[126:129], v[140:147], v[18:25], v[126:129]
	v_mfma_f32_16x16x128_f8f6f4 v[110:113], v[132:139], v[26:33], v[110:113]
	v_mfma_f32_16x16x128_f8f6f4 v[106:109], v[140:147], v[26:33], v[106:109]
	v_mfma_f32_16x16x128_f8f6f4 v[94:97], v[132:139], v[34:41], v[164:167]
	v_mfma_f32_16x16x128_f8f6f4 v[90:93], v[140:147], v[34:41], v[168:171]
	v_mfma_f32_16x16x128_f8f6f4 v[78:81], v[132:139], v[42:49], v[172:175]
	v_mfma_f32_16x16x128_f8f6f4 v[74:77], v[140:147], v[42:49], v[176:179]
	s_setprio 0
	s_barrier
	s_add_u32 s24, s4, 0x80
	ds_read_b128 v[26:29], v198 offset:49152
	ds_read_b128 v[30:33], v198 offset:50176
	ds_read_b128 v[148:151], v198 offset:51200
	ds_read_b128 v[152:155], v198 offset:52224
	ds_read_b128 v[156:159], v198 offset:53248
	ds_read_b128 v[160:163], v198 offset:54272
	ds_read_b128 v[164:167], v198 offset:55296
	ds_read_b128 v[168:171], v198 offset:56320
	s_addc_u32 s25, s5, 0
	s_add_i32 s46, s45, 0x18000
	s_mov_b32 m0, s46
	s_nop 0
	global_load_lds_dwordx4 v195, s[24:25]
	s_add_i32 s46, s45, 0x1a000
	s_mov_b32 m0, s46
	s_nop 0
	global_load_lds_dwordx4 v196, s[24:25]
	s_add_u32 s4, s4, 0x2080
	s_addc_u32 s5, s5, 0
	s_add_i32 s24, s45, 0x1c000
	s_mov_b32 m0, s24
	s_nop 0
	global_load_lds_dwordx4 v195, s[4:5]
	s_add_i32 s24, s45, 0x1e000
	s_mov_b32 m0, s24
	s_nop 0
	global_load_lds_dwordx4 v196, s[4:5]
	s_waitcnt vmcnt(6)
	s_waitcnt lgkmcnt(0)
	s_barrier
	s_setprio 1
	s_waitcnt lgkmcnt(6)
	v_mfma_f32_16x16x128_f8f6f4 v[54:57], v[2:9], v[26:33], v[54:57]
	v_mfma_f32_16x16x128_f8f6f4 v[50:53], v[10:17], v[26:33], v[50:53]
	s_waitcnt lgkmcnt(4)
	v_mfma_f32_16x16x128_f8f6f4 v[38:41], v[2:9], v[148:155], v[180:183]
	v_mfma_f32_16x16x128_f8f6f4 v[34:37], v[10:17], v[148:155], v[184:187]
	s_waitcnt lgkmcnt(2)
	v_mfma_f32_16x16x128_f8f6f4 v[22:25], v[2:9], v[156:163], v[202:205]
	v_mfma_f32_16x16x128_f8f6f4 v[18:21], v[10:17], v[156:163], v[206:209]
	s_waitcnt lgkmcnt(0)
	v_mfma_f32_16x16x128_f8f6f4 v[6:9], v[2:9], v[164:171], v[222:225]
	v_mfma_f32_16x16x128_f8f6f4 v[2:5], v[10:17], v[164:171], v[226:229]
	v_mfma_f32_16x16x128_f8f6f4 v[62:65], v[132:139], v[26:33], v[62:65]
	v_mfma_f32_16x16x128_f8f6f4 v[58:61], v[140:147], v[26:33], v[58:61]
	v_mfma_f32_16x16x128_f8f6f4 v[46:49], v[132:139], v[148:155], v[230:233]
	v_mfma_f32_16x16x128_f8f6f4 v[42:45], v[140:147], v[148:155], v[234:237]
	v_mfma_f32_16x16x128_f8f6f4 v[30:33], v[132:139], v[156:163], v[238:241]
	v_mfma_f32_16x16x128_f8f6f4 v[26:29], v[140:147], v[156:163], v[242:245]
	v_mfma_f32_16x16x128_f8f6f4 v[14:17], v[132:139], v[164:171], v[246:249]
	v_mfma_f32_16x16x128_f8f6f4 v[10:13], v[140:147], v[164:171], v[250:253]
	s_setprio 0
	s_barrier
	s_add_i32 s44, s44, 2
	s_add_u32 s42, s42, 0x100
	s_addc_u32 s43, s43, 0
	s_add_u32 s0, s0, 0x100
	s_addc_u32 s1, s1, 0
	s_cmp_gt_u32 s44, 5
	s_cbranch_scc0 .LBB0_641
	s_and_b64 vcc, exec, s[22:23]
	s_cbranch_vccz .LBB0_644
	s_barrier

; #define PG8_STAGE(bufoff, gbase, voff) do { PG8_GLDS((const char*)(gbase), (voff)[0], ldsb + (bufoff)); PG8_GLDS((const char*)(gbase), (voff)[1], ldsb + (bufoff) + 8192u); } while (0)
; #define PG8_STAGEA(bufoff, gbase, o0, o1) do { PG8_GLDS((const char*)(gbase), (o0), ldsb + (bufoff)); PG8_GLDS((const char*)(gbase), (o1), ldsb + (bufoff) + 8192u); } while (0)
; #define PG8_STAGEA1(bufoff, gbase) do { if constexpr (Sched::GATHER) { PG8_STAGEA(bufoff, gbase, vA2, vA3); } else { PG8_STAGEA(bufoff, (gbase) + hstep, vA0, vA1); } } while (0)
; #define PG8_LDA(dst, b, h) do { if constexpr (F8) { _Pragma("unroll") for (int m = 0; m < 4; ++m) dst##8[m] = PG8_LD32(lds + PG8_SA(b, h) + aoff + m * 2048); } else { \
;         _Pragma("unroll") for (int m = 0; m < 4; ++m) _Pragma("unroll") for (int k = 0; k < 2; ++k) dst[m][k] = *(const LAS bf16x8*)(lds + PG8_SA(b, h) + aoff + m * 2048 + k * 1024); } } while (0)
; #define PG8_WAIT_VR() PG8_WAIT_V(8)
; #define PG8_WAIT_VX() do { if (relax) asm volatile("s_waitcnt vmcnt(%0)" :: "n"(8 + Epi::RELAX) : "memory"); else PG8_WAIT_V(8); } while (0)
; template <class Epi, class Sched, bool F8 = false, bool PF = false, bool I8 = false, int PID = -1>
; __device__ __forceinline__ void gemm_phase(LAS unsigned char* lds, LAS unsigned char* xlds, const int RP, const int RPB, const int nt, const Sched& S, const Epi& E, const int stagger_ticks) {
;     ...
;             PG8_LDB(B0, 0, 0); PG8_LDB(B1, 0, 1); PG8_SCHED; PG8_LDA(At, 0, 0); PG8_STAGEA1(PG8_SA(1, 1), a1);
;             if (Sched::GATHER) { if (last) { const u32x4 nv = *nslot; vA0 = nv.x; vA1 = nv.y; vA2 = nv.z; vA3 = nv.w; } }
;             PG8_WAIT_VX(); PG8_WAIT_L(0); PG8_BAR; PG8_MMA(0, 0, At, B0); PG8_MMA(0, 1, At, B1); PG8_BAR; PG8_SCHED;
;             if constexpr (Epi::BIAS_DMA) { if (t == 0 && has_next) E.bias_dma(nxt, xlds + 8192 + ((ui + 1) & 1) * Epi::BIAS_STRIDE, wid, lane); }
;             PG8_LDA(At, 0, 1); PG8_STAGE(PG8_SB(0, 0), b2, voffB); PG8_STAGE(PG8_SB(0, 1), b2 + hstepB, voffB); PG8_STAGEA(PG8_SA(0, 0), a2, vA0, vA1);
;             PG8_WAIT_VX(); PG8_WAIT_L(0); PG8_BAR; PG8_MMA(1, 0, At, B0); PG8_MMA(1, 1, At, B1); PG8_BAR; PG8_SCHED;
;             PG8_LDB(B0, 1, 0); PG8_LDB(B1, 1, 1); PG8_SCHED; PG8_LDA(At, 1, 0); PG8_STAGEA1(PG8_SA(0, 1), a2);
;             PG8_WAIT_VR(); PG8_WAIT_L(0); PG8_BAR; PG8_MMA(0, 0, At, B0); PG8_MMA(0, 1, At, B1); PG8_BAR; PG8_SCHED;
.LBB0_752:
	s_mov_b64 s[30:31], s[8:9]
	s_add_u32 s43, s30, 0x100
	s_mov_b64 s[28:29], s[6:7]
	s_addc_u32 s44, s31, 0
	s_mov_b64 s[6:7], s[0:1]
	s_add_u32 s0, s28, 0x20080
	s_mov_b64 s[8:9], s[2:3]
	s_mov_b32 s13, s27
	s_mov_b32 s14, s4
	s_mov_b32 s4, s12
	s_mov_b32 s27, s5
	s_addc_u32 s1, s29, 0
	s_mov_b32 s45, -2
	s_mov_b32 s46, s38
	s_add_u32 s100, s0, 0xfffe0000
	s_addc_u32 s101, s1, -1
	s_add_i32 s47, s46, 0x8000
	s_mov_b32 m0, s47
	s_nop 0
	global_load_lds_dwordx4 v1, s[100:101]
	s_add_i32 s47, s46, 0xa000
	s_mov_b32 m0, s47
	s_nop 0
	global_load_lds_dwordx4 v174, s[100:101]
	v_add_u32_e32 v142, 0x10000, v177
	v_add_u32_e32 v155, 0x14000, v177
	ds_read_b128 v[130:133], v142
	ds_read_b128 v[134:137], v142 offset:1024
	ds_read_b128 v[138:141], v142 offset:2048
	ds_read_b128 v[142:145], v142 offset:3072
	ds_read_b128 v[146:149], v155
	ds_read_b128 v[150:153], v155 offset:1024
	ds_read_b128 v[156:159], v155 offset:2048
	ds_read_b128 v[160:163], v155 offset:3072
	s_add_u32 s2, s0, 0xfffe0080
	s_addc_u32 s3, s1, -1
	s_cmp_eq_u32 s45, 4
	s_cselect_b32 s30, s6, s2
	s_cselect_b32 s31, s7, s3
	s_cselect_b32 s28, s8, s43
	s_cselect_b32 s29, s9, s44
	s_add_u32 s2, s30, 0x80
	s_addc_u32 s3, s31, 0
	ds_read_b128 v[164:167], v178
	ds_read_b128 v[168:171], v178 offset:1024
	ds_read_b128 v[180:183], v178 offset:2048
	ds_read_b128 v[184:187], v178 offset:3072
	ds_read_b128 v[188:191], v178 offset:4096
	ds_read_b128 v[192:195], v178 offset:5120
	ds_read_b128 v[196:199], v178 offset:6144
	ds_read_b128 v[200:203], v178 offset:7168
	s_add_i32 s47, s46, 0xc000
	s_mov_b32 m0, s47
	s_nop 0
	global_load_lds_dwordx4 v1, s[0:1]
	s_add_i32 s47, s46, 0xe000
	s_mov_b32 m0, s47
	s_nop 0
	global_load_lds_dwordx4 v174, s[0:1]
	s_waitcnt vmcnt(8)
	s_waitcnt lgkmcnt(0)
	s_barrier
	s_setprio 1
	s_waitcnt lgkmcnt(6)
	v_mfma_f32_16x16x128_f8f6f4 v[114:117], v[130:137], v[164:171], 0
	v_mfma_f32_16x16x128_f8f6f4 v[118:121], v[138:145], v[164:171], 0
	s_waitcnt lgkmcnt(4)
	v_mfma_f32_16x16x128_f8f6f4 v[110:113], v[130:137], v[180:187], 0
	v_mfma_f32_16x16x128_f8f6f4 v[106:109], v[138:145], v[180:187], 0
	s_waitcnt lgkmcnt(2)
	v_mfma_f32_16x16x128_f8f6f4 v[204:207], v[130:137], v[188:195], 0
	v_mfma_f32_16x16x128_f8f6f4 v[208:211], v[138:145], v[188:195], 0
	s_waitcnt lgkmcnt(0)
	v_mfma_f32_16x16x128_f8f6f4 v[212:215], v[130:137], v[196:203], 0
	v_mfma_f32_16x16x128_f8f6f4 v[216:219], v[138:145], v[196:203], 0
	v_mfma_f32_16x16x128_f8f6f4 v[122:125], v[146:153], v[164:171], 0
	v_mfma_f32_16x16x128_f8f6f4 v[126:129], v[156:163], v[164:171], 0
	v_mfma_f32_16x16x128_f8f6f4 v[102:105], v[146:153], v[180:187], 0
	v_mfma_f32_16x16x128_f8f6f4 v[98:101], v[156:163], v[180:187], 0
	v_mfma_f32_16x16x128_f8f6f4 v[164:167], v[146:153], v[188:195], 0
	v_mfma_f32_16x16x128_f8f6f4 v[168:171], v[156:163], v[188:195], 0
	v_mfma_f32_16x16x128_f8f6f4 v[180:183], v[146:153], v[196:203], 0
	v_mfma_f32_16x16x128_f8f6f4 v[184:187], v[156:163], v[196:203], 0
	s_setprio 0
	s_barrier
	s_nop 4
	ds_read_b128 v[66:69], v178 offset:16384
	ds_read_b128 v[70:73], v178 offset:17408
	ds_read_b128 v[74:77], v178 offset:18432
	ds_read_b128 v[78:81], v178 offset:19456
	ds_read_b128 v[82:85], v178 offset:20480
	ds_read_b128 v[86:89], v178 offset:21504
	ds_read_b128 v[90:93], v178 offset:22528
	ds_read_b128 v[94:97], v178 offset:23552
	s_add_i32 s47, s46, 0x10000
	s_mov_b32 m0, s47
	s_nop 0
	global_load_lds_dwordx4 v175, s[28:29]
	s_add_i32 s47, s46, 0x12000
	s_mov_b32 m0, s47
	s_nop 0
	global_load_lds_dwordx4 v176, s[28:29]
	s_add_u32 s48, s28, 0x2000
	s_addc_u32 s49, s29, 0
	s_add_i32 s47, s46, 0x14000
	s_mov_b32 m0, s47
	s_nop 0
	global_load_lds_dwordx4 v175, s[48:49]
	s_add_i32 s47, s46, 0x16000
	s_mov_b32 m0, s47
	s_nop 0
	global_load_lds_dwordx4 v176, s[48:49]
	s_waitcnt vmcnt(6)
	s_waitcnt lgkmcnt(0)
	s_barrier
	s_setprio 1
	s_waitcnt lgkmcnt(6)
	v_mfma_f32_16x16x128_f8f6f4 v[62:65], v[130:137], v[66:73], 0
	v_mfma_f32_16x16x128_f8f6f4 v[58:61], v[138:145], v[66:73], 0
	s_waitcnt lgkmcnt(4)
	v_mfma_f32_16x16x128_f8f6f4 v[188:191], v[130:137], v[74:81], 0
	v_mfma_f32_16x16x128_f8f6f4 v[192:195], v[138:145], v[74:81], 0
	s_waitcnt lgkmcnt(2)
	v_mfma_f32_16x16x128_f8f6f4 v[196:199], v[130:137], v[82:89], 0
	v_mfma_f32_16x16x128_f8f6f4 v[200:203], v[138:145], v[82:89], 0
	s_waitcnt lgkmcnt(0)
	v_mfma_f32_16x16x128_f8f6f4 v[220:223], v[130:137], v[90:97], 0
	v_mfma_f32_16x16x128_f8f6f4 v[224:227], v[138:145], v[90:97], 0
	v_mfma_f32_16x16x128_f8f6f4 v[54:57], v[146:153], v[66:73], 0
	v_mfma_f32_16x16x128_f8f6f4 v[50:53], v[156:163], v[66:73], 0
	v_mfma_f32_16x16x128_f8f6f4 v[228:231], v[146:153], v[74:81], 0
	v_mfma_f32_16x16x128_f8f6f4 v[232:235], v[156:163], v[74:81], 0
	v_mfma_f32_16x16x128_f8f6f4 v[236:239], v[146:153], v[82:89], 0
	v_mfma_f32_16x16x128_f8f6f4 v[240:243], v[156:163], v[82:89], 0
	v_mfma_f32_16x16x128_f8f6f4 v[244:247], v[146:153], v[90:97], 0
	v_mfma_f32_16x16x128_f8f6f4 v[248:251], v[156:163], v[90:97], 0
	s_setprio 0
	s_barrier
	s_add_i32 s47, s46, 0x2000
	s_mov_b32 m0, s46
	s_nop 0
	global_load_lds_dwordx4 v1, s[30:31]
	s_nop 0
	s_mov_b32 m0, s47
	s_nop 0
	global_load_lds_dwordx4 v174, s[30:31]
	v_add_u32_e32 v10, 0x18000, v177
	s_nop 3
	ds_read_b128 v[2:5], v10
	ds_read_b128 v[6:9], v10 offset:1024
	ds_read_b128 v[18:21], v10 offset:2048
	ds_read_b128 v[22:25], v10 offset:3072
	v_add_u32_e32 v10, 0x1c000, v177
	ds_read_b128 v[130:133], v10
	ds_read_b128 v[134:137], v10 offset:1024
	ds_read_b128 v[138:141], v10 offset:2048
	ds_read_b128 v[142:145], v10 offset:3072
	ds_read_b128 v[10:13], v178 offset:32768
	ds_read_b128 v[14:17], v178 offset:33792
	ds_read_b128 v[26:29], v178 offset:34816
	ds_read_b128 v[30:33], v178 offset:35840
	ds_read_b128 v[34:37], v178 offset:36864
	ds_read_b128 v[38:41], v178 offset:37888
	ds_read_b128 v[42:45], v178 offset:38912
	ds_read_b128 v[46:49], v178 offset:39936
	s_add_u32 s30, s30, 0x20000
	s_addc_u32 s31, s31, 0
	s_add_i32 s47, s46, 0x4000
	s_mov_b32 m0, s47
	s_nop 0
	global_load_lds_dwordx4 v1, s[30:31]
	s_add_i32 s47, s46, 0x6000
	s_mov_b32 m0, s47
	s_nop 0
	global_load_lds_dwordx4 v174, s[30:31]
	s_waitcnt vmcnt(8)
	s_waitcnt lgkmcnt(0)
	s_barrier
; #define PG8_STAGE(bufoff, gbase, voff) do { PG8_GLDS((const char*)(gbase), (voff)[0], ldsb + (bufoff)); PG8_GLDS((const char*)(gbase), (voff)[1], ldsb + (bufoff) + 8192u); } while (0)
; #define PG8_STAGEA(bufoff, gbase, o0, o1) do { PG8_GLDS((const char*)(gbase), (o0), ldsb + (bufoff)); PG8_GLDS((const char*)(gbase), (o1), ldsb + (bufoff) + 8192u); } while (0)
; #define PG8_STAGEA1(bufoff, gbase) do { if constexpr (Sched::GATHER) { PG8_STAGEA(bufoff, gbase, vA2, vA3); } else { PG8_STAGEA(bufoff, (gbase) + hstep, vA0, vA1); } } while (0)
; #define PG8_WAIT_VR() PG8_WAIT_V(8)
; #define PG8_WAIT_VX() do { if (relax) asm volatile("s_waitcnt vmcnt(%0)" :: "n"(8 + Epi::RELAX) : "memory"); else PG8_WAIT_V(8); } while (0)
; #define PG8_WAIT_L(n) asm volatile("s_waitcnt lgkmcnt(" #n ")" ::: "memory")
; template <class Epi, class Sched, bool F8 = false, bool PF = false, bool I8 = false, int PID = -1>
; __device__ __forceinline__ void gemm_phase(LAS unsigned char* lds, LAS unsigned char* xlds, const int RP, const int RPB, const int nt, const Sched& S, const Epi& E, const int stagger_ticks) {
;     ...
;             PG8_LDB(B0, 0, 0); PG8_LDB(B1, 0, 1); PG8_SCHED; PG8_LDA(At, 0, 0); PG8_STAGEA1(PG8_SA(1, 1), a1);
;             if (Sched::GATHER) { if (last) { const u32x4 nv = *nslot; vA0 = nv.x; vA1 = nv.y; vA2 = nv.z; vA3 = nv.w; } }
;             PG8_WAIT_VX(); PG8_WAIT_L(0); PG8_BAR; PG8_MMA(0, 0, At, B0); PG8_MMA(0, 1, At, B1); PG8_BAR; PG8_SCHED;
;             if constexpr (Epi::BIAS_DMA) { if (t == 0 && has_next) E.bias_dma(nxt, xlds + 8192 + ((ui + 1) & 1) * Epi::BIAS_STRIDE, wid, lane); }
;             PG8_LDA(At, 0, 1); PG8_STAGE(PG8_SB(0, 0), b2, voffB); PG8_STAGE(PG8_SB(0, 1), b2 + hstepB, voffB); PG8_STAGEA(PG8_SA(0, 0), a2, vA0, vA1);
;             PG8_WAIT_VX(); PG8_WAIT_L(0); PG8_BAR; PG8_MMA(1, 0, At, B0); PG8_MMA(1, 1, At, B1); PG8_BAR; PG8_SCHED;
;             PG8_LDB(B0, 1, 0); PG8_LDB(B1, 1, 1); PG8_SCHED; PG8_LDA(At, 1, 0); PG8_STAGEA1(PG8_SA(0, 1), a2);
;             PG8_WAIT_VR(); PG8_WAIT_L(0); PG8_BAR; PG8_MMA(0, 0, At, B0); PG8_MMA(0, 1, At, B1); PG8_BAR; PG8_SCHED;
;             PG8_LDA(At, 1, 1); PG8_STAGE(PG8_SB(1, 0), b3, voffB); PG8_STAGE(PG8_SB(1, 1), b3 + hstepB, voffB); PG8_STAGEA(PG8_SA(1, 0), a3, vA0, vA1);
;             PG8_WAIT_VR(); PG8_WAIT_L(0); PG8_BAR; PG8_MMA(1, 0, At, B0); PG8_MMA(1, 1, At, B1); PG8_BAR; PG8_SCHED;
	s_setprio 1
	s_waitcnt lgkmcnt(6)
	v_mfma_f32_16x16x128_f8f6f4 v[114:117], v[2:9], v[10:17], v[114:117]
	v_mfma_f32_16x16x128_f8f6f4 v[118:121], v[18:25], v[10:17], v[118:121]
	s_waitcnt lgkmcnt(4)
	v_mfma_f32_16x16x128_f8f6f4 v[110:113], v[2:9], v[26:33], v[110:113]
	v_mfma_f32_16x16x128_f8f6f4 v[106:109], v[18:25], v[26:33], v[106:109]
	s_waitcnt lgkmcnt(2)
	v_mfma_f32_16x16x128_f8f6f4 v[94:97], v[2:9], v[34:41], v[204:207]
	v_mfma_f32_16x16x128_f8f6f4 v[90:93], v[18:25], v[34:41], v[208:211]
	s_waitcnt lgkmcnt(0)
	v_mfma_f32_16x16x128_f8f6f4 v[78:81], v[2:9], v[42:49], v[212:215]
	v_mfma_f32_16x16x128_f8f6f4 v[74:77], v[18:25], v[42:49], v[216:219]
	v_mfma_f32_16x16x128_f8f6f4 v[122:125], v[130:137], v[10:17], v[122:125]
	v_mfma_f32_16x16x128_f8f6f4 v[126:129], v[138:145], v[10:17], v[126:129]
	v_mfma_f32_16x16x128_f8f6f4 v[102:105], v[130:137], v[26:33], v[102:105]
	v_mfma_f32_16x16x128_f8f6f4 v[98:101], v[138:145], v[26:33], v[98:101]
	v_mfma_f32_16x16x128_f8f6f4 v[86:89], v[130:137], v[34:41], v[164:167]
	v_mfma_f32_16x16x128_f8f6f4 v[82:85], v[138:145], v[34:41], v[168:171]
	v_mfma_f32_16x16x128_f8f6f4 v[70:73], v[130:137], v[42:49], v[180:183]
	v_mfma_f32_16x16x128_f8f6f4 v[66:69], v[138:145], v[42:49], v[184:187]
	s_setprio 0
	s_barrier
	s_add_u32 s30, s28, 0x80
	ds_read_b128 v[34:37], v178 offset:49152
	ds_read_b128 v[38:41], v178 offset:50176
	ds_read_b128 v[146:149], v178 offset:51200
	ds_read_b128 v[150:153], v178 offset:52224
	ds_read_b128 v[156:159], v178 offset:53248
	ds_read_b128 v[160:163], v178 offset:54272
	ds_read_b128 v[164:167], v178 offset:55296
	ds_read_b128 v[168:171], v178 offset:56320
	s_addc_u32 s31, s29, 0
	s_add_i32 s47, s46, 0x18000
	s_mov_b32 m0, s47
	s_nop 0
	global_load_lds_dwordx4 v175, s[30:31]
	s_add_i32 s47, s46, 0x1a000
	s_mov_b32 m0, s47
	s_nop 0
	global_load_lds_dwordx4 v176, s[30:31]
	s_add_u32 s28, s28, 0x2080
	s_addc_u32 s29, s29, 0
	s_add_i32 s30, s46, 0x1c000
	s_mov_b32 m0, s30
	s_nop 0
	global_load_lds_dwordx4 v175, s[28:29]
	s_add_i32 s30, s46, 0x1e000
	s_mov_b32 m0, s30
	s_nop 0
	global_load_lds_dwordx4 v176, s[28:29]
	s_waitcnt vmcnt(6)
	s_waitcnt lgkmcnt(0)
	s_barrier
	s_setprio 1
	s_waitcnt lgkmcnt(6)
	v_mfma_f32_16x16x128_f8f6f4 v[62:65], v[2:9], v[34:41], v[62:65]
	v_mfma_f32_16x16x128_f8f6f4 v[58:61], v[18:25], v[34:41], v[58:61]
	s_waitcnt lgkmcnt(4)
	v_mfma_f32_16x16x128_f8f6f4 v[46:49], v[2:9], v[146:153], v[188:191]
	v_mfma_f32_16x16x128_f8f6f4 v[42:45], v[18:25], v[146:153], v[192:195]
	s_waitcnt lgkmcnt(2)
	v_mfma_f32_16x16x128_f8f6f4 v[30:33], v[2:9], v[156:163], v[196:199]
	v_mfma_f32_16x16x128_f8f6f4 v[26:29], v[18:25], v[156:163], v[200:203]
	s_waitcnt lgkmcnt(0)
	v_mfma_f32_16x16x128_f8f6f4 v[14:17], v[2:9], v[164:171], v[220:223]
	v_mfma_f32_16x16x128_f8f6f4 v[10:13], v[18:25], v[164:171], v[224:227]
	v_mfma_f32_16x16x128_f8f6f4 v[54:57], v[130:137], v[34:41], v[54:57]
	v_mfma_f32_16x16x128_f8f6f4 v[50:53], v[138:145], v[34:41], v[50:53]
	v_mfma_f32_16x16x128_f8f6f4 v[38:41], v[130:137], v[146:153], v[228:231]
	v_mfma_f32_16x16x128_f8f6f4 v[34:37], v[138:145], v[146:153], v[232:235]
	v_mfma_f32_16x16x128_f8f6f4 v[22:25], v[130:137], v[156:163], v[236:239]
	v_mfma_f32_16x16x128_f8f6f4 v[18:21], v[138:145], v[156:163], v[240:243]
	v_mfma_f32_16x16x128_f8f6f4 v[6:9], v[130:137], v[164:171], v[244:247]
	v_mfma_f32_16x16x128_f8f6f4 v[2:5], v[138:145], v[164:171], v[248:251]
	s_setprio 0
	s_barrier
	s_add_i32 s45, s45, 2
	s_add_u32 s43, s43, 0x100
	s_addc_u32 s44, s44, 0
	s_add_u32 s0, s0, 0x100
	s_addc_u32 s1, s1, 0
	s_cmp_gt_u32 s45, 5
.LBB0_753:
	s_mov_b32 s46, s38
	s_add_u32 s100, s0, 0xfffe0000
	s_addc_u32 s101, s1, -1
	s_add_i32 s47, s46, 0x8000
	s_mov_b32 m0, s47
	s_nop 0
	global_load_lds_dwordx4 v1, s[100:101]
	s_add_i32 s47, s46, 0xa000
	s_mov_b32 m0, s47
	s_nop 0
	global_load_lds_dwordx4 v174, s[100:101]
	v_add_u32_e32 v142, 0x10000, v177
	v_add_u32_e32 v155, 0x14000, v177
	ds_read_b128 v[130:133], v142
	ds_read_b128 v[134:137], v142 offset:1024
	ds_read_b128 v[138:141], v142 offset:2048
	ds_read_b128 v[142:145], v142 offset:3072
	ds_read_b128 v[146:149], v155
	ds_read_b128 v[150:153], v155 offset:1024
	ds_read_b128 v[156:159], v155 offset:2048
	ds_read_b128 v[160:163], v155 offset:3072
	s_add_u32 s2, s0, 0xfffe0080
	s_addc_u32 s3, s1, -1
	s_cmp_eq_u32 s45, 4
	s_cselect_b32 s30, s6, s2
	s_cselect_b32 s31, s7, s3
	s_cselect_b32 s28, s8, s43
	s_cselect_b32 s29, s9, s44
	s_add_u32 s2, s30, 0x80
	s_addc_u32 s3, s31, 0
	ds_read_b128 v[164:167], v178
	ds_read_b128 v[168:171], v178 offset:1024
	ds_read_b128 v[180:183], v178 offset:2048
	ds_read_b128 v[184:187], v178 offset:3072
	ds_read_b128 v[188:191], v178 offset:4096
	ds_read_b128 v[192:195], v178 offset:5120
	ds_read_b128 v[196:199], v178 offset:6144
	ds_read_b128 v[200:203], v178 offset:7168
	s_add_i32 s47, s46, 0xc000
	s_mov_b32 m0, s47
	s_nop 0
	global_load_lds_dwordx4 v1, s[0:1]
	s_add_i32 s47, s46, 0xe000
	s_mov_b32 m0, s47
	s_nop 0
	global_load_lds_dwordx4 v174, s[0:1]
	s_waitcnt vmcnt(8)
	s_waitcnt lgkmcnt(0)
	s_barrier
; #define PG8_STAGE(bufoff, gbase, voff) do { PG8_GLDS((const char*)(gbase), (voff)[0], ldsb + (bufoff)); PG8_GLDS((const char*)(gbase), (voff)[1], ldsb + (bufoff) + 8192u); } while (0)
; #define PG8_STAGEA(bufoff, gbase, o0, o1) do { PG8_GLDS((const char*)(gbase), (o0), ldsb + (bufoff)); PG8_GLDS((const char*)(gbase), (o1), ldsb + (bufoff) + 8192u); } while (0)
; #define PG8_STAGEA1(bufoff, gbase) do { if constexpr (Sched::GATHER) { PG8_STAGEA(bufoff, gbase, vA2, vA3); } else { PG8_STAGEA(bufoff, (gbase) + hstep, vA0, vA1); } } while (0)
; #define PG8_LDA(dst, b, h) do { if constexpr (F8) { _Pragma("unroll") for (int m = 0; m < 4; ++m) dst##8[m] = PG8_LD32(lds + PG8_SA(b, h) + aoff + m * 2048); } else { \
;         _Pragma("unroll") for (int m = 0; m < 4; ++m) _Pragma("unroll") for (int k = 0; k < 2; ++k) dst[m][k] = *(const LAS bf16x8*)(lds + PG8_SA(b, h) + aoff + m * 2048 + k * 1024); } } while (0)
; #define PG8_LDB(dst, b, h) do { if constexpr (F8) { _Pragma("unroll") for (int n = 0; n < 2; ++n) dst##8[n] = PG8_LD32(lds + PG8_SB(b, h) + boff + n * 2048); } else { \
;         _Pragma("unroll") for (int n = 0; n < 2; ++n) _Pragma("unroll") for (int k = 0; k < 2; ++k) dst[n][k] = *(const LAS bf16x8*)(lds + PG8_SB(b, h) + boff + n * 2048 + k * 1024); } } while (0)
; #define PG8_WAIT_VR() PG8_WAIT_V(8)
; template <class Epi, class Sched, bool F8 = false, bool PF = false, bool I8 = false, int PID = -1>
; __device__ __forceinline__ void gemm_phase(LAS unsigned char* lds, LAS unsigned char* xlds, const int RP, const int RPB, const int nt, const Sched& S, const Epi& E, const int stagger_ticks) {
;     ...
;             PG8_WAIT_VX(); PG8_WAIT_L(0); PG8_BAR; PG8_MMA(0, 0, At, B0); PG8_MMA(0, 1, At, B1); PG8_BAR; PG8_SCHED;
;             if constexpr (Epi::BIAS_DMA) { if (t == 0 && has_next) E.bias_dma(nxt, xlds + 8192 + ((ui + 1) & 1) * Epi::BIAS_STRIDE, wid, lane); }
;             PG8_LDA(At, 0, 1); PG8_STAGE(PG8_SB(0, 0), b2, voffB); PG8_STAGE(PG8_SB(0, 1), b2 + hstepB, voffB); PG8_STAGEA(PG8_SA(0, 0), a2, vA0, vA1);
;             PG8_WAIT_VX(); PG8_WAIT_L(0); PG8_BAR; PG8_MMA(1, 0, At, B0); PG8_MMA(1, 1, At, B1); PG8_BAR; PG8_SCHED;
;             PG8_LDB(B0, 1, 0); PG8_LDB(B1, 1, 1); PG8_SCHED; PG8_LDA(At, 1, 0); PG8_STAGEA1(PG8_SA(0, 1), a2);
;             PG8_WAIT_VR(); PG8_WAIT_L(0); PG8_BAR; PG8_MMA(0, 0, At, B0); PG8_MMA(0, 1, At, B1); PG8_BAR; PG8_SCHED;
	s_setprio 1
	s_waitcnt lgkmcnt(6)
	v_mfma_f32_16x16x128_f8f6f4 v[114:117], v[130:137], v[164:171], v[114:117]
	v_mfma_f32_16x16x128_f8f6f4 v[118:121], v[138:145], v[164:171], v[118:121]
	s_waitcnt lgkmcnt(4)
	v_mfma_f32_16x16x128_f8f6f4 v[110:113], v[130:137], v[180:187], v[110:113]
	v_mfma_f32_16x16x128_f8f6f4 v[106:109], v[138:145], v[180:187], v[106:109]
	s_waitcnt lgkmcnt(2)
	v_mfma_f32_16x16x128_f8f6f4 v[204:207], v[130:137], v[188:195], v[94:97]
	v_mfma_f32_16x16x128_f8f6f4 v[208:211], v[138:145], v[188:195], v[90:93]
	s_waitcnt lgkmcnt(0)
	v_mfma_f32_16x16x128_f8f6f4 v[212:215], v[130:137], v[196:203], v[78:81]
	v_mfma_f32_16x16x128_f8f6f4 v[216:219], v[138:145], v[196:203], v[74:77]
	v_mfma_f32_16x16x128_f8f6f4 v[122:125], v[146:153], v[164:171], v[122:125]
	v_mfma_f32_16x16x128_f8f6f4 v[126:129], v[156:163], v[164:171], v[126:129]
	v_mfma_f32_16x16x128_f8f6f4 v[102:105], v[146:153], v[180:187], v[102:105]
	v_mfma_f32_16x16x128_f8f6f4 v[98:101], v[156:163], v[180:187], v[98:101]
	v_mfma_f32_16x16x128_f8f6f4 v[164:167], v[146:153], v[188:195], v[86:89]
	v_mfma_f32_16x16x128_f8f6f4 v[168:171], v[156:163], v[188:195], v[82:85]
	v_mfma_f32_16x16x128_f8f6f4 v[180:183], v[146:153], v[196:203], v[70:73]
	v_mfma_f32_16x16x128_f8f6f4 v[184:187], v[156:163], v[196:203], v[66:69]
	s_setprio 0
	s_barrier
	s_nop 4
	ds_read_b128 v[66:69], v178 offset:16384
	ds_read_b128 v[70:73], v178 offset:17408
	ds_read_b128 v[74:77], v178 offset:18432
	ds_read_b128 v[78:81], v178 offset:19456
	ds_read_b128 v[82:85], v178 offset:20480
	ds_read_b128 v[86:89], v178 offset:21504
	ds_read_b128 v[90:93], v178 offset:22528
	ds_read_b128 v[94:97], v178 offset:23552
	s_add_i32 s47, s46, 0x10000
	s_mov_b32 m0, s47
	s_nop 0
	global_load_lds_dwordx4 v175, s[28:29]
	s_add_i32 s47, s46, 0x12000
	s_mov_b32 m0, s47
	s_nop 0
	global_load_lds_dwordx4 v176, s[28:29]
	s_add_u32 s48, s28, 0x2000
	s_addc_u32 s49, s29, 0
	s_add_i32 s47, s46, 0x14000
	s_mov_b32 m0, s47
	s_nop 0
	global_load_lds_dwordx4 v175, s[48:49]
	s_add_i32 s47, s46, 0x16000
	s_mov_b32 m0, s47
	s_nop 0
	global_load_lds_dwordx4 v176, s[48:49]
	s_waitcnt vmcnt(6)
	s_waitcnt lgkmcnt(0)
	s_barrier
	s_setprio 1
	s_waitcnt lgkmcnt(6)
	v_mfma_f32_16x16x128_f8f6f4 v[62:65], v[130:137], v[66:73], v[62:65]
	v_mfma_f32_16x16x128_f8f6f4 v[58:61], v[138:145], v[66:73], v[58:61]
	s_waitcnt lgkmcnt(4)
	v_mfma_f32_16x16x128_f8f6f4 v[188:191], v[130:137], v[74:81], v[46:49]
	v_mfma_f32_16x16x128_f8f6f4 v[192:195], v[138:145], v[74:81], v[42:45]
	s_waitcnt lgkmcnt(2)
	v_mfma_f32_16x16x128_f8f6f4 v[196:199], v[130:137], v[82:89], v[30:33]
	v_mfma_f32_16x16x128_f8f6f4 v[200:203], v[138:145], v[82:89], v[26:29]
	s_waitcnt lgkmcnt(0)
	v_mfma_f32_16x16x128_f8f6f4 v[220:223], v[130:137], v[90:97], v[14:17]
	v_mfma_f32_16x16x128_f8f6f4 v[224:227], v[138:145], v[90:97], v[10:13]
	v_mfma_f32_16x16x128_f8f6f4 v[54:57], v[146:153], v[66:73], v[54:57]
	v_mfma_f32_16x16x128_f8f6f4 v[50:53], v[156:163], v[66:73], v[50:53]
	v_mfma_f32_16x16x128_f8f6f4 v[228:231], v[146:153], v[74:81], v[38:41]
	v_mfma_f32_16x16x128_f8f6f4 v[232:235], v[156:163], v[74:81], v[34:37]
	v_mfma_f32_16x16x128_f8f6f4 v[236:239], v[146:153], v[82:89], v[22:25]
	v_mfma_f32_16x16x128_f8f6f4 v[240:243], v[156:163], v[82:89], v[18:21]
	v_mfma_f32_16x16x128_f8f6f4 v[244:247], v[146:153], v[90:97], v[6:9]
	v_mfma_f32_16x16x128_f8f6f4 v[248:251], v[156:163], v[90:97], v[2:5]
	s_setprio 0
	s_barrier
	s_add_i32 s47, s46, 0x2000
	s_mov_b32 m0, s46
	s_nop 0
	global_load_lds_dwordx4 v1, s[30:31]
	s_nop 0
	s_mov_b32 m0, s47
	s_nop 0
	global_load_lds_dwordx4 v174, s[30:31]
	v_add_u32_e32 v10, 0x18000, v177
	s_nop 3
	ds_read_b128 v[2:5], v10
	ds_read_b128 v[6:9], v10 offset:1024
	ds_read_b128 v[18:21], v10 offset:2048
	ds_read_b128 v[22:25], v10 offset:3072
	v_add_u32_e32 v10, 0x1c000, v177
	ds_read_b128 v[130:133], v10
	ds_read_b128 v[134:137], v10 offset:1024
	ds_read_b128 v[138:141], v10 offset:2048
	ds_read_b128 v[142:145], v10 offset:3072
	ds_read_b128 v[10:13], v178 offset:32768
	ds_read_b128 v[14:17], v178 offset:33792
	ds_read_b128 v[26:29], v178 offset:34816
	ds_read_b128 v[30:33], v178 offset:35840
	ds_read_b128 v[34:37], v178 offset:36864
	ds_read_b128 v[38:41], v178 offset:37888
	ds_read_b128 v[42:45], v178 offset:38912
	ds_read_b128 v[46:49], v178 offset:39936
	s_add_u32 s30, s30, 0x20000
	s_addc_u32 s31, s31, 0
	s_add_i32 s47, s46, 0x4000
	s_mov_b32 m0, s47
	s_nop 0
	global_load_lds_dwordx4 v1, s[30:31]
	s_add_i32 s47, s46, 0x6000
	s_mov_b32 m0, s47
	s_nop 0
	global_load_lds_dwordx4 v174, s[30:31]
	s_waitcnt vmcnt(8)
	s_waitcnt lgkmcnt(0)
	s_barrier
; #define PG8_STAGE(bufoff, gbase, voff) do { PG8_GLDS((const char*)(gbase), (voff)[0], ldsb + (bufoff)); PG8_GLDS((const char*)(gbase), (voff)[1], ldsb + (bufoff) + 8192u); } while (0)
; #define PG8_STAGEA(bufoff, gbase, o0, o1) do { PG8_GLDS((const char*)(gbase), (o0), ldsb + (bufoff)); PG8_GLDS((const char*)(gbase), (o1), ldsb + (bufoff) + 8192u); } while (0)
; #define PG8_STAGEA1(bufoff, gbase) do { if constexpr (Sched::GATHER) { PG8_STAGEA(bufoff, gbase, vA2, vA3); } else { PG8_STAGEA(bufoff, (gbase) + hstep, vA0, vA1); } } while (0)
; #define PG8_LDA(dst, b, h) do { if constexpr (F8) { _Pragma("unroll") for (int m = 0; m < 4; ++m) dst##8[m] = PG8_LD32(lds + PG8_SA(b, h) + aoff + m * 2048); } else { \
;         _Pragma("unroll") for (int m = 0; m < 4; ++m) _Pragma("unroll") for (int k = 0; k < 2; ++k) dst[m][k] = *(const LAS bf16x8*)(lds + PG8_SA(b, h) + aoff + m * 2048 + k * 1024); } } while (0)
; #define PG8_LDB(dst, b, h) do { if constexpr (F8) { _Pragma("unroll") for (int n = 0; n < 2; ++n) dst##8[n] = PG8_LD32(lds + PG8_SB(b, h) + boff + n * 2048); } else { \
;         _Pragma("unroll") for (int n = 0; n < 2; ++n) _Pragma("unroll") for (int k = 0; k < 2; ++k) dst[n][k] = *(const LAS bf16x8*)(lds + PG8_SB(b, h) + boff + n * 2048 + k * 1024); } } while (0)
; #define PG8_WAIT_VR() PG8_WAIT_V(8)
; #define PG8_WAIT_L(n) asm volatile("s_waitcnt lgkmcnt(" #n ")" ::: "memory")
; #define PG8_BAR __builtin_amdgcn_s_barrier()
; #define PG8_SCHED __builtin_amdgcn_sched_barrier(0)
; template <class Epi, class Sched, bool F8 = false, bool PF = false, bool I8 = false, int PID = -1>
; __device__ __forceinline__ void gemm_phase(LAS unsigned char* lds, LAS unsigned char* xlds, const int RP, const int RPB, const int nt, const Sched& S, const Epi& E, const int stagger_ticks) {
;     ...
;             PG8_LDB(B0, 1, 0); PG8_LDB(B1, 1, 1); PG8_SCHED; PG8_LDA(At, 1, 0); PG8_STAGEA1(PG8_SA(0, 1), a2);
;             PG8_WAIT_VR(); PG8_WAIT_L(0); PG8_BAR; PG8_MMA(0, 0, At, B0); PG8_MMA(0, 1, At, B1); PG8_BAR; PG8_SCHED;
;             PG8_LDA(At, 1, 1); PG8_STAGE(PG8_SB(1, 0), b3, voffB); PG8_STAGE(PG8_SB(1, 1), b3 + hstepB, voffB); PG8_STAGEA(PG8_SA(1, 0), a3, vA0, vA1);
;             PG8_WAIT_VR(); PG8_WAIT_L(0); PG8_BAR; PG8_MMA(1, 0, At, B0); PG8_MMA(1, 1, At, B1); PG8_BAR; PG8_SCHED;
;         }
	s_setprio 1
	s_waitcnt lgkmcnt(6)
	v_mfma_f32_16x16x128_f8f6f4 v[114:117], v[2:9], v[10:17], v[114:117]
	v_mfma_f32_16x16x128_f8f6f4 v[118:121], v[18:25], v[10:17], v[118:121]
	s_waitcnt lgkmcnt(4)
	v_mfma_f32_16x16x128_f8f6f4 v[110:113], v[2:9], v[26:33], v[110:113]
	v_mfma_f32_16x16x128_f8f6f4 v[106:109], v[18:25], v[26:33], v[106:109]
	s_waitcnt lgkmcnt(2)
	v_mfma_f32_16x16x128_f8f6f4 v[94:97], v[2:9], v[34:41], v[204:207]
	v_mfma_f32_16x16x128_f8f6f4 v[90:93], v[18:25], v[34:41], v[208:211]
	s_waitcnt lgkmcnt(0)
	v_mfma_f32_16x16x128_f8f6f4 v[78:81], v[2:9], v[42:49], v[212:215]
	v_mfma_f32_16x16x128_f8f6f4 v[74:77], v[18:25], v[42:49], v[216:219]
	v_mfma_f32_16x16x128_f8f6f4 v[122:125], v[130:137], v[10:17], v[122:125]
	v_mfma_f32_16x16x128_f8f6f4 v[126:129], v[138:145], v[10:17], v[126:129]
	v_mfma_f32_16x16x128_f8f6f4 v[102:105], v[130:137], v[26:33], v[102:105]
	v_mfma_f32_16x16x128_f8f6f4 v[98:101], v[138:145], v[26:33], v[98:101]
	v_mfma_f32_16x16x128_f8f6f4 v[86:89], v[130:137], v[34:41], v[164:167]
	v_mfma_f32_16x16x128_f8f6f4 v[82:85], v[138:145], v[34:41], v[168:171]
	v_mfma_f32_16x16x128_f8f6f4 v[70:73], v[130:137], v[42:49], v[180:183]
	v_mfma_f32_16x16x128_f8f6f4 v[66:69], v[138:145], v[42:49], v[184:187]
	s_setprio 0
	s_barrier
	s_add_u32 s30, s28, 0x80
	ds_read_b128 v[34:37], v178 offset:49152
	ds_read_b128 v[38:41], v178 offset:50176
	ds_read_b128 v[146:149], v178 offset:51200
	ds_read_b128 v[150:153], v178 offset:52224
	ds_read_b128 v[156:159], v178 offset:53248
	ds_read_b128 v[160:163], v178 offset:54272
	ds_read_b128 v[164:167], v178 offset:55296
	ds_read_b128 v[168:171], v178 offset:56320
	s_addc_u32 s31, s29, 0
	s_add_i32 s47, s46, 0x18000
	s_mov_b32 m0, s47
	s_nop 0
	global_load_lds_dwordx4 v175, s[30:31]
	s_add_i32 s47, s46, 0x1a000
	s_mov_b32 m0, s47
	s_nop 0
	global_load_lds_dwordx4 v176, s[30:31]
	s_add_u32 s28, s28, 0x2080
	s_addc_u32 s29, s29, 0
	s_add_i32 s30, s46, 0x1c000
	s_mov_b32 m0, s30
	s_nop 0
	global_load_lds_dwordx4 v175, s[28:29]
	s_add_i32 s30, s46, 0x1e000
	s_mov_b32 m0, s30
	s_nop 0
	global_load_lds_dwordx4 v176, s[28:29]
	s_waitcnt vmcnt(6)
	s_waitcnt lgkmcnt(0)
	s_barrier
	s_setprio 1
	s_waitcnt lgkmcnt(6)
	v_mfma_f32_16x16x128_f8f6f4 v[62:65], v[2:9], v[34:41], v[62:65]
	v_mfma_f32_16x16x128_f8f6f4 v[58:61], v[18:25], v[34:41], v[58:61]
	s_waitcnt lgkmcnt(4)
	v_mfma_f32_16x16x128_f8f6f4 v[46:49], v[2:9], v[146:153], v[188:191]
	v_mfma_f32_16x16x128_f8f6f4 v[42:45], v[18:25], v[146:153], v[192:195]
	s_waitcnt lgkmcnt(2)
	v_mfma_f32_16x16x128_f8f6f4 v[30:33], v[2:9], v[156:163], v[196:199]
	v_mfma_f32_16x16x128_f8f6f4 v[26:29], v[18:25], v[156:163], v[200:203]
	s_waitcnt lgkmcnt(0)
	v_mfma_f32_16x16x128_f8f6f4 v[14:17], v[2:9], v[164:171], v[220:223]
	v_mfma_f32_16x16x128_f8f6f4 v[10:13], v[18:25], v[164:171], v[224:227]
	v_mfma_f32_16x16x128_f8f6f4 v[54:57], v[130:137], v[34:41], v[54:57]
	v_mfma_f32_16x16x128_f8f6f4 v[50:53], v[138:145], v[34:41], v[50:53]
	v_mfma_f32_16x16x128_f8f6f4 v[38:41], v[130:137], v[146:153], v[228:231]
	v_mfma_f32_16x16x128_f8f6f4 v[34:37], v[138:145], v[146:153], v[232:235]
	v_mfma_f32_16x16x128_f8f6f4 v[22:25], v[130:137], v[156:163], v[236:239]
	v_mfma_f32_16x16x128_f8f6f4 v[18:21], v[138:145], v[156:163], v[240:243]
	v_mfma_f32_16x16x128_f8f6f4 v[6:9], v[130:137], v[164:171], v[244:247]
	v_mfma_f32_16x16x128_f8f6f4 v[2:5], v[138:145], v[164:171], v[248:251]
	s_setprio 0
	s_barrier
	s_add_i32 s45, s45, 2
	s_add_u32 s43, s43, 0x100
	s_addc_u32 s44, s44, 0
	s_add_u32 s0, s0, 0x100
	s_addc_u32 s1, s1, 0
	s_cmp_gt_u32 s45, 5
	s_cbranch_scc0 .LBB0_753
	s_and_b64 vcc, exec, s[24:25]
	s_cbranch_vccz .LBB0_756
	s_barrier
